# 72 converter workgroups + MMA segments without already-satisfied lgkmcnt waits and mid-segment setprio pairs + LDS-DMA blocks without m0 save/restore
# speedup vs baseline: 1.0060x; 1.0060x over previous
; #define LAS __attribute__((address_space(3)))
; #define PG8_STAGEB(bufoff, gbase) PG8_STAGE2(bufoff, gbase, voffB[0], voffB[1])
; #define PG8_STAGEA(bufoff, gbase, h) PG8_STAGE2(bufoff, gbase, voffA[h][0], voffA[h][1])
; #define PG8_STAGEAS(bufoff, gbase, h) PG8_STAGE2(bufoff, gbase, voffA[h][0], voffA[h][1])
; #define PG8_LDA(dst, b, h) do { _Pragma("unroll") for (int m = 0; m < 4; ++m) _Pragma("unroll") for (int k = 0; k < 2; ++k) dst[m][k] = *(const LAS bf16x8*)(lds + PG8_SA(b, h) + aoff + m * 2048 + k * 1024); } while (0)
; #define PG8_LDB(dst, b, h) do { _Pragma("unroll") for (int n = 0; n < 2; ++n) _Pragma("unroll") for (int k = 0; k < 2; ++k) dst[n][k] = *(const LAS bf16x8*)(lds + PG8_SB(b, h) + boff + n * 2048 + k * 1024); } while (0)
; #define PG8_WAIT_K0() do { if (EST > 0 && t == 0 && ui > 0) asm volatile("s_waitcnt vmcnt(%0)" :: "n"((HM ? 6 : 8) + EST) : "memory"); else PG8_WAIT_K(); } while (0)
; #define PG8_WAIT_L(n) asm volatile("s_waitcnt lgkmcnt(" #n ")" ::: "memory")
; #define PG8_BAR __builtin_amdgcn_s_barrier()
; #define PG8_SCHED __builtin_amdgcn_sched_barrier(0)
;     ...
;             PG8_LDB(B0, 0, 0); PG8_LDB(B1, 0, 1); PG8_SCHED; PG8_LDA(At, 0, 0); if constexpr (!HM) PG8_STAGEA(PG8_SA(1, 1), a1, 1);
;             if constexpr (Sched::kGather) { if (last && has_next) { const u32x4 tn = *(const LAS u32x4*)(S.aux + tid * 16); voffA[0][0] = tn.x; voffA[0][1] = tn.y; voffA[1][0] = tn.z; voffA[1][1] = tn.w; } }
;             PG8_WAIT_K0(); PG8_WAIT_L(0); PG8_BAR; PG8_MMA(0, 0, At, B0); PG8_MMA(0, 1, At, B1); PG8_BAR; PG8_SCHED;
;             if constexpr (!HM) PG8_LDA(At, 0, 1);
;             PG8_STAGEB(PG8_SB(0, 0), b2); PG8_STAGEB(PG8_SB(0, 1), b2 + hstepB); PG8_STAGEAS(PG8_SA(0, 0), a2, 0);
;             PG8_WAIT_K0(); PG8_WAIT_L(0); PG8_BAR; if constexpr (!HM) { PG8_MMA(1, 0, At, B0); PG8_MMA(1, 1, At, B1); } PG8_BAR; PG8_SCHED;
.LBB0_140:
	ds_read_b128 v[142:145], v163
	ds_read_b128 v[146:149], v163 offset:1024
	ds_read_b128 v[150:153], v163 offset:2048
	ds_read_b128 v[170:173], v163 offset:3072
	ds_read_b128 v[174:177], v164
	ds_read_b128 v[178:181], v164 offset:1024
	ds_read_b128 v[182:185], v164 offset:2048
	ds_read_b128 v[186:189], v164 offset:3072
	s_cmp_eq_u32 s47, 28
	s_cselect_b32 s56, s48, s4
	s_cselect_b32 s57, s49, s11
	s_cselect_b32 s54, s50, s33
	s_cselect_b32 s55, s51, s45
	s_add_u32 s12, s56, 0x80
	s_addc_u32 s13, s57, 0
	ds_read_b128 v[190:193], v165
	ds_read_b128 v[194:197], v165 offset:1024
	ds_read_b128 v[198:201], v165 offset:2048
	ds_read_b128 v[202:205], v165 offset:3072
	ds_read_b128 v[206:209], v165 offset:4096
	ds_read_b128 v[210:213], v165 offset:5120
	ds_read_b128 v[214:217], v165 offset:6144
	ds_read_b128 v[218:221], v165 offset:7168
	s_mov_b32 m0, s72
	s_nop 0
	global_load_lds_dwordx4 v159, s[0:1]
	s_mov_b32 m0, s73
	s_nop 0
	global_load_lds_dwordx4 v160, s[0:1]
	s_waitcnt vmcnt(8)
	s_waitcnt lgkmcnt(0)
	s_barrier
	s_setprio 1
	v_mfma_f32_16x16x32_bf16 v[126:129], v[142:145], v[190:193], v[126:129]
	v_mfma_f32_16x16x32_bf16 v[122:125], v[150:153], v[190:193], v[122:125]
	v_mfma_f32_16x16x32_bf16 v[110:113], v[142:145], v[198:201], v[110:113]
	v_mfma_f32_16x16x32_bf16 v[106:109], v[150:153], v[198:201], v[106:109]
	v_mfma_f32_16x16x32_bf16 v[94:97], v[142:145], v[206:209], v[94:97]
	v_mfma_f32_16x16x32_bf16 v[90:93], v[150:153], v[206:209], v[90:93]
	v_mfma_f32_16x16x32_bf16 v[78:81], v[142:145], v[214:217], v[78:81]
	v_mfma_f32_16x16x32_bf16 v[74:77], v[150:153], v[214:217], v[74:77]
	v_mfma_f32_16x16x32_bf16 v[126:129], v[146:149], v[194:197], v[126:129]
	v_mfma_f32_16x16x32_bf16 v[122:125], v[170:173], v[194:197], v[122:125]
	v_mfma_f32_16x16x32_bf16 v[110:113], v[146:149], v[202:205], v[110:113]
	v_mfma_f32_16x16x32_bf16 v[106:109], v[170:173], v[202:205], v[106:109]
	v_mfma_f32_16x16x32_bf16 v[94:97], v[146:149], v[210:213], v[94:97]
	v_mfma_f32_16x16x32_bf16 v[90:93], v[170:173], v[210:213], v[90:93]
	v_mfma_f32_16x16x32_bf16 v[78:81], v[146:149], v[218:221], v[78:81]
	v_mfma_f32_16x16x32_bf16 v[74:77], v[170:173], v[218:221], v[74:77]
	v_mfma_f32_16x16x32_bf16 v[118:121], v[174:177], v[190:193], v[118:121]
	v_mfma_f32_16x16x32_bf16 v[114:117], v[182:185], v[190:193], v[114:117]
	v_mfma_f32_16x16x32_bf16 v[102:105], v[174:177], v[198:201], v[102:105]
	v_mfma_f32_16x16x32_bf16 v[98:101], v[182:185], v[198:201], v[98:101]
	v_mfma_f32_16x16x32_bf16 v[86:89], v[174:177], v[206:209], v[86:89]
	v_mfma_f32_16x16x32_bf16 v[82:85], v[182:185], v[206:209], v[82:85]
	v_mfma_f32_16x16x32_bf16 v[70:73], v[174:177], v[214:217], v[70:73]
	v_mfma_f32_16x16x32_bf16 v[66:69], v[182:185], v[214:217], v[66:69]
	v_mfma_f32_16x16x32_bf16 v[118:121], v[178:181], v[194:197], v[118:121]
	v_mfma_f32_16x16x32_bf16 v[114:117], v[186:189], v[194:197], v[114:117]
	v_mfma_f32_16x16x32_bf16 v[102:105], v[178:181], v[202:205], v[102:105]
	v_mfma_f32_16x16x32_bf16 v[98:101], v[186:189], v[202:205], v[98:101]
	v_mfma_f32_16x16x32_bf16 v[86:89], v[178:181], v[210:213], v[86:89]
	v_mfma_f32_16x16x32_bf16 v[82:85], v[186:189], v[210:213], v[82:85]
	v_mfma_f32_16x16x32_bf16 v[70:73], v[178:181], v[218:221], v[70:73]
	v_mfma_f32_16x16x32_bf16 v[66:69], v[186:189], v[218:221], v[66:69]
	s_setprio 0
	s_barrier
	ds_read_b128 v[190:193], v165 offset:16384
	ds_read_b128 v[194:197], v165 offset:17408
	ds_read_b128 v[198:201], v165 offset:18432
	ds_read_b128 v[202:205], v165 offset:19456
	ds_read_b128 v[206:209], v165 offset:20480
	ds_read_b128 v[210:213], v165 offset:21504
	ds_read_b128 v[214:217], v165 offset:22528
	ds_read_b128 v[218:221], v165 offset:23552
	s_mov_b32 m0, s41
	s_nop 0
	global_load_lds_dwordx4 v1, s[54:55]
	s_mov_b32 m0, s43
	s_nop 0
	global_load_lds_dwordx4 v156, s[54:55]
	s_add_u32 s80, s54, 0x80000
	s_addc_u32 s81, s55, 0
	s_mov_b32 m0, s53
	s_nop 0
	global_load_lds_dwordx4 v1, s[80:81]
	s_mov_b32 m0, s58
	s_nop 0
	global_load_lds_dwordx4 v156, s[80:81]
	s_mov_b32 m0, s29
	s_nop 0
	global_load_lds_dwordx4 v157, s[56:57]
	s_mov_b32 m0, s59
	s_nop 0
	global_load_lds_dwordx4 v158, s[56:57]
	s_waitcnt vmcnt(8)
	s_waitcnt lgkmcnt(0)
	s_barrier
	s_setprio 1
	v_mfma_f32_16x16x32_bf16 v[62:65], v[142:145], v[190:193], v[62:65]
	v_mfma_f32_16x16x32_bf16 v[58:61], v[150:153], v[190:193], v[58:61]
	v_mfma_f32_16x16x32_bf16 v[46:49], v[142:145], v[198:201], v[46:49]
	v_mfma_f32_16x16x32_bf16 v[42:45], v[150:153], v[198:201], v[42:45]
	v_mfma_f32_16x16x32_bf16 v[30:33], v[142:145], v[206:209], v[30:33]
	v_mfma_f32_16x16x32_bf16 v[26:29], v[150:153], v[206:209], v[26:29]
	v_mfma_f32_16x16x32_bf16 v[14:17], v[142:145], v[214:217], v[14:17]
	v_mfma_f32_16x16x32_bf16 v[10:13], v[150:153], v[214:217], v[10:13]
	v_mfma_f32_16x16x32_bf16 v[62:65], v[146:149], v[194:197], v[62:65]
	v_mfma_f32_16x16x32_bf16 v[58:61], v[170:173], v[194:197], v[58:61]
	v_mfma_f32_16x16x32_bf16 v[46:49], v[146:149], v[202:205], v[46:49]
	v_mfma_f32_16x16x32_bf16 v[42:45], v[170:173], v[202:205], v[42:45]
	v_mfma_f32_16x16x32_bf16 v[30:33], v[146:149], v[210:213], v[30:33]
	v_mfma_f32_16x16x32_bf16 v[26:29], v[170:173], v[210:213], v[26:29]
	v_mfma_f32_16x16x32_bf16 v[14:17], v[146:149], v[218:221], v[14:17]
	v_mfma_f32_16x16x32_bf16 v[10:13], v[170:173], v[218:221], v[10:13]
	v_mfma_f32_16x16x32_bf16 v[54:57], v[174:177], v[190:193], v[54:57]
	v_mfma_f32_16x16x32_bf16 v[50:53], v[182:185], v[190:193], v[50:53]
	v_mfma_f32_16x16x32_bf16 v[38:41], v[174:177], v[198:201], v[38:41]
	v_mfma_f32_16x16x32_bf16 v[34:37], v[182:185], v[198:201], v[34:37]
	v_mfma_f32_16x16x32_bf16 v[22:25], v[174:177], v[206:209], v[22:25]
	v_mfma_f32_16x16x32_bf16 v[18:21], v[182:185], v[206:209], v[18:21]
	v_mfma_f32_16x16x32_bf16 v[6:9], v[174:177], v[214:217], v[6:9]
	v_mfma_f32_16x16x32_bf16 v[2:5], v[182:185], v[214:217], v[2:5]
	v_mfma_f32_16x16x32_bf16 v[54:57], v[178:181], v[194:197], v[54:57]
	v_mfma_f32_16x16x32_bf16 v[50:53], v[186:189], v[194:197], v[50:53]
	v_mfma_f32_16x16x32_bf16 v[38:41], v[178:181], v[202:205], v[38:41]
	v_mfma_f32_16x16x32_bf16 v[34:37], v[186:189], v[202:205], v[34:37]
	v_mfma_f32_16x16x32_bf16 v[22:25], v[178:181], v[210:213], v[22:25]
	v_mfma_f32_16x16x32_bf16 v[18:21], v[186:189], v[210:213], v[18:21]
	v_mfma_f32_16x16x32_bf16 v[6:9], v[178:181], v[218:221], v[6:9]
	v_mfma_f32_16x16x32_bf16 v[2:5], v[186:189], v[218:221], v[2:5]
	s_setprio 0
	s_barrier
; #define PG8_STAGEB(bufoff, gbase) PG8_STAGE2(bufoff, gbase, voffB[0], voffB[1])
; #define PG8_STAGEAS(bufoff, gbase, h) PG8_STAGE2(bufoff, gbase, voffA[h][0], voffA[h][1])
; #define PG8_LDA(dst, b, h) do { _Pragma("unroll") for (int m = 0; m < 4; ++m) _Pragma("unroll") for (int k = 0; k < 2; ++k) dst[m][k] = *(const LAS bf16x8*)(lds + PG8_SA(b, h) + aoff + m * 2048 + k * 1024); } while (0)
; #define PG8_LDB(dst, b, h) do { _Pragma("unroll") for (int n = 0; n < 2; ++n) _Pragma("unroll") for (int k = 0; k < 2; ++k) dst[n][k] = *(const LAS bf16x8*)(lds + PG8_SB(b, h) + boff + n * 2048 + k * 1024); } while (0)
; #define PG8_WAIT_K() do { if constexpr (HM) PG8_WAIT_V(6); else PG8_WAIT_V(8); } while (0)
; #define PG8_WAIT_L(n) asm volatile("s_waitcnt lgkmcnt(" #n ")" ::: "memory")
; #define PG8_BAR __builtin_amdgcn_s_barrier()
; #define PG8_SCHED __builtin_amdgcn_sched_barrier(0)
;     ...
;             PG8_LDB(B0, 1, 0); PG8_LDB(B1, 1, 1); PG8_SCHED; PG8_LDA(At, 1, 0); if constexpr (!HM) PG8_STAGEAS(PG8_SA(0, 1), a2, 1);
;             PG8_WAIT_K(); PG8_WAIT_L(0); PG8_BAR; PG8_MMA(0, 0, At, B0); PG8_MMA(0, 1, At, B1); PG8_BAR; PG8_SCHED;
;             if constexpr (!HM) PG8_LDA(At, 1, 1);
;             PG8_STAGEB(PG8_SB(1, 0), b3); PG8_STAGEB(PG8_SB(1, 1), b3 + hstepB); PG8_STAGEAS(PG8_SA(1, 0), a3, 0);
;             PG8_WAIT_K(); PG8_WAIT_L(0); PG8_BAR; if constexpr (!HM) { PG8_MMA(1, 0, At, B0); PG8_MMA(1, 1, At, B1); } PG8_BAR; PG8_SCHED;
;         }
	ds_read_b128 v[142:145], v166
	ds_read_b128 v[146:149], v166 offset:1024
	ds_read_b128 v[150:153], v166 offset:2048
	ds_read_b128 v[170:173], v166 offset:3072
	ds_read_b128 v[174:177], v167
	ds_read_b128 v[178:181], v167 offset:1024
	ds_read_b128 v[182:185], v167 offset:2048
	ds_read_b128 v[186:189], v167 offset:3072
	ds_read_b128 v[190:193], v165 offset:32768
	ds_read_b128 v[194:197], v165 offset:33792
	ds_read_b128 v[198:201], v165 offset:34816
	ds_read_b128 v[202:205], v165 offset:35840
	ds_read_b128 v[206:209], v165 offset:36864
	ds_read_b128 v[210:213], v165 offset:37888
	ds_read_b128 v[214:217], v165 offset:38912
	ds_read_b128 v[218:221], v165 offset:39936
	s_mov_b32 m0, s60
	s_nop 0
	global_load_lds_dwordx4 v159, s[56:57]
	s_mov_b32 m0, s61
	s_nop 0
	global_load_lds_dwordx4 v160, s[56:57]
	s_waitcnt vmcnt(8)
	s_waitcnt lgkmcnt(0)
	s_barrier
	s_setprio 1
	v_mfma_f32_16x16x32_bf16 v[126:129], v[142:145], v[190:193], v[126:129]
	v_mfma_f32_16x16x32_bf16 v[122:125], v[150:153], v[190:193], v[122:125]
	v_mfma_f32_16x16x32_bf16 v[110:113], v[142:145], v[198:201], v[110:113]
	v_mfma_f32_16x16x32_bf16 v[106:109], v[150:153], v[198:201], v[106:109]
	v_mfma_f32_16x16x32_bf16 v[94:97], v[142:145], v[206:209], v[94:97]
	v_mfma_f32_16x16x32_bf16 v[90:93], v[150:153], v[206:209], v[90:93]
	v_mfma_f32_16x16x32_bf16 v[78:81], v[142:145], v[214:217], v[78:81]
	v_mfma_f32_16x16x32_bf16 v[74:77], v[150:153], v[214:217], v[74:77]
	v_mfma_f32_16x16x32_bf16 v[126:129], v[146:149], v[194:197], v[126:129]
	v_mfma_f32_16x16x32_bf16 v[122:125], v[170:173], v[194:197], v[122:125]
	v_mfma_f32_16x16x32_bf16 v[110:113], v[146:149], v[202:205], v[110:113]
	v_mfma_f32_16x16x32_bf16 v[106:109], v[170:173], v[202:205], v[106:109]
	v_mfma_f32_16x16x32_bf16 v[94:97], v[146:149], v[210:213], v[94:97]
	v_mfma_f32_16x16x32_bf16 v[90:93], v[170:173], v[210:213], v[90:93]
	v_mfma_f32_16x16x32_bf16 v[78:81], v[146:149], v[218:221], v[78:81]
	v_mfma_f32_16x16x32_bf16 v[74:77], v[170:173], v[218:221], v[74:77]
	v_mfma_f32_16x16x32_bf16 v[118:121], v[174:177], v[190:193], v[118:121]
	v_mfma_f32_16x16x32_bf16 v[114:117], v[182:185], v[190:193], v[114:117]
	v_mfma_f32_16x16x32_bf16 v[102:105], v[174:177], v[198:201], v[102:105]
	v_mfma_f32_16x16x32_bf16 v[98:101], v[182:185], v[198:201], v[98:101]
	v_mfma_f32_16x16x32_bf16 v[86:89], v[174:177], v[206:209], v[86:89]
	v_mfma_f32_16x16x32_bf16 v[82:85], v[182:185], v[206:209], v[82:85]
	v_mfma_f32_16x16x32_bf16 v[70:73], v[174:177], v[214:217], v[70:73]
	v_mfma_f32_16x16x32_bf16 v[66:69], v[182:185], v[214:217], v[66:69]
	v_mfma_f32_16x16x32_bf16 v[118:121], v[178:181], v[194:197], v[118:121]
	v_mfma_f32_16x16x32_bf16 v[114:117], v[186:189], v[194:197], v[114:117]
	v_mfma_f32_16x16x32_bf16 v[102:105], v[178:181], v[202:205], v[102:105]
	v_mfma_f32_16x16x32_bf16 v[98:101], v[186:189], v[202:205], v[98:101]
	v_mfma_f32_16x16x32_bf16 v[86:89], v[178:181], v[210:213], v[86:89]
	v_mfma_f32_16x16x32_bf16 v[82:85], v[186:189], v[210:213], v[82:85]
	v_mfma_f32_16x16x32_bf16 v[70:73], v[178:181], v[218:221], v[70:73]
	v_mfma_f32_16x16x32_bf16 v[66:69], v[186:189], v[218:221], v[66:69]
	s_setprio 0
	s_barrier
	ds_read_b128 v[190:193], v165 offset:49152
	ds_read_b128 v[194:197], v165 offset:50176
	ds_read_b128 v[198:201], v165 offset:51200
	ds_read_b128 v[202:205], v165 offset:52224
	ds_read_b128 v[206:209], v165 offset:53248
	ds_read_b128 v[210:213], v165 offset:54272
	ds_read_b128 v[214:217], v165 offset:55296
	ds_read_b128 v[218:221], v165 offset:56320
	s_add_u32 s56, s54, 0x80
	s_addc_u32 s57, s55, 0
	s_mov_b32 m0, s66
	s_nop 0
	global_load_lds_dwordx4 v1, s[56:57]
	s_add_u32 s54, s54, 0x80080
	s_mov_b32 m0, s67
	s_nop 0
	global_load_lds_dwordx4 v156, s[56:57]
	s_addc_u32 s55, s55, 0
	s_mov_b32 m0, s70
	s_nop 0
	global_load_lds_dwordx4 v1, s[54:55]
	s_mov_b32 m0, s71
	s_nop 0
	global_load_lds_dwordx4 v156, s[54:55]
	s_mov_b32 m0, s68
	s_nop 0
	global_load_lds_dwordx4 v157, s[12:13]
	s_mov_b32 m0, s69
	s_nop 0
	global_load_lds_dwordx4 v158, s[12:13]
	s_waitcnt vmcnt(8)
	s_waitcnt lgkmcnt(0)
	s_barrier
	s_setprio 1
	v_mfma_f32_16x16x32_bf16 v[62:65], v[142:145], v[190:193], v[62:65]
	v_mfma_f32_16x16x32_bf16 v[58:61], v[150:153], v[190:193], v[58:61]
	v_mfma_f32_16x16x32_bf16 v[46:49], v[142:145], v[198:201], v[46:49]
	v_mfma_f32_16x16x32_bf16 v[42:45], v[150:153], v[198:201], v[42:45]
	v_mfma_f32_16x16x32_bf16 v[30:33], v[142:145], v[206:209], v[30:33]
	v_mfma_f32_16x16x32_bf16 v[26:29], v[150:153], v[206:209], v[26:29]
	v_mfma_f32_16x16x32_bf16 v[14:17], v[142:145], v[214:217], v[14:17]
	v_mfma_f32_16x16x32_bf16 v[10:13], v[150:153], v[214:217], v[10:13]
	v_mfma_f32_16x16x32_bf16 v[62:65], v[146:149], v[194:197], v[62:65]
	v_mfma_f32_16x16x32_bf16 v[58:61], v[170:173], v[194:197], v[58:61]
	v_mfma_f32_16x16x32_bf16 v[46:49], v[146:149], v[202:205], v[46:49]
	v_mfma_f32_16x16x32_bf16 v[42:45], v[170:173], v[202:205], v[42:45]
	v_mfma_f32_16x16x32_bf16 v[30:33], v[146:149], v[210:213], v[30:33]
	v_mfma_f32_16x16x32_bf16 v[26:29], v[170:173], v[210:213], v[26:29]
	v_mfma_f32_16x16x32_bf16 v[14:17], v[146:149], v[218:221], v[14:17]
	v_mfma_f32_16x16x32_bf16 v[10:13], v[170:173], v[218:221], v[10:13]
	v_mfma_f32_16x16x32_bf16 v[54:57], v[174:177], v[190:193], v[54:57]
	v_mfma_f32_16x16x32_bf16 v[50:53], v[182:185], v[190:193], v[50:53]
	v_mfma_f32_16x16x32_bf16 v[38:41], v[174:177], v[198:201], v[38:41]
	v_mfma_f32_16x16x32_bf16 v[34:37], v[182:185], v[198:201], v[34:37]
	v_mfma_f32_16x16x32_bf16 v[22:25], v[174:177], v[206:209], v[22:25]
	v_mfma_f32_16x16x32_bf16 v[18:21], v[182:185], v[206:209], v[18:21]
	v_mfma_f32_16x16x32_bf16 v[6:9], v[174:177], v[214:217], v[6:9]
	v_mfma_f32_16x16x32_bf16 v[2:5], v[182:185], v[214:217], v[2:5]
	v_mfma_f32_16x16x32_bf16 v[54:57], v[178:181], v[194:197], v[54:57]
	v_mfma_f32_16x16x32_bf16 v[50:53], v[186:189], v[194:197], v[50:53]
	v_mfma_f32_16x16x32_bf16 v[38:41], v[178:181], v[202:205], v[38:41]
	v_mfma_f32_16x16x32_bf16 v[34:37], v[186:189], v[202:205], v[34:37]
	v_mfma_f32_16x16x32_bf16 v[22:25], v[178:181], v[210:213], v[22:25]
	v_mfma_f32_16x16x32_bf16 v[18:21], v[186:189], v[210:213], v[18:21]
	v_mfma_f32_16x16x32_bf16 v[6:9], v[178:181], v[218:221], v[6:9]
	v_mfma_f32_16x16x32_bf16 v[2:5], v[186:189], v[218:221], v[2:5]
	s_setprio 0
	s_barrier
	s_add_i32 s47, s47, 2
	s_add_u32 s4, s4, 0x100
	s_addc_u32 s11, s11, 0
	s_add_u32 s33, s33, 0x100
	s_addc_u32 s45, s45, 0
	s_add_u32 s0, s0, 0x100
	s_addc_u32 s1, s1, 0
	s_cmp_gt_u32 s47, 29
	s_cbranch_scc0 .LBB0_140
	s_and_b64 vcc, exec, s[20:21]
	s_cbranch_vccnz .LBB0_144
	v_lshl_add_u32 v142, s10, 8, v161
	s_cmp_gt_i32 s52, 7
	s_mov_b64 s[0:1], -1
	s_cbranch_scc1 .LBB0_145

; #define PG8_STAGEB(bufoff, gbase) PG8_STAGE2(bufoff, gbase, voffB[0], voffB[1])
; #define PG8_STAGEAS(bufoff, gbase, h) PG8_STAGE2(bufoff, gbase, voffA[h][0], voffA[h][1])
; #define PG8_LDA(dst, b, h) do { _Pragma("unroll") for (int m = 0; m < 4; ++m) _Pragma("unroll") for (int k = 0; k < 2; ++k) dst[m][k] = *(const LAS bf16x8*)(lds + PG8_SA(b, h) + aoff + m * 2048 + k * 1024); } while (0)
; #define PG8_WAIT_K0() do { if (EST > 0 && t == 0 && ui > 0) asm volatile("s_waitcnt vmcnt(%0)" :: "n"((HM ? 6 : 8) + EST) : "memory"); else PG8_WAIT_K(); } while (0)
; #define PG8_WAIT_L(n) asm volatile("s_waitcnt lgkmcnt(" #n ")" ::: "memory")
; #define PG8_BAR __builtin_amdgcn_s_barrier()
; #define PG8_SCHED __builtin_amdgcn_sched_barrier(0)
;     ...
;             PG8_WAIT_K0(); PG8_WAIT_L(0); PG8_BAR; PG8_MMA(0, 0, At, B0); PG8_MMA(0, 1, At, B1); PG8_BAR; PG8_SCHED;
;             if constexpr (!HM) PG8_LDA(At, 0, 1);
;             PG8_STAGEB(PG8_SB(0, 0), b2); PG8_STAGEB(PG8_SB(0, 1), b2 + hstepB); PG8_STAGEAS(PG8_SA(0, 0), a2, 0);
.LBB0_577:
	s_add_u32 s44, s38, 0x100
	s_waitcnt lgkmcnt(0)
	s_addc_u32 s45, s39, 0
	s_add_u32 s46, s40, 0x100
	s_addc_u32 s47, s41, 0
	s_barrier
	s_setprio 1
	v_mfma_f32_16x16x32_bf16 v[34:37], v[18:21], v[74:77], 0
	v_mfma_f32_16x16x32_bf16 v[38:41], v[26:29], v[74:77], 0
	v_mfma_f32_16x16x32_bf16 v[42:45], v[18:21], v[82:85], 0
	v_mfma_f32_16x16x32_bf16 v[46:49], v[26:29], v[82:85], 0
	v_mfma_f32_16x16x32_bf16 v[50:53], v[18:21], v[94:97], 0
	v_mfma_f32_16x16x32_bf16 v[54:57], v[26:29], v[94:97], 0
	v_mfma_f32_16x16x32_bf16 v[58:61], v[18:21], v[70:73], 0
	v_mfma_f32_16x16x32_bf16 v[62:65], v[26:29], v[70:73], 0
	v_mfma_f32_16x16x32_bf16 v[34:37], v[22:25], v[78:81], v[34:37]
	v_mfma_f32_16x16x32_bf16 v[38:41], v[30:33], v[78:81], v[38:41]
	v_mfma_f32_16x16x32_bf16 v[42:45], v[22:25], v[90:93], v[42:45]
	v_mfma_f32_16x16x32_bf16 v[46:49], v[30:33], v[90:93], v[46:49]
	v_mfma_f32_16x16x32_bf16 v[50:53], v[22:25], v[98:101], v[50:53]
	v_mfma_f32_16x16x32_bf16 v[54:57], v[30:33], v[98:101], v[54:57]
	v_mfma_f32_16x16x32_bf16 v[58:61], v[22:25], v[86:89], v[58:61]
	v_mfma_f32_16x16x32_bf16 v[62:65], v[30:33], v[86:89], v[62:65]
	v_mfma_f32_16x16x32_bf16 v[66:69], v[2:5], v[74:77], 0
	v_mfma_f32_16x16x32_bf16 v[74:77], v[10:13], v[74:77], 0
	v_mfma_f32_16x16x32_bf16 v[66:69], v[6:9], v[78:81], v[66:69]
	v_mfma_f32_16x16x32_bf16 v[74:77], v[14:17], v[78:81], v[74:77]
	v_mfma_f32_16x16x32_bf16 v[78:81], v[2:5], v[82:85], 0
	v_mfma_f32_16x16x32_bf16 v[82:85], v[10:13], v[82:85], 0
	v_mfma_f32_16x16x32_bf16 v[78:81], v[6:9], v[90:93], v[78:81]
	v_mfma_f32_16x16x32_bf16 v[82:85], v[14:17], v[90:93], v[82:85]
	v_mfma_f32_16x16x32_bf16 v[90:93], v[2:5], v[94:97], 0
	v_mfma_f32_16x16x32_bf16 v[94:97], v[10:13], v[94:97], 0
	v_mfma_f32_16x16x32_bf16 v[130:133], v[14:17], v[98:101], v[94:97]
	v_mfma_f32_16x16x32_bf16 v[94:97], v[2:5], v[70:73], 0
	v_mfma_f32_16x16x32_bf16 v[70:73], v[10:13], v[70:73], 0
	v_mfma_f32_16x16x32_bf16 v[90:93], v[6:9], v[98:101], v[90:93]
	v_mfma_f32_16x16x32_bf16 v[134:137], v[6:9], v[86:89], v[94:97]
	v_mfma_f32_16x16x32_bf16 v[138:141], v[14:17], v[86:89], v[70:73]
	s_setprio 0
	s_barrier
	ds_read_b128 v[110:113], v169 offset:16384
	ds_read_b128 v[114:117], v169 offset:17408
	ds_read_b128 v[102:105], v169 offset:18432
	ds_read_b128 v[106:109], v169 offset:19456
	ds_read_b128 v[94:97], v169 offset:20480
	ds_read_b128 v[98:101], v169 offset:21504
	ds_read_b128 v[70:73], v169 offset:22528
	ds_read_b128 v[86:89], v169 offset:23552
	s_mov_b32 m0, s37
	s_nop 0
	global_load_lds_dwordx4 v158, s[46:47]
	s_mov_b32 m0, s56
	s_nop 0
	global_load_lds_dwordx4 v159, s[46:47]
	s_add_u32 s46, s40, 0x40100
	s_addc_u32 s47, s41, 0
	s_mov_b32 m0, s57
	s_nop 0
	global_load_lds_dwordx4 v158, s[46:47]
	s_and_b64 vcc, exec, s[42:43]
	s_mov_b32 m0, s58
	s_nop 0
	global_load_lds_dwordx4 v159, s[46:47]
	s_mov_b32 m0, s55
	s_nop 0
	global_load_lds_dwordx4 v160, s[44:45]
	s_mov_b32 m0, s59
	s_nop 0
	global_load_lds_dwordx4 v161, s[44:45]
	s_cbranch_vccz .LBB0_588
	s_waitcnt vmcnt(24)
	s_cbranch_execnz .LBB0_580

; #define PG8_STAGEAS(bufoff, gbase, h) PG8_STAGE2(bufoff, gbase, voffA[h][0], voffA[h][1])
; #define PG8_LDA(dst, b, h) do { _Pragma("unroll") for (int m = 0; m < 4; ++m) _Pragma("unroll") for (int k = 0; k < 2; ++k) dst[m][k] = *(const LAS bf16x8*)(lds + PG8_SA(b, h) + aoff + m * 2048 + k * 1024); } while (0)
; #define PG8_LDB(dst, b, h) do { _Pragma("unroll") for (int n = 0; n < 2; ++n) _Pragma("unroll") for (int k = 0; k < 2; ++k) dst[n][k] = *(const LAS bf16x8*)(lds + PG8_SB(b, h) + boff + n * 2048 + k * 1024); } while (0)
; #define PG8_WAIT_K() do { if constexpr (HM) PG8_WAIT_V(6); else PG8_WAIT_V(8); } while (0)
; #define PG8_WAIT_K0() do { if (EST > 0 && t == 0 && ui > 0) asm volatile("s_waitcnt vmcnt(%0)" :: "n"((HM ? 6 : 8) + EST) : "memory"); else PG8_WAIT_K(); } while (0)
; #define PG8_WAIT_L(n) asm volatile("s_waitcnt lgkmcnt(" #n ")" ::: "memory")
; #define PG8_BAR __builtin_amdgcn_s_barrier()
; #define PG8_SCHED __builtin_amdgcn_sched_barrier(0)
;     ...
;             PG8_WAIT_K0(); PG8_WAIT_L(0); PG8_BAR; if constexpr (!HM) { PG8_MMA(1, 0, At, B0); PG8_MMA(1, 1, At, B1); } PG8_BAR; PG8_SCHED;
;             PG8_LDB(B0, 1, 0); PG8_LDB(B1, 1, 1); PG8_SCHED; PG8_LDA(At, 1, 0); if constexpr (!HM) PG8_STAGEAS(PG8_SA(0, 1), a2, 1);
;             PG8_WAIT_K(); PG8_WAIT_L(0); PG8_BAR; PG8_MMA(0, 0, At, B0); PG8_MMA(0, 1, At, B1); PG8_BAR; PG8_SCHED;
.LBB0_580:
	s_add_u32 s42, s38, 0x180
	s_waitcnt lgkmcnt(0)
	s_addc_u32 s43, s39, 0
	s_add_u32 s46, s40, 0x180
	s_addc_u32 s47, s41, 0
	s_barrier
	s_setprio 1
	v_mfma_f32_16x16x32_bf16 v[118:121], v[18:21], v[110:113], 0
	v_mfma_f32_16x16x32_bf16 v[150:153], v[22:25], v[114:117], v[118:121]
	v_mfma_f32_16x16x32_bf16 v[118:121], v[26:29], v[110:113], 0
	v_mfma_f32_16x16x32_bf16 v[154:157], v[30:33], v[114:117], v[118:121]
	v_mfma_f32_16x16x32_bf16 v[118:121], v[18:21], v[102:105], 0
	v_mfma_f32_16x16x32_bf16 v[170:173], v[22:25], v[106:109], v[118:121]
	v_mfma_f32_16x16x32_bf16 v[118:121], v[26:29], v[102:105], 0
	v_mfma_f32_16x16x32_bf16 v[174:177], v[30:33], v[106:109], v[118:121]
	v_mfma_f32_16x16x32_bf16 v[118:121], v[18:21], v[94:97], 0
	v_mfma_f32_16x16x32_bf16 v[18:21], v[18:21], v[70:73], 0
	v_mfma_f32_16x16x32_bf16 v[178:181], v[22:25], v[98:101], v[118:121]
	v_mfma_f32_16x16x32_bf16 v[18:21], v[22:25], v[86:89], v[18:21]
	v_mfma_f32_16x16x32_bf16 v[22:25], v[26:29], v[70:73], 0
	v_mfma_f32_16x16x32_bf16 v[118:121], v[26:29], v[94:97], 0
	v_mfma_f32_16x16x32_bf16 v[22:25], v[30:33], v[86:89], v[22:25]
	v_mfma_f32_16x16x32_bf16 v[182:185], v[30:33], v[98:101], v[118:121]
	v_mfma_f32_16x16x32_bf16 v[26:29], v[2:5], v[110:113], 0
	v_mfma_f32_16x16x32_bf16 v[186:189], v[6:9], v[114:117], v[26:29]
	v_mfma_f32_16x16x32_bf16 v[26:29], v[10:13], v[110:113], 0
	v_mfma_f32_16x16x32_bf16 v[190:193], v[14:17], v[114:117], v[26:29]
	v_mfma_f32_16x16x32_bf16 v[26:29], v[2:5], v[102:105], 0
	v_mfma_f32_16x16x32_bf16 v[194:197], v[6:9], v[106:109], v[26:29]
	v_mfma_f32_16x16x32_bf16 v[26:29], v[10:13], v[102:105], 0
	v_mfma_f32_16x16x32_bf16 v[198:201], v[14:17], v[106:109], v[26:29]
	v_mfma_f32_16x16x32_bf16 v[26:29], v[2:5], v[94:97], 0
	v_mfma_f32_16x16x32_bf16 v[2:5], v[2:5], v[70:73], 0
	v_mfma_f32_16x16x32_bf16 v[202:205], v[6:9], v[98:101], v[26:29]
	v_mfma_f32_16x16x32_bf16 v[26:29], v[10:13], v[94:97], 0
	v_mfma_f32_16x16x32_bf16 v[2:5], v[6:9], v[86:89], v[2:5]
	v_mfma_f32_16x16x32_bf16 v[6:9], v[10:13], v[70:73], 0
	v_mfma_f32_16x16x32_bf16 v[206:209], v[14:17], v[98:101], v[26:29]
	v_mfma_f32_16x16x32_bf16 v[210:213], v[14:17], v[86:89], v[6:9]
	s_setprio 0
	s_barrier
	v_add_u32_e32 v142, 0x18000, v166
	v_add_u32_e32 v143, 0x1c000, v166
	s_nop 1
	ds_read_b128 v[6:9], v142
	ds_read_b128 v[10:13], v142 offset:1024
	ds_read_b128 v[214:217], v142 offset:2048
	ds_read_b128 v[218:221], v142 offset:3072
	ds_read_b128 v[222:225], v143
	ds_read_b128 v[226:229], v143 offset:1024
	ds_read_b128 v[230:233], v143 offset:2048
	ds_read_b128 v[234:237], v143 offset:3072
	ds_read_b128 v[14:17], v169 offset:32768
	ds_read_b128 v[26:29], v169 offset:33792
	ds_read_b128 v[30:33], v169 offset:34816
	ds_read_b128 v[98:101], v169 offset:35840
	ds_read_b128 v[238:241], v169 offset:36864
	ds_read_b128 v[242:245], v169 offset:37888
	ds_read_b128 v[246:249], v169 offset:38912
	ds_read_b128 v[250:253], v169 offset:39936
	s_mov_b32 m0, s60
	s_nop 0
	global_load_lds_dwordx4 v162, s[44:45]
	s_mov_b32 m0, s61
	s_nop 0
	global_load_lds_dwordx4 v163, s[44:45]
	s_waitcnt vmcnt(8)
	s_waitcnt lgkmcnt(0)
	s_barrier
	s_setprio 1
	v_mfma_f32_16x16x32_bf16 v[34:37], v[6:9], v[14:17], v[34:37]
	v_mfma_f32_16x16x32_bf16 v[114:117], v[10:13], v[26:29], v[34:37]
	v_mfma_f32_16x16x32_bf16 v[34:37], v[214:217], v[14:17], v[38:41]
	v_mfma_f32_16x16x32_bf16 v[110:113], v[218:221], v[26:29], v[34:37]
	v_mfma_f32_16x16x32_bf16 v[34:37], v[6:9], v[30:33], v[42:45]
	v_mfma_f32_16x16x32_bf16 v[106:109], v[10:13], v[98:101], v[34:37]
	v_mfma_f32_16x16x32_bf16 v[34:37], v[214:217], v[30:33], v[46:49]
	v_mfma_f32_16x16x32_bf16 v[102:105], v[218:221], v[98:101], v[34:37]
	v_mfma_f32_16x16x32_bf16 v[34:37], v[6:9], v[238:241], v[50:53]
	v_mfma_f32_16x16x32_bf16 v[94:97], v[10:13], v[242:245], v[34:37]
	v_mfma_f32_16x16x32_bf16 v[34:37], v[214:217], v[238:241], v[54:57]
	v_mfma_f32_16x16x32_bf16 v[86:89], v[218:221], v[242:245], v[34:37]
	v_mfma_f32_16x16x32_bf16 v[34:37], v[6:9], v[246:249], v[58:61]
	v_mfma_f32_16x16x32_bf16 v[70:73], v[10:13], v[250:253], v[34:37]
	v_mfma_f32_16x16x32_bf16 v[34:37], v[214:217], v[246:249], v[62:65]
	v_mfma_f32_16x16x32_bf16 v[58:61], v[218:221], v[250:253], v[34:37]
	v_mfma_f32_16x16x32_bf16 v[34:37], v[222:225], v[14:17], v[66:69]
	v_mfma_f32_16x16x32_bf16 v[14:17], v[230:233], v[14:17], v[74:77]
	v_mfma_f32_16x16x32_bf16 v[122:125], v[234:237], v[26:29], v[14:17]
	v_mfma_f32_16x16x32_bf16 v[14:17], v[222:225], v[30:33], v[78:81]
	v_mfma_f32_16x16x32_bf16 v[118:121], v[226:229], v[98:101], v[14:17]
	v_mfma_f32_16x16x32_bf16 v[14:17], v[230:233], v[30:33], v[82:85]
	v_mfma_f32_16x16x32_bf16 v[98:101], v[234:237], v[98:101], v[14:17]
	v_mfma_f32_16x16x32_bf16 v[14:17], v[222:225], v[238:241], v[90:93]
	v_mfma_f32_16x16x32_bf16 v[90:93], v[226:229], v[242:245], v[14:17]
	v_mfma_f32_16x16x32_bf16 v[14:17], v[230:233], v[238:241], v[130:133]
	v_mfma_f32_16x16x32_bf16 v[82:85], v[234:237], v[242:245], v[14:17]
	v_mfma_f32_16x16x32_bf16 v[14:17], v[222:225], v[246:249], v[134:137]
	v_mfma_f32_16x16x32_bf16 v[66:69], v[226:229], v[250:253], v[14:17]
	v_mfma_f32_16x16x32_bf16 v[14:17], v[230:233], v[246:249], v[138:141]
	v_mfma_f32_16x16x32_bf16 v[126:129], v[226:229], v[26:29], v[34:37]
	v_mfma_f32_16x16x32_bf16 v[54:57], v[234:237], v[250:253], v[14:17]
	s_setprio 0
	s_barrier
; #define LAS __attribute__((address_space(3)))
; #define PG8_STAGEB(bufoff, gbase) PG8_STAGE2(bufoff, gbase, voffB[0], voffB[1])
; #define PG8_STAGEA(bufoff, gbase, h) PG8_STAGE2(bufoff, gbase, voffA[h][0], voffA[h][1])
; #define PG8_STAGEAS(bufoff, gbase, h) PG8_STAGE2(bufoff, gbase, voffA[h][0], voffA[h][1])
; #define PG8_LDA(dst, b, h) do { _Pragma("unroll") for (int m = 0; m < 4; ++m) _Pragma("unroll") for (int k = 0; k < 2; ++k) dst[m][k] = *(const LAS bf16x8*)(lds + PG8_SA(b, h) + aoff + m * 2048 + k * 1024); } while (0)
; #define PG8_LDB(dst, b, h) do { _Pragma("unroll") for (int n = 0; n < 2; ++n) _Pragma("unroll") for (int k = 0; k < 2; ++k) dst[n][k] = *(const LAS bf16x8*)(lds + PG8_SB(b, h) + boff + n * 2048 + k * 1024); } while (0)
; #define PG8_WAIT_K() do { if constexpr (HM) PG8_WAIT_V(6); else PG8_WAIT_V(8); } while (0)
; #define PG8_WAIT_K0() do { if (EST > 0 && t == 0 && ui > 0) asm volatile("s_waitcnt vmcnt(%0)" :: "n"((HM ? 6 : 8) + EST) : "memory"); else PG8_WAIT_K(); } while (0)
; #define PG8_WAIT_L(n) asm volatile("s_waitcnt lgkmcnt(" #n ")" ::: "memory")
; #define PG8_BAR __builtin_amdgcn_s_barrier()
; #define PG8_SCHED __builtin_amdgcn_sched_barrier(0)
;     ...
;             PG8_LDB(B0, 0, 0); PG8_LDB(B1, 0, 1); PG8_SCHED; PG8_LDA(At, 0, 0); if constexpr (!HM) PG8_STAGEA(PG8_SA(1, 1), a1, 1);
;             if constexpr (Sched::kGather) { if (last && has_next) { const u32x4 tn = *(const LAS u32x4*)(S.aux + tid * 16); voffA[0][0] = tn.x; voffA[0][1] = tn.y; voffA[1][0] = tn.z; voffA[1][1] = tn.w; } }
;             PG8_WAIT_K0(); PG8_WAIT_L(0); PG8_BAR; PG8_MMA(0, 0, At, B0); PG8_MMA(0, 1, At, B1); PG8_BAR; PG8_SCHED;
;     ...
;             if constexpr (!HM) PG8_LDA(At, 1, 1);
;             PG8_STAGEB(PG8_SB(1, 0), b3); PG8_STAGEB(PG8_SB(1, 1), b3 + hstepB); PG8_STAGEAS(PG8_SA(1, 0), a3, 0);
;             PG8_WAIT_K(); PG8_WAIT_L(0); PG8_BAR; if constexpr (!HM) { PG8_MMA(1, 0, At, B0); PG8_MMA(1, 1, At, B1); } PG8_BAR; PG8_SCHED;
	ds_read_b128 v[34:37], v169 offset:49152
	ds_read_b128 v[38:41], v169 offset:50176
	ds_read_b128 v[130:133], v169 offset:51200
	ds_read_b128 v[134:137], v169 offset:52224
	ds_read_b128 v[138:141], v169 offset:53248
	ds_read_b128 v[238:241], v169 offset:54272
	ds_read_b128 v[242:245], v169 offset:55296
	ds_read_b128 v[246:249], v169 offset:56320
	s_mov_b32 m0, s62
	s_nop 0
	global_load_lds_dwordx4 v158, s[46:47]
	s_add_u32 s44, s40, 0x40180
	s_mov_b32 m0, s63
	s_nop 0
	global_load_lds_dwordx4 v159, s[46:47]
	s_addc_u32 s45, s41, 0
	s_mov_b32 m0, s66
	s_nop 0
	global_load_lds_dwordx4 v158, s[44:45]
	s_mov_b32 m0, s67
	s_nop 0
	global_load_lds_dwordx4 v159, s[44:45]
	s_mov_b32 m0, s64
	s_nop 0
	global_load_lds_dwordx4 v160, s[42:43]
	s_mov_b32 m0, s65
	s_nop 0
	global_load_lds_dwordx4 v161, s[42:43]
	s_waitcnt vmcnt(8)
	s_waitcnt lgkmcnt(0)
	s_barrier
	s_setprio 1
	v_mfma_f32_16x16x32_bf16 v[14:17], v[6:9], v[34:37], v[150:153]
	v_mfma_f32_16x16x32_bf16 v[78:81], v[10:13], v[38:41], v[14:17]
	v_mfma_f32_16x16x32_bf16 v[14:17], v[214:217], v[34:37], v[154:157]
	v_mfma_f32_16x16x32_bf16 v[74:77], v[218:221], v[38:41], v[14:17]
	v_mfma_f32_16x16x32_bf16 v[14:17], v[6:9], v[130:133], v[170:173]
	v_mfma_f32_16x16x32_bf16 v[46:49], v[10:13], v[134:137], v[14:17]
	v_mfma_f32_16x16x32_bf16 v[14:17], v[214:217], v[130:133], v[174:177]
	v_mfma_f32_16x16x32_bf16 v[42:45], v[218:221], v[134:137], v[14:17]
	v_mfma_f32_16x16x32_bf16 v[14:17], v[6:9], v[138:141], v[178:181]
	v_mfma_f32_16x16x32_bf16 v[30:33], v[10:13], v[238:241], v[14:17]
	v_mfma_f32_16x16x32_bf16 v[14:17], v[214:217], v[138:141], v[182:185]
	v_mfma_f32_16x16x32_bf16 v[6:9], v[6:9], v[242:245], v[18:21]
	v_mfma_f32_16x16x32_bf16 v[26:29], v[218:221], v[238:241], v[14:17]
	v_mfma_f32_16x16x32_bf16 v[14:17], v[10:13], v[246:249], v[6:9]
	v_mfma_f32_16x16x32_bf16 v[6:9], v[214:217], v[242:245], v[22:25]
	v_mfma_f32_16x16x32_bf16 v[10:13], v[218:221], v[246:249], v[6:9]
	v_mfma_f32_16x16x32_bf16 v[6:9], v[222:225], v[34:37], v[186:189]
	v_mfma_f32_16x16x32_bf16 v[62:65], v[226:229], v[38:41], v[6:9]
	v_mfma_f32_16x16x32_bf16 v[6:9], v[230:233], v[34:37], v[190:193]
	v_mfma_f32_16x16x32_bf16 v[50:53], v[234:237], v[38:41], v[6:9]
	v_mfma_f32_16x16x32_bf16 v[6:9], v[222:225], v[130:133], v[194:197]
	v_mfma_f32_16x16x32_bf16 v[38:41], v[226:229], v[134:137], v[6:9]
	v_mfma_f32_16x16x32_bf16 v[6:9], v[230:233], v[130:133], v[198:201]
	v_mfma_f32_16x16x32_bf16 v[34:37], v[234:237], v[134:137], v[6:9]
	v_mfma_f32_16x16x32_bf16 v[6:9], v[222:225], v[138:141], v[202:205]
	v_mfma_f32_16x16x32_bf16 v[22:25], v[226:229], v[238:241], v[6:9]
	v_mfma_f32_16x16x32_bf16 v[6:9], v[230:233], v[138:141], v[206:209]
	v_mfma_f32_16x16x32_bf16 v[2:5], v[222:225], v[242:245], v[2:5]
	v_mfma_f32_16x16x32_bf16 v[18:21], v[234:237], v[238:241], v[6:9]
	v_mfma_f32_16x16x32_bf16 v[6:9], v[226:229], v[246:249], v[2:5]
	v_mfma_f32_16x16x32_bf16 v[2:5], v[230:233], v[242:245], v[210:213]
	v_mfma_f32_16x16x32_bf16 v[2:5], v[234:237], v[246:249], v[2:5]
	s_setprio 0
	s_barrier
	s_add_u32 s29, s38, 0x200
	s_addc_u32 s31, s39, 0
	s_add_u32 s72, s40, 0x200
	s_addc_u32 s73, s41, 0
	s_mov_b32 s74, 0
.LBB0_581:
	ds_read_b128 v[130:133], v167
	ds_read_b128 v[134:137], v167 offset:1024
	ds_read_b128 v[138:141], v167 offset:2048
	ds_read_b128 v[150:153], v167 offset:3072
	ds_read_b128 v[154:157], v168
	ds_read_b128 v[170:173], v168 offset:1024
	ds_read_b128 v[174:177], v168 offset:2048
	ds_read_b128 v[178:181], v168 offset:3072
	s_cmp_eq_u32 s74, 12
	s_cselect_b32 s46, s0, s29
	s_cselect_b32 s47, s1, s31
	s_cselect_b32 s40, s34, s72
	s_cselect_b32 s41, s35, s73
	s_add_u32 s38, s46, 0x80
	s_addc_u32 s39, s47, 0
	ds_read_b128 v[182:185], v169
	ds_read_b128 v[186:189], v169 offset:1024
	ds_read_b128 v[190:193], v169 offset:2048
	ds_read_b128 v[194:197], v169 offset:3072
	ds_read_b128 v[198:201], v169 offset:4096
	ds_read_b128 v[202:205], v169 offset:5120
	ds_read_b128 v[206:209], v169 offset:6144
	ds_read_b128 v[210:213], v169 offset:7168
	s_mov_b32 m0, s68
	s_nop 0
	global_load_lds_dwordx4 v162, s[42:43]
	s_add_u32 s44, s40, 0x80
	s_mov_b32 m0, s69
	s_nop 0
	global_load_lds_dwordx4 v163, s[42:43]
	s_waitcnt vmcnt(8)
	s_waitcnt lgkmcnt(0)
	s_addc_u32 s45, s41, 0
	s_barrier
	s_setprio 1
	v_mfma_f32_16x16x32_bf16 v[114:117], v[130:133], v[182:185], v[114:117]
	v_mfma_f32_16x16x32_bf16 v[110:113], v[138:141], v[182:185], v[110:113]
	v_mfma_f32_16x16x32_bf16 v[106:109], v[130:133], v[190:193], v[106:109]
	v_mfma_f32_16x16x32_bf16 v[102:105], v[138:141], v[190:193], v[102:105]
	v_mfma_f32_16x16x32_bf16 v[94:97], v[130:133], v[198:201], v[94:97]
	v_mfma_f32_16x16x32_bf16 v[86:89], v[138:141], v[198:201], v[86:89]
	v_mfma_f32_16x16x32_bf16 v[70:73], v[130:133], v[206:209], v[70:73]
	v_mfma_f32_16x16x32_bf16 v[58:61], v[138:141], v[206:209], v[58:61]
	v_mfma_f32_16x16x32_bf16 v[114:117], v[134:137], v[186:189], v[114:117]
	v_mfma_f32_16x16x32_bf16 v[110:113], v[150:153], v[186:189], v[110:113]
	v_mfma_f32_16x16x32_bf16 v[106:109], v[134:137], v[194:197], v[106:109]
	v_mfma_f32_16x16x32_bf16 v[102:105], v[150:153], v[194:197], v[102:105]
	v_mfma_f32_16x16x32_bf16 v[94:97], v[134:137], v[202:205], v[94:97]
	v_mfma_f32_16x16x32_bf16 v[86:89], v[150:153], v[202:205], v[86:89]
	v_mfma_f32_16x16x32_bf16 v[70:73], v[134:137], v[210:213], v[70:73]
	v_mfma_f32_16x16x32_bf16 v[58:61], v[150:153], v[210:213], v[58:61]
	v_mfma_f32_16x16x32_bf16 v[126:129], v[154:157], v[182:185], v[126:129]
	v_mfma_f32_16x16x32_bf16 v[122:125], v[174:177], v[182:185], v[122:125]
	v_mfma_f32_16x16x32_bf16 v[118:121], v[154:157], v[190:193], v[118:121]
	v_mfma_f32_16x16x32_bf16 v[98:101], v[174:177], v[190:193], v[98:101]
	v_mfma_f32_16x16x32_bf16 v[90:93], v[154:157], v[198:201], v[90:93]
	v_mfma_f32_16x16x32_bf16 v[82:85], v[174:177], v[198:201], v[82:85]
	v_mfma_f32_16x16x32_bf16 v[66:69], v[154:157], v[206:209], v[66:69]
	v_mfma_f32_16x16x32_bf16 v[54:57], v[174:177], v[206:209], v[54:57]
	v_mfma_f32_16x16x32_bf16 v[126:129], v[170:173], v[186:189], v[126:129]
	v_mfma_f32_16x16x32_bf16 v[122:125], v[178:181], v[186:189], v[122:125]
	v_mfma_f32_16x16x32_bf16 v[118:121], v[170:173], v[194:197], v[118:121]
	v_mfma_f32_16x16x32_bf16 v[98:101], v[178:181], v[194:197], v[98:101]
	v_mfma_f32_16x16x32_bf16 v[90:93], v[170:173], v[202:205], v[90:93]
	v_mfma_f32_16x16x32_bf16 v[82:85], v[178:181], v[202:205], v[82:85]
	v_mfma_f32_16x16x32_bf16 v[66:69], v[170:173], v[210:213], v[66:69]
	v_mfma_f32_16x16x32_bf16 v[54:57], v[178:181], v[210:213], v[54:57]
	s_setprio 0
	s_barrier
; #define PG8_STAGEB(bufoff, gbase) PG8_STAGE2(bufoff, gbase, voffB[0], voffB[1])
; #define PG8_STAGEAS(bufoff, gbase, h) PG8_STAGE2(bufoff, gbase, voffA[h][0], voffA[h][1])
; #define PG8_LDA(dst, b, h) do { _Pragma("unroll") for (int m = 0; m < 4; ++m) _Pragma("unroll") for (int k = 0; k < 2; ++k) dst[m][k] = *(const LAS bf16x8*)(lds + PG8_SA(b, h) + aoff + m * 2048 + k * 1024); } while (0)
; #define PG8_LDB(dst, b, h) do { _Pragma("unroll") for (int n = 0; n < 2; ++n) _Pragma("unroll") for (int k = 0; k < 2; ++k) dst[n][k] = *(const LAS bf16x8*)(lds + PG8_SB(b, h) + boff + n * 2048 + k * 1024); } while (0)
; #define PG8_WAIT_K() do { if constexpr (HM) PG8_WAIT_V(6); else PG8_WAIT_V(8); } while (0)
; #define PG8_WAIT_K0() do { if (EST > 0 && t == 0 && ui > 0) asm volatile("s_waitcnt vmcnt(%0)" :: "n"((HM ? 6 : 8) + EST) : "memory"); else PG8_WAIT_K(); } while (0)
; #define PG8_WAIT_L(n) asm volatile("s_waitcnt lgkmcnt(" #n ")" ::: "memory")
; #define PG8_BAR __builtin_amdgcn_s_barrier()
; #define PG8_SCHED __builtin_amdgcn_sched_barrier(0)
;     ...
;             if constexpr (!HM) PG8_LDA(At, 0, 1);
;             PG8_STAGEB(PG8_SB(0, 0), b2); PG8_STAGEB(PG8_SB(0, 1), b2 + hstepB); PG8_STAGEAS(PG8_SA(0, 0), a2, 0);
;             PG8_WAIT_K0(); PG8_WAIT_L(0); PG8_BAR; if constexpr (!HM) { PG8_MMA(1, 0, At, B0); PG8_MMA(1, 1, At, B1); } PG8_BAR; PG8_SCHED;
;             PG8_LDB(B0, 1, 0); PG8_LDB(B1, 1, 1); PG8_SCHED; PG8_LDA(At, 1, 0); if constexpr (!HM) PG8_STAGEAS(PG8_SA(0, 1), a2, 1);
;             PG8_WAIT_K(); PG8_WAIT_L(0); PG8_BAR; PG8_MMA(0, 0, At, B0); PG8_MMA(0, 1, At, B1); PG8_BAR; PG8_SCHED;
	ds_read_b128 v[182:185], v169 offset:16384
	ds_read_b128 v[186:189], v169 offset:17408
	ds_read_b128 v[190:193], v169 offset:18432
	ds_read_b128 v[194:197], v169 offset:19456
	ds_read_b128 v[198:201], v169 offset:20480
	ds_read_b128 v[202:205], v169 offset:21504
	ds_read_b128 v[206:209], v169 offset:22528
	ds_read_b128 v[210:213], v169 offset:23552
	s_mov_b32 m0, s37
	s_nop 0
	global_load_lds_dwordx4 v158, s[40:41]
	s_add_u32 s76, s40, 0x40000
	s_mov_b32 m0, s56
	s_nop 0
	global_load_lds_dwordx4 v159, s[40:41]
	s_addc_u32 s77, s41, 0
	s_mov_b32 m0, s57
	s_nop 0
	global_load_lds_dwordx4 v158, s[76:77]
	s_mov_b32 m0, s58
	s_nop 0
	global_load_lds_dwordx4 v159, s[76:77]
	s_mov_b32 m0, s55
	s_nop 0
	global_load_lds_dwordx4 v160, s[46:47]
	s_mov_b32 m0, s59
	s_nop 0
	global_load_lds_dwordx4 v161, s[46:47]
	s_waitcnt vmcnt(8)
	s_waitcnt lgkmcnt(0)
	s_barrier
	s_setprio 1
	v_mfma_f32_16x16x32_bf16 v[78:81], v[130:133], v[182:185], v[78:81]
	v_mfma_f32_16x16x32_bf16 v[74:77], v[138:141], v[182:185], v[74:77]
	v_mfma_f32_16x16x32_bf16 v[46:49], v[130:133], v[190:193], v[46:49]
	v_mfma_f32_16x16x32_bf16 v[42:45], v[138:141], v[190:193], v[42:45]
	v_mfma_f32_16x16x32_bf16 v[30:33], v[130:133], v[198:201], v[30:33]
	v_mfma_f32_16x16x32_bf16 v[26:29], v[138:141], v[198:201], v[26:29]
	v_mfma_f32_16x16x32_bf16 v[14:17], v[130:133], v[206:209], v[14:17]
	v_mfma_f32_16x16x32_bf16 v[10:13], v[138:141], v[206:209], v[10:13]
	v_mfma_f32_16x16x32_bf16 v[78:81], v[134:137], v[186:189], v[78:81]
	v_mfma_f32_16x16x32_bf16 v[74:77], v[150:153], v[186:189], v[74:77]
	v_mfma_f32_16x16x32_bf16 v[46:49], v[134:137], v[194:197], v[46:49]
	v_mfma_f32_16x16x32_bf16 v[42:45], v[150:153], v[194:197], v[42:45]
	v_mfma_f32_16x16x32_bf16 v[30:33], v[134:137], v[202:205], v[30:33]
	v_mfma_f32_16x16x32_bf16 v[26:29], v[150:153], v[202:205], v[26:29]
	v_mfma_f32_16x16x32_bf16 v[14:17], v[134:137], v[210:213], v[14:17]
	v_mfma_f32_16x16x32_bf16 v[10:13], v[150:153], v[210:213], v[10:13]
	v_mfma_f32_16x16x32_bf16 v[62:65], v[154:157], v[182:185], v[62:65]
	v_mfma_f32_16x16x32_bf16 v[50:53], v[174:177], v[182:185], v[50:53]
	v_mfma_f32_16x16x32_bf16 v[38:41], v[154:157], v[190:193], v[38:41]
	v_mfma_f32_16x16x32_bf16 v[34:37], v[174:177], v[190:193], v[34:37]
	v_mfma_f32_16x16x32_bf16 v[22:25], v[154:157], v[198:201], v[22:25]
	v_mfma_f32_16x16x32_bf16 v[18:21], v[174:177], v[198:201], v[18:21]
	v_mfma_f32_16x16x32_bf16 v[6:9], v[154:157], v[206:209], v[6:9]
	v_mfma_f32_16x16x32_bf16 v[2:5], v[174:177], v[206:209], v[2:5]
	v_mfma_f32_16x16x32_bf16 v[62:65], v[170:173], v[186:189], v[62:65]
	v_mfma_f32_16x16x32_bf16 v[50:53], v[178:181], v[186:189], v[50:53]
	v_mfma_f32_16x16x32_bf16 v[38:41], v[170:173], v[194:197], v[38:41]
	v_mfma_f32_16x16x32_bf16 v[34:37], v[178:181], v[194:197], v[34:37]
	v_mfma_f32_16x16x32_bf16 v[22:25], v[170:173], v[202:205], v[22:25]
	v_mfma_f32_16x16x32_bf16 v[18:21], v[178:181], v[202:205], v[18:21]
	v_mfma_f32_16x16x32_bf16 v[6:9], v[170:173], v[210:213], v[6:9]
	v_mfma_f32_16x16x32_bf16 v[2:5], v[178:181], v[210:213], v[2:5]
	s_setprio 0
	s_barrier
	ds_read_b128 v[130:133], v142
	ds_read_b128 v[134:137], v142 offset:1024
	ds_read_b128 v[138:141], v142 offset:2048
	ds_read_b128 v[150:153], v142 offset:3072
	ds_read_b128 v[154:157], v143
	ds_read_b128 v[170:173], v143 offset:1024
	ds_read_b128 v[174:177], v143 offset:2048
	ds_read_b128 v[178:181], v143 offset:3072
	ds_read_b128 v[182:185], v169 offset:32768
	ds_read_b128 v[186:189], v169 offset:33792
	ds_read_b128 v[190:193], v169 offset:34816
	ds_read_b128 v[194:197], v169 offset:35840
	ds_read_b128 v[198:201], v169 offset:36864
	ds_read_b128 v[202:205], v169 offset:37888
	ds_read_b128 v[206:209], v169 offset:38912
	ds_read_b128 v[210:213], v169 offset:39936
	s_mov_b32 m0, s60
	s_nop 0
	global_load_lds_dwordx4 v162, s[46:47]
	s_mov_b32 m0, s61
	s_nop 0
	global_load_lds_dwordx4 v163, s[46:47]
	s_waitcnt vmcnt(8)
	s_waitcnt lgkmcnt(0)
	s_barrier
; #define PG8_STAGEB(bufoff, gbase) PG8_STAGE2(bufoff, gbase, voffB[0], voffB[1])
; #define PG8_STAGEAS(bufoff, gbase, h) PG8_STAGE2(bufoff, gbase, voffA[h][0], voffA[h][1])
; #define PG8_LDA(dst, b, h) do { _Pragma("unroll") for (int m = 0; m < 4; ++m) _Pragma("unroll") for (int k = 0; k < 2; ++k) dst[m][k] = *(const LAS bf16x8*)(lds + PG8_SA(b, h) + aoff + m * 2048 + k * 1024); } while (0)
; #define PG8_WAIT_K() do { if constexpr (HM) PG8_WAIT_V(6); else PG8_WAIT_V(8); } while (0)
; #define PG8_WAIT_L(n) asm volatile("s_waitcnt lgkmcnt(" #n ")" ::: "memory")
; #define PG8_BAR __builtin_amdgcn_s_barrier()
; #define PG8_SCHED __builtin_amdgcn_sched_barrier(0)
;     ...
;             PG8_WAIT_K(); PG8_WAIT_L(0); PG8_BAR; PG8_MMA(0, 0, At, B0); PG8_MMA(0, 1, At, B1); PG8_BAR; PG8_SCHED;
;             if constexpr (!HM) PG8_LDA(At, 1, 1);
;             PG8_STAGEB(PG8_SB(1, 0), b3); PG8_STAGEB(PG8_SB(1, 1), b3 + hstepB); PG8_STAGEAS(PG8_SA(1, 0), a3, 0);
;             PG8_WAIT_K(); PG8_WAIT_L(0); PG8_BAR; if constexpr (!HM) { PG8_MMA(1, 0, At, B0); PG8_MMA(1, 1, At, B1); } PG8_BAR; PG8_SCHED;
;         }
	s_setprio 1
	v_mfma_f32_16x16x32_bf16 v[114:117], v[130:133], v[182:185], v[114:117]
	v_mfma_f32_16x16x32_bf16 v[110:113], v[138:141], v[182:185], v[110:113]
	v_mfma_f32_16x16x32_bf16 v[106:109], v[130:133], v[190:193], v[106:109]
	v_mfma_f32_16x16x32_bf16 v[102:105], v[138:141], v[190:193], v[102:105]
	v_mfma_f32_16x16x32_bf16 v[94:97], v[130:133], v[198:201], v[94:97]
	v_mfma_f32_16x16x32_bf16 v[86:89], v[138:141], v[198:201], v[86:89]
	v_mfma_f32_16x16x32_bf16 v[70:73], v[130:133], v[206:209], v[70:73]
	v_mfma_f32_16x16x32_bf16 v[58:61], v[138:141], v[206:209], v[58:61]
	v_mfma_f32_16x16x32_bf16 v[114:117], v[134:137], v[186:189], v[114:117]
	v_mfma_f32_16x16x32_bf16 v[110:113], v[150:153], v[186:189], v[110:113]
	v_mfma_f32_16x16x32_bf16 v[106:109], v[134:137], v[194:197], v[106:109]
	v_mfma_f32_16x16x32_bf16 v[102:105], v[150:153], v[194:197], v[102:105]
	v_mfma_f32_16x16x32_bf16 v[94:97], v[134:137], v[202:205], v[94:97]
	v_mfma_f32_16x16x32_bf16 v[86:89], v[150:153], v[202:205], v[86:89]
	v_mfma_f32_16x16x32_bf16 v[70:73], v[134:137], v[210:213], v[70:73]
	v_mfma_f32_16x16x32_bf16 v[58:61], v[150:153], v[210:213], v[58:61]
	v_mfma_f32_16x16x32_bf16 v[126:129], v[154:157], v[182:185], v[126:129]
	v_mfma_f32_16x16x32_bf16 v[122:125], v[174:177], v[182:185], v[122:125]
	v_mfma_f32_16x16x32_bf16 v[118:121], v[154:157], v[190:193], v[118:121]
	v_mfma_f32_16x16x32_bf16 v[98:101], v[174:177], v[190:193], v[98:101]
	v_mfma_f32_16x16x32_bf16 v[90:93], v[154:157], v[198:201], v[90:93]
	v_mfma_f32_16x16x32_bf16 v[82:85], v[174:177], v[198:201], v[82:85]
	v_mfma_f32_16x16x32_bf16 v[66:69], v[154:157], v[206:209], v[66:69]
	v_mfma_f32_16x16x32_bf16 v[54:57], v[174:177], v[206:209], v[54:57]
	v_mfma_f32_16x16x32_bf16 v[126:129], v[170:173], v[186:189], v[126:129]
	v_mfma_f32_16x16x32_bf16 v[122:125], v[178:181], v[186:189], v[122:125]
	v_mfma_f32_16x16x32_bf16 v[118:121], v[170:173], v[194:197], v[118:121]
	v_mfma_f32_16x16x32_bf16 v[98:101], v[178:181], v[194:197], v[98:101]
	v_mfma_f32_16x16x32_bf16 v[90:93], v[170:173], v[202:205], v[90:93]
	v_mfma_f32_16x16x32_bf16 v[82:85], v[178:181], v[202:205], v[82:85]
	v_mfma_f32_16x16x32_bf16 v[66:69], v[170:173], v[210:213], v[66:69]
	v_mfma_f32_16x16x32_bf16 v[54:57], v[178:181], v[210:213], v[54:57]
	s_setprio 0
	s_barrier
	ds_read_b128 v[182:185], v169 offset:49152
	ds_read_b128 v[186:189], v169 offset:50176
	ds_read_b128 v[190:193], v169 offset:51200
	ds_read_b128 v[194:197], v169 offset:52224
	ds_read_b128 v[198:201], v169 offset:53248
	ds_read_b128 v[202:205], v169 offset:54272
	ds_read_b128 v[206:209], v169 offset:55296
	ds_read_b128 v[210:213], v169 offset:56320
	s_mov_b32 m0, s62
	s_nop 0
	global_load_lds_dwordx4 v158, s[44:45]
	s_add_u32 s40, s40, 0x40080
	s_mov_b32 m0, s63
	s_nop 0
	global_load_lds_dwordx4 v159, s[44:45]
	s_addc_u32 s41, s41, 0
	s_mov_b32 m0, s66
	s_nop 0
	global_load_lds_dwordx4 v158, s[40:41]
	s_mov_b32 m0, s67
	s_nop 0
	global_load_lds_dwordx4 v159, s[40:41]
	s_mov_b32 m0, s64
	s_nop 0
	global_load_lds_dwordx4 v160, s[38:39]
	s_mov_b32 m0, s65
	s_nop 0
	global_load_lds_dwordx4 v161, s[38:39]
	s_waitcnt vmcnt(8)
	s_waitcnt lgkmcnt(0)
	s_barrier
	s_setprio 1
	v_mfma_f32_16x16x32_bf16 v[78:81], v[130:133], v[182:185], v[78:81]
	v_mfma_f32_16x16x32_bf16 v[74:77], v[138:141], v[182:185], v[74:77]
	v_mfma_f32_16x16x32_bf16 v[46:49], v[130:133], v[190:193], v[46:49]
	v_mfma_f32_16x16x32_bf16 v[42:45], v[138:141], v[190:193], v[42:45]
	v_mfma_f32_16x16x32_bf16 v[30:33], v[130:133], v[198:201], v[30:33]
	v_mfma_f32_16x16x32_bf16 v[26:29], v[138:141], v[198:201], v[26:29]
	v_mfma_f32_16x16x32_bf16 v[14:17], v[130:133], v[206:209], v[14:17]
	v_mfma_f32_16x16x32_bf16 v[10:13], v[138:141], v[206:209], v[10:13]
	v_mfma_f32_16x16x32_bf16 v[78:81], v[134:137], v[186:189], v[78:81]
	v_mfma_f32_16x16x32_bf16 v[74:77], v[150:153], v[186:189], v[74:77]
	v_mfma_f32_16x16x32_bf16 v[46:49], v[134:137], v[194:197], v[46:49]
	v_mfma_f32_16x16x32_bf16 v[42:45], v[150:153], v[194:197], v[42:45]
	v_mfma_f32_16x16x32_bf16 v[30:33], v[134:137], v[202:205], v[30:33]
	v_mfma_f32_16x16x32_bf16 v[26:29], v[150:153], v[202:205], v[26:29]
	v_mfma_f32_16x16x32_bf16 v[14:17], v[134:137], v[210:213], v[14:17]
	v_mfma_f32_16x16x32_bf16 v[10:13], v[150:153], v[210:213], v[10:13]
	v_mfma_f32_16x16x32_bf16 v[62:65], v[154:157], v[182:185], v[62:65]
	v_mfma_f32_16x16x32_bf16 v[50:53], v[174:177], v[182:185], v[50:53]
	v_mfma_f32_16x16x32_bf16 v[38:41], v[154:157], v[190:193], v[38:41]
	v_mfma_f32_16x16x32_bf16 v[34:37], v[174:177], v[190:193], v[34:37]
	v_mfma_f32_16x16x32_bf16 v[22:25], v[154:157], v[198:201], v[22:25]
	v_mfma_f32_16x16x32_bf16 v[18:21], v[174:177], v[198:201], v[18:21]
	v_mfma_f32_16x16x32_bf16 v[6:9], v[154:157], v[206:209], v[6:9]
	v_mfma_f32_16x16x32_bf16 v[2:5], v[174:177], v[206:209], v[2:5]
	v_mfma_f32_16x16x32_bf16 v[62:65], v[170:173], v[186:189], v[62:65]
	v_mfma_f32_16x16x32_bf16 v[50:53], v[178:181], v[186:189], v[50:53]
	v_mfma_f32_16x16x32_bf16 v[38:41], v[170:173], v[194:197], v[38:41]
	v_mfma_f32_16x16x32_bf16 v[34:37], v[178:181], v[194:197], v[34:37]
	v_mfma_f32_16x16x32_bf16 v[22:25], v[170:173], v[202:205], v[22:25]
	v_mfma_f32_16x16x32_bf16 v[18:21], v[178:181], v[202:205], v[18:21]
	v_mfma_f32_16x16x32_bf16 v[6:9], v[170:173], v[210:213], v[6:9]
	v_mfma_f32_16x16x32_bf16 v[2:5], v[178:181], v[210:213], v[2:5]
	s_setprio 0
	s_barrier
	s_add_i32 s74, s74, 2
	s_add_u32 s29, s29, 0x100
	s_addc_u32 s31, s31, 0
	s_add_u32 s72, s72, 0x100
	s_addc_u32 s73, s73, 0
	s_add_u32 s42, s42, 0x100
	s_addc_u32 s43, s43, 0
	s_cmp_gt_u32 s74, 13
	s_cbranch_scc0 .LBB0_581
	s_and_b64 vcc, exec, s[18:19]
	s_cbranch_vccz .LBB0_584
	s_barrier

; #define PG8_STAGEB(bufoff, gbase) PG8_STAGE2(bufoff, gbase, voffB[0], voffB[1])
; #define PG8_STAGEAS(bufoff, gbase, h) PG8_STAGE2(bufoff, gbase, voffA[h][0], voffA[h][1])
; #define PG8_LDA(dst, b, h) do { _Pragma("unroll") for (int m = 0; m < 4; ++m) _Pragma("unroll") for (int k = 0; k < 2; ++k) dst[m][k] = *(const LAS bf16x8*)(lds + PG8_SA(b, h) + aoff + m * 2048 + k * 1024); } while (0)
; #define PG8_WAIT_K0() do { if (EST > 0 && t == 0 && ui > 0) asm volatile("s_waitcnt vmcnt(%0)" :: "n"((HM ? 6 : 8) + EST) : "memory"); else PG8_WAIT_K(); } while (0)
; #define PG8_WAIT_L(n) asm volatile("s_waitcnt lgkmcnt(" #n ")" ::: "memory")
; #define PG8_BAR __builtin_amdgcn_s_barrier()
; #define PG8_SCHED __builtin_amdgcn_sched_barrier(0)
;     ...
;             PG8_WAIT_K0(); PG8_WAIT_L(0); PG8_BAR; PG8_MMA(0, 0, At, B0); PG8_MMA(0, 1, At, B1); PG8_BAR; PG8_SCHED;
;             if constexpr (!HM) PG8_LDA(At, 0, 1);
;             PG8_STAGEB(PG8_SB(0, 0), b2); PG8_STAGEB(PG8_SB(0, 1), b2 + hstepB); PG8_STAGEAS(PG8_SA(0, 0), a2, 0);
.LBB0_607:
	s_add_u32 s30, s24, 0x100
	s_waitcnt lgkmcnt(0)
	s_addc_u32 s31, s25, 0
	s_add_u32 s34, s26, 0x100
	s_addc_u32 s35, s27, 0
	s_barrier
	s_setprio 1
	v_mfma_f32_16x16x32_bf16 v[34:37], v[18:21], v[70:73], 0
	v_mfma_f32_16x16x32_bf16 v[38:41], v[26:29], v[70:73], 0
	v_mfma_f32_16x16x32_bf16 v[42:45], v[18:21], v[86:89], 0
	v_mfma_f32_16x16x32_bf16 v[46:49], v[26:29], v[86:89], 0
	v_mfma_f32_16x16x32_bf16 v[50:53], v[18:21], v[90:93], 0
	v_mfma_f32_16x16x32_bf16 v[54:57], v[26:29], v[90:93], 0
	v_mfma_f32_16x16x32_bf16 v[58:61], v[18:21], v[74:77], 0
	v_mfma_f32_16x16x32_bf16 v[62:65], v[26:29], v[74:77], 0
	v_mfma_f32_16x16x32_bf16 v[118:121], v[22:25], v[82:85], v[34:37]
	v_mfma_f32_16x16x32_bf16 v[38:41], v[30:33], v[82:85], v[38:41]
	v_mfma_f32_16x16x32_bf16 v[42:45], v[22:25], v[98:101], v[42:45]
	v_mfma_f32_16x16x32_bf16 v[46:49], v[30:33], v[98:101], v[46:49]
	v_mfma_f32_16x16x32_bf16 v[50:53], v[22:25], v[94:97], v[50:53]
	v_mfma_f32_16x16x32_bf16 v[54:57], v[30:33], v[94:97], v[54:57]
	v_mfma_f32_16x16x32_bf16 v[58:61], v[22:25], v[78:81], v[58:61]
	v_mfma_f32_16x16x32_bf16 v[62:65], v[30:33], v[78:81], v[62:65]
	v_mfma_f32_16x16x32_bf16 v[66:69], v[2:5], v[70:73], 0
	v_mfma_f32_16x16x32_bf16 v[70:73], v[10:13], v[70:73], 0
	v_mfma_f32_16x16x32_bf16 v[66:69], v[6:9], v[82:85], v[66:69]
	v_mfma_f32_16x16x32_bf16 v[70:73], v[14:17], v[82:85], v[70:73]
	v_mfma_f32_16x16x32_bf16 v[82:85], v[2:5], v[86:89], 0
	v_mfma_f32_16x16x32_bf16 v[86:89], v[10:13], v[86:89], 0
	v_mfma_f32_16x16x32_bf16 v[82:85], v[6:9], v[98:101], v[82:85]
	v_mfma_f32_16x16x32_bf16 v[86:89], v[14:17], v[98:101], v[86:89]
	v_mfma_f32_16x16x32_bf16 v[98:101], v[2:5], v[90:93], 0
	v_mfma_f32_16x16x32_bf16 v[90:93], v[10:13], v[90:93], 0
	v_mfma_f32_16x16x32_bf16 v[134:137], v[14:17], v[94:97], v[90:93]
	v_mfma_f32_16x16x32_bf16 v[90:93], v[2:5], v[74:77], 0
	v_mfma_f32_16x16x32_bf16 v[74:77], v[10:13], v[74:77], 0
	v_mfma_f32_16x16x32_bf16 v[130:133], v[6:9], v[94:97], v[98:101]
	v_mfma_f32_16x16x32_bf16 v[138:141], v[6:9], v[78:81], v[90:93]
	v_mfma_f32_16x16x32_bf16 v[142:145], v[14:17], v[78:81], v[74:77]
	s_setprio 0
	s_barrier
	ds_read_b128 v[106:109], v182 offset:16384
	ds_read_b128 v[110:113], v182 offset:17408
	ds_read_b128 v[98:101], v182 offset:18432
	ds_read_b128 v[102:105], v182 offset:19456
	ds_read_b128 v[90:93], v182 offset:20480
	ds_read_b128 v[94:97], v182 offset:21504
	ds_read_b128 v[74:77], v182 offset:22528
	ds_read_b128 v[78:81], v182 offset:23552
	s_mov_b32 m0, s23
	s_nop 0
	global_load_lds_dwordx4 v1, s[34:35]
	s_mov_b32 m0, s41
	s_nop 0
	global_load_lds_dwordx4 v172, s[34:35]
	s_add_u32 s34, s26, 0x80100
	s_addc_u32 s35, s27, 0
	s_mov_b32 m0, s42
	s_nop 0
	global_load_lds_dwordx4 v1, s[34:35]
	s_and_b64 vcc, exec, s[28:29]
	s_mov_b32 m0, s43
	s_nop 0
	global_load_lds_dwordx4 v172, s[34:35]
	s_mov_b32 m0, s36
	s_nop 0
	global_load_lds_dwordx4 v173, s[30:31]
	s_mov_b32 m0, s44
	s_nop 0
	global_load_lds_dwordx4 v174, s[30:31]
	s_cbranch_vccz .LBB0_618
	s_waitcnt vmcnt(24)
	s_cbranch_execnz .LBB0_610

; #define PG8_STAGEAS(bufoff, gbase, h) PG8_STAGE2(bufoff, gbase, voffA[h][0], voffA[h][1])
; #define PG8_LDA(dst, b, h) do { _Pragma("unroll") for (int m = 0; m < 4; ++m) _Pragma("unroll") for (int k = 0; k < 2; ++k) dst[m][k] = *(const LAS bf16x8*)(lds + PG8_SA(b, h) + aoff + m * 2048 + k * 1024); } while (0)
; #define PG8_LDB(dst, b, h) do { _Pragma("unroll") for (int n = 0; n < 2; ++n) _Pragma("unroll") for (int k = 0; k < 2; ++k) dst[n][k] = *(const LAS bf16x8*)(lds + PG8_SB(b, h) + boff + n * 2048 + k * 1024); } while (0)
; #define PG8_WAIT_K() do { if constexpr (HM) PG8_WAIT_V(6); else PG8_WAIT_V(8); } while (0)
; #define PG8_WAIT_K0() do { if (EST > 0 && t == 0 && ui > 0) asm volatile("s_waitcnt vmcnt(%0)" :: "n"((HM ? 6 : 8) + EST) : "memory"); else PG8_WAIT_K(); } while (0)
; #define PG8_WAIT_L(n) asm volatile("s_waitcnt lgkmcnt(" #n ")" ::: "memory")
; #define PG8_BAR __builtin_amdgcn_s_barrier()
; #define PG8_SCHED __builtin_amdgcn_sched_barrier(0)
;     ...
;             PG8_WAIT_K0(); PG8_WAIT_L(0); PG8_BAR; if constexpr (!HM) { PG8_MMA(1, 0, At, B0); PG8_MMA(1, 1, At, B1); } PG8_BAR; PG8_SCHED;
;             PG8_LDB(B0, 1, 0); PG8_LDB(B1, 1, 1); PG8_SCHED; PG8_LDA(At, 1, 0); if constexpr (!HM) PG8_STAGEAS(PG8_SA(0, 1), a2, 1);
;             PG8_WAIT_K(); PG8_WAIT_L(0); PG8_BAR; PG8_MMA(0, 0, At, B0); PG8_MMA(0, 1, At, B1); PG8_BAR; PG8_SCHED;
.LBB0_610:
	s_add_u32 s28, s24, 0x180
	s_waitcnt lgkmcnt(0)
	s_addc_u32 s29, s25, 0
	s_add_u32 s34, s26, 0x180
	s_addc_u32 s35, s27, 0
	s_barrier
	s_setprio 1
	v_mfma_f32_16x16x32_bf16 v[114:117], v[18:21], v[106:109], 0
	v_mfma_f32_16x16x32_bf16 v[148:151], v[22:25], v[110:113], v[114:117]
	v_mfma_f32_16x16x32_bf16 v[114:117], v[26:29], v[106:109], 0
	v_mfma_f32_16x16x32_bf16 v[152:155], v[30:33], v[110:113], v[114:117]
	v_mfma_f32_16x16x32_bf16 v[114:117], v[18:21], v[98:101], 0
	v_mfma_f32_16x16x32_bf16 v[162:165], v[22:25], v[102:105], v[114:117]
	v_mfma_f32_16x16x32_bf16 v[114:117], v[26:29], v[98:101], 0
	v_mfma_f32_16x16x32_bf16 v[166:169], v[30:33], v[102:105], v[114:117]
	v_mfma_f32_16x16x32_bf16 v[114:117], v[18:21], v[90:93], 0
	v_mfma_f32_16x16x32_bf16 v[18:21], v[18:21], v[74:77], 0
	v_mfma_f32_16x16x32_bf16 v[184:187], v[22:25], v[94:97], v[114:117]
	v_mfma_f32_16x16x32_bf16 v[18:21], v[22:25], v[78:81], v[18:21]
	v_mfma_f32_16x16x32_bf16 v[22:25], v[26:29], v[74:77], 0
	v_mfma_f32_16x16x32_bf16 v[114:117], v[26:29], v[90:93], 0
	v_mfma_f32_16x16x32_bf16 v[22:25], v[30:33], v[78:81], v[22:25]
	v_mfma_f32_16x16x32_bf16 v[188:191], v[30:33], v[94:97], v[114:117]
	v_mfma_f32_16x16x32_bf16 v[26:29], v[2:5], v[106:109], 0
	v_mfma_f32_16x16x32_bf16 v[192:195], v[6:9], v[110:113], v[26:29]
	v_mfma_f32_16x16x32_bf16 v[26:29], v[10:13], v[106:109], 0
	v_mfma_f32_16x16x32_bf16 v[196:199], v[14:17], v[110:113], v[26:29]
	v_mfma_f32_16x16x32_bf16 v[26:29], v[2:5], v[98:101], 0
	v_mfma_f32_16x16x32_bf16 v[200:203], v[6:9], v[102:105], v[26:29]
	v_mfma_f32_16x16x32_bf16 v[26:29], v[10:13], v[98:101], 0
	v_mfma_f32_16x16x32_bf16 v[204:207], v[14:17], v[102:105], v[26:29]
	v_mfma_f32_16x16x32_bf16 v[26:29], v[2:5], v[90:93], 0
	v_mfma_f32_16x16x32_bf16 v[2:5], v[2:5], v[74:77], 0
	v_mfma_f32_16x16x32_bf16 v[208:211], v[6:9], v[94:97], v[26:29]
	v_mfma_f32_16x16x32_bf16 v[26:29], v[10:13], v[90:93], 0
	v_mfma_f32_16x16x32_bf16 v[2:5], v[6:9], v[78:81], v[2:5]
	v_mfma_f32_16x16x32_bf16 v[6:9], v[10:13], v[74:77], 0
	v_mfma_f32_16x16x32_bf16 v[212:215], v[14:17], v[94:97], v[26:29]
	v_mfma_f32_16x16x32_bf16 v[216:219], v[14:17], v[78:81], v[6:9]
	s_setprio 0
	s_barrier
	v_add_u32_e32 v146, 0x18000, v179
	v_add_u32_e32 v147, 0x1c000, v179
	s_nop 1
	ds_read_b128 v[6:9], v146
	ds_read_b128 v[10:13], v146 offset:1024
	ds_read_b128 v[220:223], v146 offset:2048
	ds_read_b128 v[224:227], v146 offset:3072
	ds_read_b128 v[228:231], v147
	ds_read_b128 v[232:235], v147 offset:1024
	ds_read_b128 v[236:239], v147 offset:2048
	ds_read_b128 v[240:243], v147 offset:3072
	ds_read_b128 v[14:17], v182 offset:32768
	ds_read_b128 v[26:29], v182 offset:33792
	ds_read_b128 v[30:33], v182 offset:34816
	ds_read_b128 v[98:101], v182 offset:35840
	ds_read_b128 v[244:247], v182 offset:36864
	ds_read_b128 v[248:251], v182 offset:37888
	ds_read_b128 v[156:159], v182 offset:38912
	ds_read_b128 v[34:37], v182 offset:39936
	s_mov_b32 m0, s45
	s_nop 0
	global_load_lds_dwordx4 v175, s[30:31]
	s_mov_b32 m0, s46
	s_nop 0
	global_load_lds_dwordx4 v176, s[30:31]
	s_waitcnt vmcnt(8)
	s_waitcnt lgkmcnt(0)
	s_barrier
	s_setprio 1
	v_mfma_f32_16x16x32_bf16 v[38:41], v[220:223], v[14:17], v[38:41]
	v_mfma_f32_16x16x32_bf16 v[122:125], v[224:227], v[26:29], v[38:41]
	v_mfma_f32_16x16x32_bf16 v[38:41], v[6:9], v[30:33], v[42:45]
	v_mfma_f32_16x16x32_bf16 v[110:113], v[10:13], v[98:101], v[38:41]
	v_mfma_f32_16x16x32_bf16 v[38:41], v[220:223], v[30:33], v[46:49]
	v_mfma_f32_16x16x32_bf16 v[106:109], v[224:227], v[98:101], v[38:41]
	v_mfma_f32_16x16x32_bf16 v[38:41], v[6:9], v[244:247], v[50:53]
	v_mfma_f32_16x16x32_bf16 v[94:97], v[10:13], v[248:251], v[38:41]
	v_mfma_f32_16x16x32_bf16 v[38:41], v[220:223], v[244:247], v[54:57]
	v_mfma_f32_16x16x32_bf16 v[90:93], v[224:227], v[248:251], v[38:41]
	v_mfma_f32_16x16x32_bf16 v[38:41], v[6:9], v[156:159], v[58:61]
	v_mfma_f32_16x16x32_bf16 v[74:77], v[6:9], v[14:17], v[118:121]
	v_mfma_f32_16x16x32_bf16 v[78:81], v[10:13], v[34:37], v[38:41]
	v_mfma_f32_16x16x32_bf16 v[38:41], v[220:223], v[156:159], v[62:65]
	v_mfma_f32_16x16x32_bf16 v[126:129], v[10:13], v[26:29], v[74:77]
	v_mfma_f32_16x16x32_bf16 v[74:77], v[224:227], v[34:37], v[38:41]
	v_mfma_f32_16x16x32_bf16 v[38:41], v[228:231], v[14:17], v[66:69]
	v_mfma_f32_16x16x32_bf16 v[14:17], v[236:239], v[14:17], v[70:73]
	v_mfma_f32_16x16x32_bf16 v[114:117], v[240:243], v[26:29], v[14:17]
	v_mfma_f32_16x16x32_bf16 v[14:17], v[228:231], v[30:33], v[82:85]
	v_mfma_f32_16x16x32_bf16 v[102:105], v[232:235], v[98:101], v[14:17]
	v_mfma_f32_16x16x32_bf16 v[14:17], v[236:239], v[30:33], v[86:89]
	v_mfma_f32_16x16x32_bf16 v[98:101], v[240:243], v[98:101], v[14:17]
	v_mfma_f32_16x16x32_bf16 v[14:17], v[228:231], v[244:247], v[130:133]
	v_mfma_f32_16x16x32_bf16 v[86:89], v[232:235], v[248:251], v[14:17]
	v_mfma_f32_16x16x32_bf16 v[14:17], v[236:239], v[244:247], v[134:137]
	v_mfma_f32_16x16x32_bf16 v[82:85], v[240:243], v[248:251], v[14:17]
	v_mfma_f32_16x16x32_bf16 v[14:17], v[228:231], v[156:159], v[138:141]
	v_mfma_f32_16x16x32_bf16 v[70:73], v[232:235], v[34:37], v[14:17]
	v_mfma_f32_16x16x32_bf16 v[14:17], v[236:239], v[156:159], v[142:145]
	v_mfma_f32_16x16x32_bf16 v[118:121], v[232:235], v[26:29], v[38:41]
	v_mfma_f32_16x16x32_bf16 v[66:69], v[240:243], v[34:37], v[14:17]
	s_setprio 0
	s_barrier
; #define LAS __attribute__((address_space(3)))
; #define PG8_STAGEB(bufoff, gbase) PG8_STAGE2(bufoff, gbase, voffB[0], voffB[1])
; #define PG8_STAGEA(bufoff, gbase, h) PG8_STAGE2(bufoff, gbase, voffA[h][0], voffA[h][1])
; #define PG8_STAGEAS(bufoff, gbase, h) PG8_STAGE2(bufoff, gbase, voffA[h][0], voffA[h][1])
; #define PG8_LDA(dst, b, h) do { _Pragma("unroll") for (int m = 0; m < 4; ++m) _Pragma("unroll") for (int k = 0; k < 2; ++k) dst[m][k] = *(const LAS bf16x8*)(lds + PG8_SA(b, h) + aoff + m * 2048 + k * 1024); } while (0)
; #define PG8_LDB(dst, b, h) do { _Pragma("unroll") for (int n = 0; n < 2; ++n) _Pragma("unroll") for (int k = 0; k < 2; ++k) dst[n][k] = *(const LAS bf16x8*)(lds + PG8_SB(b, h) + boff + n * 2048 + k * 1024); } while (0)
; #define PG8_WAIT_K() do { if constexpr (HM) PG8_WAIT_V(6); else PG8_WAIT_V(8); } while (0)
; #define PG8_WAIT_K0() do { if (EST > 0 && t == 0 && ui > 0) asm volatile("s_waitcnt vmcnt(%0)" :: "n"((HM ? 6 : 8) + EST) : "memory"); else PG8_WAIT_K(); } while (0)
; #define PG8_WAIT_L(n) asm volatile("s_waitcnt lgkmcnt(" #n ")" ::: "memory")
; #define PG8_BAR __builtin_amdgcn_s_barrier()
; #define PG8_SCHED __builtin_amdgcn_sched_barrier(0)
;     ...
;             PG8_LDB(B0, 0, 0); PG8_LDB(B1, 0, 1); PG8_SCHED; PG8_LDA(At, 0, 0); if constexpr (!HM) PG8_STAGEA(PG8_SA(1, 1), a1, 1);
;             if constexpr (Sched::kGather) { if (last && has_next) { const u32x4 tn = *(const LAS u32x4*)(S.aux + tid * 16); voffA[0][0] = tn.x; voffA[0][1] = tn.y; voffA[1][0] = tn.z; voffA[1][1] = tn.w; } }
;             PG8_WAIT_K0(); PG8_WAIT_L(0); PG8_BAR; PG8_MMA(0, 0, At, B0); PG8_MMA(0, 1, At, B1); PG8_BAR; PG8_SCHED;
;     ...
;             if constexpr (!HM) PG8_LDA(At, 1, 1);
;             PG8_STAGEB(PG8_SB(1, 0), b3); PG8_STAGEB(PG8_SB(1, 1), b3 + hstepB); PG8_STAGEAS(PG8_SA(1, 0), a3, 0);
;             PG8_WAIT_K(); PG8_WAIT_L(0); PG8_BAR; if constexpr (!HM) { PG8_MMA(1, 0, At, B0); PG8_MMA(1, 1, At, B1); } PG8_BAR; PG8_SCHED;
	ds_read_b128 v[34:37], v182 offset:49152
	ds_read_b128 v[38:41], v182 offset:50176
	ds_read_b128 v[130:133], v182 offset:51200
	ds_read_b128 v[134:137], v182 offset:52224
	ds_read_b128 v[138:141], v182 offset:53248
	ds_read_b128 v[142:145], v182 offset:54272
	ds_read_b128 v[156:159], v182 offset:55296
	ds_read_b128 v[244:247], v182 offset:56320
	s_mov_b32 m0, s47
	s_nop 0
	global_load_lds_dwordx4 v1, s[34:35]
	s_add_u32 s30, s26, 0x80180
	s_mov_b32 m0, s48
	s_nop 0
	global_load_lds_dwordx4 v172, s[34:35]
	s_addc_u32 s31, s27, 0
	s_mov_b32 m0, s51
	s_nop 0
	global_load_lds_dwordx4 v1, s[30:31]
	s_mov_b32 m0, s52
	s_nop 0
	global_load_lds_dwordx4 v172, s[30:31]
	s_mov_b32 m0, s49
	s_nop 0
	global_load_lds_dwordx4 v173, s[28:29]
	s_mov_b32 m0, s50
	s_nop 0
	global_load_lds_dwordx4 v174, s[28:29]
	s_waitcnt vmcnt(8)
	s_waitcnt lgkmcnt(0)
	s_barrier
	s_setprio 1
	v_mfma_f32_16x16x32_bf16 v[14:17], v[6:9], v[34:37], v[148:151]
	v_mfma_f32_16x16x32_bf16 v[62:65], v[10:13], v[38:41], v[14:17]
	v_mfma_f32_16x16x32_bf16 v[14:17], v[220:223], v[34:37], v[152:155]
	v_mfma_f32_16x16x32_bf16 v[58:61], v[224:227], v[38:41], v[14:17]
	v_mfma_f32_16x16x32_bf16 v[14:17], v[6:9], v[130:133], v[162:165]
	v_mfma_f32_16x16x32_bf16 v[46:49], v[10:13], v[134:137], v[14:17]
	v_mfma_f32_16x16x32_bf16 v[14:17], v[220:223], v[130:133], v[166:169]
	v_mfma_f32_16x16x32_bf16 v[42:45], v[224:227], v[134:137], v[14:17]
	v_mfma_f32_16x16x32_bf16 v[14:17], v[6:9], v[138:141], v[184:187]
	v_mfma_f32_16x16x32_bf16 v[30:33], v[10:13], v[142:145], v[14:17]
	v_mfma_f32_16x16x32_bf16 v[14:17], v[220:223], v[138:141], v[188:191]
	v_mfma_f32_16x16x32_bf16 v[6:9], v[6:9], v[156:159], v[18:21]
	v_mfma_f32_16x16x32_bf16 v[26:29], v[224:227], v[142:145], v[14:17]
	v_mfma_f32_16x16x32_bf16 v[14:17], v[10:13], v[244:247], v[6:9]
	v_mfma_f32_16x16x32_bf16 v[6:9], v[220:223], v[156:159], v[22:25]
	v_mfma_f32_16x16x32_bf16 v[10:13], v[224:227], v[244:247], v[6:9]
	v_mfma_f32_16x16x32_bf16 v[6:9], v[228:231], v[34:37], v[192:195]
	v_mfma_f32_16x16x32_bf16 v[54:57], v[232:235], v[38:41], v[6:9]
	v_mfma_f32_16x16x32_bf16 v[6:9], v[236:239], v[34:37], v[196:199]
	v_mfma_f32_16x16x32_bf16 v[50:53], v[240:243], v[38:41], v[6:9]
	v_mfma_f32_16x16x32_bf16 v[6:9], v[228:231], v[130:133], v[200:203]
	v_mfma_f32_16x16x32_bf16 v[38:41], v[232:235], v[134:137], v[6:9]
	v_mfma_f32_16x16x32_bf16 v[6:9], v[236:239], v[130:133], v[204:207]
	v_mfma_f32_16x16x32_bf16 v[34:37], v[240:243], v[134:137], v[6:9]
	v_mfma_f32_16x16x32_bf16 v[6:9], v[228:231], v[138:141], v[208:211]
	v_mfma_f32_16x16x32_bf16 v[22:25], v[232:235], v[142:145], v[6:9]
	v_mfma_f32_16x16x32_bf16 v[6:9], v[236:239], v[138:141], v[212:215]
	v_mfma_f32_16x16x32_bf16 v[2:5], v[228:231], v[156:159], v[2:5]
	v_mfma_f32_16x16x32_bf16 v[18:21], v[240:243], v[142:145], v[6:9]
	v_mfma_f32_16x16x32_bf16 v[6:9], v[232:235], v[244:247], v[2:5]
	v_mfma_f32_16x16x32_bf16 v[2:5], v[236:239], v[156:159], v[216:219]
	v_mfma_f32_16x16x32_bf16 v[2:5], v[240:243], v[244:247], v[2:5]
	s_setprio 0
	s_barrier
	s_add_u32 s17, s24, 0x200
	s_addc_u32 s19, s25, 0
	s_add_u32 s57, s26, 0x200
	s_addc_u32 s58, s27, 0
	s_mov_b32 s59, 0
.LBB0_611:
	ds_read_b128 v[130:133], v180
	ds_read_b128 v[134:137], v180 offset:1024
	ds_read_b128 v[138:141], v180 offset:2048
	ds_read_b128 v[142:145], v180 offset:3072
	ds_read_b128 v[148:151], v181
	ds_read_b128 v[152:155], v181 offset:1024
	ds_read_b128 v[156:159], v181 offset:2048
	ds_read_b128 v[162:165], v181 offset:3072
	s_cmp_eq_u32 s59, 28
	s_cselect_b32 s34, s0, s17
	s_cselect_b32 s35, s1, s19
	s_cselect_b32 s26, s20, s57
	s_cselect_b32 s27, s21, s58
	s_add_u32 s24, s34, 0x80
	s_addc_u32 s25, s35, 0
	ds_read_b128 v[166:169], v182
	ds_read_b128 v[184:187], v182 offset:1024
	ds_read_b128 v[188:191], v182 offset:2048
	ds_read_b128 v[192:195], v182 offset:3072
	ds_read_b128 v[196:199], v182 offset:4096
	ds_read_b128 v[200:203], v182 offset:5120
	ds_read_b128 v[204:207], v182 offset:6144
	ds_read_b128 v[208:211], v182 offset:7168
	s_mov_b32 m0, s53
	s_nop 0
	global_load_lds_dwordx4 v175, s[28:29]
	s_add_u32 s30, s26, 0x80
	s_mov_b32 m0, s54
	s_nop 0
	global_load_lds_dwordx4 v176, s[28:29]
	s_waitcnt vmcnt(8)
	s_waitcnt lgkmcnt(0)
	s_addc_u32 s31, s27, 0
	s_barrier
	s_setprio 1
	v_mfma_f32_16x16x32_bf16 v[126:129], v[130:133], v[166:169], v[126:129]
	v_mfma_f32_16x16x32_bf16 v[122:125], v[138:141], v[166:169], v[122:125]
	v_mfma_f32_16x16x32_bf16 v[110:113], v[130:133], v[188:191], v[110:113]
	v_mfma_f32_16x16x32_bf16 v[106:109], v[138:141], v[188:191], v[106:109]
	v_mfma_f32_16x16x32_bf16 v[94:97], v[130:133], v[196:199], v[94:97]
	v_mfma_f32_16x16x32_bf16 v[90:93], v[138:141], v[196:199], v[90:93]
	v_mfma_f32_16x16x32_bf16 v[78:81], v[130:133], v[204:207], v[78:81]
	v_mfma_f32_16x16x32_bf16 v[74:77], v[138:141], v[204:207], v[74:77]
	v_mfma_f32_16x16x32_bf16 v[126:129], v[134:137], v[184:187], v[126:129]
	v_mfma_f32_16x16x32_bf16 v[122:125], v[142:145], v[184:187], v[122:125]
	v_mfma_f32_16x16x32_bf16 v[110:113], v[134:137], v[192:195], v[110:113]
	v_mfma_f32_16x16x32_bf16 v[106:109], v[142:145], v[192:195], v[106:109]
	v_mfma_f32_16x16x32_bf16 v[94:97], v[134:137], v[200:203], v[94:97]
	v_mfma_f32_16x16x32_bf16 v[90:93], v[142:145], v[200:203], v[90:93]
	v_mfma_f32_16x16x32_bf16 v[78:81], v[134:137], v[208:211], v[78:81]
	v_mfma_f32_16x16x32_bf16 v[74:77], v[142:145], v[208:211], v[74:77]
	v_mfma_f32_16x16x32_bf16 v[118:121], v[148:151], v[166:169], v[118:121]
	v_mfma_f32_16x16x32_bf16 v[114:117], v[156:159], v[166:169], v[114:117]
	v_mfma_f32_16x16x32_bf16 v[102:105], v[148:151], v[188:191], v[102:105]
	v_mfma_f32_16x16x32_bf16 v[98:101], v[156:159], v[188:191], v[98:101]
	v_mfma_f32_16x16x32_bf16 v[86:89], v[148:151], v[196:199], v[86:89]
	v_mfma_f32_16x16x32_bf16 v[82:85], v[156:159], v[196:199], v[82:85]
	v_mfma_f32_16x16x32_bf16 v[70:73], v[148:151], v[204:207], v[70:73]
	v_mfma_f32_16x16x32_bf16 v[66:69], v[156:159], v[204:207], v[66:69]
	v_mfma_f32_16x16x32_bf16 v[118:121], v[152:155], v[184:187], v[118:121]
	v_mfma_f32_16x16x32_bf16 v[114:117], v[162:165], v[184:187], v[114:117]
	v_mfma_f32_16x16x32_bf16 v[102:105], v[152:155], v[192:195], v[102:105]
	v_mfma_f32_16x16x32_bf16 v[98:101], v[162:165], v[192:195], v[98:101]
	v_mfma_f32_16x16x32_bf16 v[86:89], v[152:155], v[200:203], v[86:89]
	v_mfma_f32_16x16x32_bf16 v[82:85], v[162:165], v[200:203], v[82:85]
	v_mfma_f32_16x16x32_bf16 v[70:73], v[152:155], v[208:211], v[70:73]
	v_mfma_f32_16x16x32_bf16 v[66:69], v[162:165], v[208:211], v[66:69]
	s_setprio 0
	s_barrier
; #define LAS __attribute__((address_space(3)))
; #define PG8_STAGEB(bufoff, gbase) PG8_STAGE2(bufoff, gbase, voffB[0], voffB[1])
; #define PG8_STAGEA(bufoff, gbase, h) PG8_STAGE2(bufoff, gbase, voffA[h][0], voffA[h][1])
; #define PG8_STAGEAS(bufoff, gbase, h) PG8_STAGE2(bufoff, gbase, voffA[h][0], voffA[h][1])
; #define PG8_LDA(dst, b, h) do { _Pragma("unroll") for (int m = 0; m < 4; ++m) _Pragma("unroll") for (int k = 0; k < 2; ++k) dst[m][k] = *(const LAS bf16x8*)(lds + PG8_SA(b, h) + aoff + m * 2048 + k * 1024); } while (0)
; #define PG8_LDB(dst, b, h) do { _Pragma("unroll") for (int n = 0; n < 2; ++n) _Pragma("unroll") for (int k = 0; k < 2; ++k) dst[n][k] = *(const LAS bf16x8*)(lds + PG8_SB(b, h) + boff + n * 2048 + k * 1024); } while (0)
; #define PG8_WAIT_K() do { if constexpr (HM) PG8_WAIT_V(6); else PG8_WAIT_V(8); } while (0)
; #define PG8_WAIT_K0() do { if (EST > 0 && t == 0 && ui > 0) asm volatile("s_waitcnt vmcnt(%0)" :: "n"((HM ? 6 : 8) + EST) : "memory"); else PG8_WAIT_K(); } while (0)
; #define PG8_WAIT_L(n) asm volatile("s_waitcnt lgkmcnt(" #n ")" ::: "memory")
;     ...
;             const char* a1 = cA + (size_t)(t + 1) * kstep;
;             const char* a2 = last ? nA : cA + (size_t)(t + 2) * kstep; const char* b2 = last ? nB : cB + (size_t)(t + 2) * kstep;
;             const char* a3 = a2 + kstep; const char* b3 = b2 + kstep;
;             PG8_LDB(B0, 0, 0); PG8_LDB(B1, 0, 1); PG8_SCHED; PG8_LDA(At, 0, 0); if constexpr (!HM) PG8_STAGEA(PG8_SA(1, 1), a1, 1);
;             if constexpr (Sched::kGather) { if (last && has_next) { const u32x4 tn = *(const LAS u32x4*)(S.aux + tid * 16); voffA[0][0] = tn.x; voffA[0][1] = tn.y; voffA[1][0] = tn.z; voffA[1][1] = tn.w; } }
;             PG8_WAIT_K0(); PG8_WAIT_L(0); PG8_BAR; PG8_MMA(0, 0, At, B0); PG8_MMA(0, 1, At, B1); PG8_BAR; PG8_SCHED;
;             if constexpr (!HM) PG8_LDA(At, 0, 1);
;             PG8_STAGEB(PG8_SB(0, 0), b2); PG8_STAGEB(PG8_SB(0, 1), b2 + hstepB); PG8_STAGEAS(PG8_SA(0, 0), a2, 0);
;             PG8_WAIT_K0(); PG8_WAIT_L(0); PG8_BAR; if constexpr (!HM) { PG8_MMA(1, 0, At, B0); PG8_MMA(1, 1, At, B1); } PG8_BAR; PG8_SCHED;
;             PG8_LDB(B0, 1, 0); PG8_LDB(B1, 1, 1); PG8_SCHED; PG8_LDA(At, 1, 0); if constexpr (!HM) PG8_STAGEAS(PG8_SA(0, 1), a2, 1);
;             PG8_WAIT_K(); PG8_WAIT_L(0); PG8_BAR; PG8_MMA(0, 0, At, B0); PG8_MMA(0, 1, At, B1); PG8_BAR; PG8_SCHED;
	ds_read_b128 v[166:169], v182 offset:16384
	ds_read_b128 v[184:187], v182 offset:17408
	ds_read_b128 v[188:191], v182 offset:18432
	ds_read_b128 v[192:195], v182 offset:19456
	ds_read_b128 v[196:199], v182 offset:20480
	ds_read_b128 v[200:203], v182 offset:21504
	ds_read_b128 v[204:207], v182 offset:22528
	ds_read_b128 v[208:211], v182 offset:23552
	s_mov_b32 m0, s23
	s_nop 0
	global_load_lds_dwordx4 v1, s[26:27]
	s_mov_b32 m0, s41
	s_nop 0
	global_load_lds_dwordx4 v172, s[26:27]
	s_add_u32 s60, s26, 0x80000
	s_addc_u32 s61, s27, 0
	s_mov_b32 m0, s42
	s_nop 0
	global_load_lds_dwordx4 v1, s[60:61]
	s_mov_b32 m0, s43
	s_nop 0
	global_load_lds_dwordx4 v172, s[60:61]
	s_mov_b32 m0, s36
	s_nop 0
	global_load_lds_dwordx4 v173, s[34:35]
	s_mov_b32 m0, s44
	s_nop 0
	global_load_lds_dwordx4 v174, s[34:35]
	s_waitcnt vmcnt(8)
	s_waitcnt lgkmcnt(0)
	s_barrier
	s_setprio 1
	v_mfma_f32_16x16x32_bf16 v[62:65], v[130:133], v[166:169], v[62:65]
	v_mfma_f32_16x16x32_bf16 v[58:61], v[138:141], v[166:169], v[58:61]
	v_mfma_f32_16x16x32_bf16 v[46:49], v[130:133], v[188:191], v[46:49]
	v_mfma_f32_16x16x32_bf16 v[42:45], v[138:141], v[188:191], v[42:45]
	v_mfma_f32_16x16x32_bf16 v[30:33], v[130:133], v[196:199], v[30:33]
	v_mfma_f32_16x16x32_bf16 v[26:29], v[138:141], v[196:199], v[26:29]
	v_mfma_f32_16x16x32_bf16 v[14:17], v[130:133], v[204:207], v[14:17]
	v_mfma_f32_16x16x32_bf16 v[10:13], v[138:141], v[204:207], v[10:13]
	v_mfma_f32_16x16x32_bf16 v[62:65], v[134:137], v[184:187], v[62:65]
	v_mfma_f32_16x16x32_bf16 v[58:61], v[142:145], v[184:187], v[58:61]
	v_mfma_f32_16x16x32_bf16 v[46:49], v[134:137], v[192:195], v[46:49]
	v_mfma_f32_16x16x32_bf16 v[42:45], v[142:145], v[192:195], v[42:45]
	v_mfma_f32_16x16x32_bf16 v[30:33], v[134:137], v[200:203], v[30:33]
	v_mfma_f32_16x16x32_bf16 v[26:29], v[142:145], v[200:203], v[26:29]
	v_mfma_f32_16x16x32_bf16 v[14:17], v[134:137], v[208:211], v[14:17]
	v_mfma_f32_16x16x32_bf16 v[10:13], v[142:145], v[208:211], v[10:13]
	v_mfma_f32_16x16x32_bf16 v[54:57], v[148:151], v[166:169], v[54:57]
	v_mfma_f32_16x16x32_bf16 v[50:53], v[156:159], v[166:169], v[50:53]
	v_mfma_f32_16x16x32_bf16 v[38:41], v[148:151], v[188:191], v[38:41]
	v_mfma_f32_16x16x32_bf16 v[34:37], v[156:159], v[188:191], v[34:37]
	v_mfma_f32_16x16x32_bf16 v[22:25], v[148:151], v[196:199], v[22:25]
	v_mfma_f32_16x16x32_bf16 v[18:21], v[156:159], v[196:199], v[18:21]
	v_mfma_f32_16x16x32_bf16 v[6:9], v[148:151], v[204:207], v[6:9]
	v_mfma_f32_16x16x32_bf16 v[2:5], v[156:159], v[204:207], v[2:5]
	v_mfma_f32_16x16x32_bf16 v[54:57], v[152:155], v[184:187], v[54:57]
	v_mfma_f32_16x16x32_bf16 v[50:53], v[162:165], v[184:187], v[50:53]
	v_mfma_f32_16x16x32_bf16 v[38:41], v[152:155], v[192:195], v[38:41]
	v_mfma_f32_16x16x32_bf16 v[34:37], v[162:165], v[192:195], v[34:37]
	v_mfma_f32_16x16x32_bf16 v[22:25], v[152:155], v[200:203], v[22:25]
	v_mfma_f32_16x16x32_bf16 v[18:21], v[162:165], v[200:203], v[18:21]
	v_mfma_f32_16x16x32_bf16 v[6:9], v[152:155], v[208:211], v[6:9]
	v_mfma_f32_16x16x32_bf16 v[2:5], v[162:165], v[208:211], v[2:5]
	s_setprio 0
	s_barrier
	ds_read_b128 v[130:133], v146
	ds_read_b128 v[134:137], v146 offset:1024
	ds_read_b128 v[138:141], v146 offset:2048
	ds_read_b128 v[142:145], v146 offset:3072
	ds_read_b128 v[148:151], v147
	ds_read_b128 v[152:155], v147 offset:1024
	ds_read_b128 v[156:159], v147 offset:2048
	ds_read_b128 v[162:165], v147 offset:3072
	ds_read_b128 v[166:169], v182 offset:32768
	ds_read_b128 v[184:187], v182 offset:33792
	ds_read_b128 v[188:191], v182 offset:34816
	ds_read_b128 v[192:195], v182 offset:35840
	ds_read_b128 v[196:199], v182 offset:36864
	ds_read_b128 v[200:203], v182 offset:37888
	ds_read_b128 v[204:207], v182 offset:38912
	ds_read_b128 v[208:211], v182 offset:39936
	s_mov_b32 m0, s45
	s_nop 0
	global_load_lds_dwordx4 v175, s[34:35]
	s_mov_b32 m0, s46
	s_nop 0
	global_load_lds_dwordx4 v176, s[34:35]
	s_waitcnt vmcnt(8)
	s_waitcnt lgkmcnt(0)
	s_barrier
; #define PG8_STAGEB(bufoff, gbase) PG8_STAGE2(bufoff, gbase, voffB[0], voffB[1])
; #define PG8_STAGEAS(bufoff, gbase, h) PG8_STAGE2(bufoff, gbase, voffA[h][0], voffA[h][1])
; #define PG8_LDA(dst, b, h) do { _Pragma("unroll") for (int m = 0; m < 4; ++m) _Pragma("unroll") for (int k = 0; k < 2; ++k) dst[m][k] = *(const LAS bf16x8*)(lds + PG8_SA(b, h) + aoff + m * 2048 + k * 1024); } while (0)
; #define PG8_WAIT_K() do { if constexpr (HM) PG8_WAIT_V(6); else PG8_WAIT_V(8); } while (0)
; #define PG8_WAIT_L(n) asm volatile("s_waitcnt lgkmcnt(" #n ")" ::: "memory")
; #define PG8_BAR __builtin_amdgcn_s_barrier()
; #define PG8_SCHED __builtin_amdgcn_sched_barrier(0)
;     ...
;             PG8_WAIT_K(); PG8_WAIT_L(0); PG8_BAR; PG8_MMA(0, 0, At, B0); PG8_MMA(0, 1, At, B1); PG8_BAR; PG8_SCHED;
;             if constexpr (!HM) PG8_LDA(At, 1, 1);
;             PG8_STAGEB(PG8_SB(1, 0), b3); PG8_STAGEB(PG8_SB(1, 1), b3 + hstepB); PG8_STAGEAS(PG8_SA(1, 0), a3, 0);
;             PG8_WAIT_K(); PG8_WAIT_L(0); PG8_BAR; if constexpr (!HM) { PG8_MMA(1, 0, At, B0); PG8_MMA(1, 1, At, B1); } PG8_BAR; PG8_SCHED;
;         }
;         if (wr == 0) PG8_BAR;
	s_setprio 1
	v_mfma_f32_16x16x32_bf16 v[126:129], v[130:133], v[166:169], v[126:129]
	v_mfma_f32_16x16x32_bf16 v[122:125], v[138:141], v[166:169], v[122:125]
	v_mfma_f32_16x16x32_bf16 v[110:113], v[130:133], v[188:191], v[110:113]
	v_mfma_f32_16x16x32_bf16 v[106:109], v[138:141], v[188:191], v[106:109]
	v_mfma_f32_16x16x32_bf16 v[94:97], v[130:133], v[196:199], v[94:97]
	v_mfma_f32_16x16x32_bf16 v[90:93], v[138:141], v[196:199], v[90:93]
	v_mfma_f32_16x16x32_bf16 v[78:81], v[130:133], v[204:207], v[78:81]
	v_mfma_f32_16x16x32_bf16 v[74:77], v[138:141], v[204:207], v[74:77]
	v_mfma_f32_16x16x32_bf16 v[126:129], v[134:137], v[184:187], v[126:129]
	v_mfma_f32_16x16x32_bf16 v[122:125], v[142:145], v[184:187], v[122:125]
	v_mfma_f32_16x16x32_bf16 v[110:113], v[134:137], v[192:195], v[110:113]
	v_mfma_f32_16x16x32_bf16 v[106:109], v[142:145], v[192:195], v[106:109]
	v_mfma_f32_16x16x32_bf16 v[94:97], v[134:137], v[200:203], v[94:97]
	v_mfma_f32_16x16x32_bf16 v[90:93], v[142:145], v[200:203], v[90:93]
	v_mfma_f32_16x16x32_bf16 v[78:81], v[134:137], v[208:211], v[78:81]
	v_mfma_f32_16x16x32_bf16 v[74:77], v[142:145], v[208:211], v[74:77]
	v_mfma_f32_16x16x32_bf16 v[118:121], v[148:151], v[166:169], v[118:121]
	v_mfma_f32_16x16x32_bf16 v[114:117], v[156:159], v[166:169], v[114:117]
	v_mfma_f32_16x16x32_bf16 v[102:105], v[148:151], v[188:191], v[102:105]
	v_mfma_f32_16x16x32_bf16 v[98:101], v[156:159], v[188:191], v[98:101]
	v_mfma_f32_16x16x32_bf16 v[86:89], v[148:151], v[196:199], v[86:89]
	v_mfma_f32_16x16x32_bf16 v[82:85], v[156:159], v[196:199], v[82:85]
	v_mfma_f32_16x16x32_bf16 v[70:73], v[148:151], v[204:207], v[70:73]
	v_mfma_f32_16x16x32_bf16 v[66:69], v[156:159], v[204:207], v[66:69]
	v_mfma_f32_16x16x32_bf16 v[118:121], v[152:155], v[184:187], v[118:121]
	v_mfma_f32_16x16x32_bf16 v[114:117], v[162:165], v[184:187], v[114:117]
	v_mfma_f32_16x16x32_bf16 v[102:105], v[152:155], v[192:195], v[102:105]
	v_mfma_f32_16x16x32_bf16 v[98:101], v[162:165], v[192:195], v[98:101]
	v_mfma_f32_16x16x32_bf16 v[86:89], v[152:155], v[200:203], v[86:89]
	v_mfma_f32_16x16x32_bf16 v[82:85], v[162:165], v[200:203], v[82:85]
	v_mfma_f32_16x16x32_bf16 v[70:73], v[152:155], v[208:211], v[70:73]
	v_mfma_f32_16x16x32_bf16 v[66:69], v[162:165], v[208:211], v[66:69]
	s_setprio 0
	s_barrier
	ds_read_b128 v[166:169], v182 offset:49152
	ds_read_b128 v[184:187], v182 offset:50176
	ds_read_b128 v[188:191], v182 offset:51200
	ds_read_b128 v[192:195], v182 offset:52224
	ds_read_b128 v[196:199], v182 offset:53248
	ds_read_b128 v[200:203], v182 offset:54272
	ds_read_b128 v[204:207], v182 offset:55296
	ds_read_b128 v[208:211], v182 offset:56320
	s_mov_b32 m0, s47
	s_nop 0
	global_load_lds_dwordx4 v1, s[30:31]
	s_add_u32 s26, s26, 0x80080
	s_mov_b32 m0, s48
	s_nop 0
	global_load_lds_dwordx4 v172, s[30:31]
	s_addc_u32 s27, s27, 0
	s_mov_b32 m0, s51
	s_nop 0
	global_load_lds_dwordx4 v1, s[26:27]
	s_mov_b32 m0, s52
	s_nop 0
	global_load_lds_dwordx4 v172, s[26:27]
	s_mov_b32 m0, s49
	s_nop 0
	global_load_lds_dwordx4 v173, s[24:25]
	s_mov_b32 m0, s50
	s_nop 0
	global_load_lds_dwordx4 v174, s[24:25]
	s_waitcnt vmcnt(8)
	s_waitcnt lgkmcnt(0)
	s_barrier
	s_setprio 1
	v_mfma_f32_16x16x32_bf16 v[62:65], v[130:133], v[166:169], v[62:65]
	v_mfma_f32_16x16x32_bf16 v[58:61], v[138:141], v[166:169], v[58:61]
	v_mfma_f32_16x16x32_bf16 v[46:49], v[130:133], v[188:191], v[46:49]
	v_mfma_f32_16x16x32_bf16 v[42:45], v[138:141], v[188:191], v[42:45]
	v_mfma_f32_16x16x32_bf16 v[30:33], v[130:133], v[196:199], v[30:33]
	v_mfma_f32_16x16x32_bf16 v[26:29], v[138:141], v[196:199], v[26:29]
	v_mfma_f32_16x16x32_bf16 v[14:17], v[130:133], v[204:207], v[14:17]
	v_mfma_f32_16x16x32_bf16 v[10:13], v[138:141], v[204:207], v[10:13]
	v_mfma_f32_16x16x32_bf16 v[62:65], v[134:137], v[184:187], v[62:65]
	v_mfma_f32_16x16x32_bf16 v[58:61], v[142:145], v[184:187], v[58:61]
	v_mfma_f32_16x16x32_bf16 v[46:49], v[134:137], v[192:195], v[46:49]
	v_mfma_f32_16x16x32_bf16 v[42:45], v[142:145], v[192:195], v[42:45]
	v_mfma_f32_16x16x32_bf16 v[30:33], v[134:137], v[200:203], v[30:33]
	v_mfma_f32_16x16x32_bf16 v[26:29], v[142:145], v[200:203], v[26:29]
	v_mfma_f32_16x16x32_bf16 v[14:17], v[134:137], v[208:211], v[14:17]
	v_mfma_f32_16x16x32_bf16 v[10:13], v[142:145], v[208:211], v[10:13]
	v_mfma_f32_16x16x32_bf16 v[54:57], v[148:151], v[166:169], v[54:57]
	v_mfma_f32_16x16x32_bf16 v[50:53], v[156:159], v[166:169], v[50:53]
	v_mfma_f32_16x16x32_bf16 v[38:41], v[148:151], v[188:191], v[38:41]
	v_mfma_f32_16x16x32_bf16 v[34:37], v[156:159], v[188:191], v[34:37]
	v_mfma_f32_16x16x32_bf16 v[22:25], v[148:151], v[196:199], v[22:25]
	v_mfma_f32_16x16x32_bf16 v[18:21], v[156:159], v[196:199], v[18:21]
	v_mfma_f32_16x16x32_bf16 v[6:9], v[148:151], v[204:207], v[6:9]
	v_mfma_f32_16x16x32_bf16 v[2:5], v[156:159], v[204:207], v[2:5]
	v_mfma_f32_16x16x32_bf16 v[54:57], v[152:155], v[184:187], v[54:57]
	v_mfma_f32_16x16x32_bf16 v[50:53], v[162:165], v[184:187], v[50:53]
	v_mfma_f32_16x16x32_bf16 v[38:41], v[152:155], v[192:195], v[38:41]
	v_mfma_f32_16x16x32_bf16 v[34:37], v[162:165], v[192:195], v[34:37]
	v_mfma_f32_16x16x32_bf16 v[22:25], v[152:155], v[200:203], v[22:25]
	v_mfma_f32_16x16x32_bf16 v[18:21], v[162:165], v[200:203], v[18:21]
	v_mfma_f32_16x16x32_bf16 v[6:9], v[152:155], v[208:211], v[6:9]
	v_mfma_f32_16x16x32_bf16 v[2:5], v[162:165], v[208:211], v[2:5]
	s_setprio 0
	s_barrier
	s_add_i32 s59, s59, 2
	s_add_u32 s17, s17, 0x100
	s_addc_u32 s19, s19, 0
	s_add_u32 s57, s57, 0x100
	s_addc_u32 s58, s58, 0
	s_add_u32 s28, s28, 0x100
	s_addc_u32 s29, s29, 0
	s_cmp_gt_u32 s59, 29
	s_cbranch_scc0 .LBB0_611
	s_and_b64 vcc, exec, s[14:15]
	s_cbranch_vccz .LBB0_614
	s_barrier

; #define PG8_STAGEB(bufoff, gbase) PG8_STAGE2(bufoff, gbase, voffB[0], voffB[1])
; #define PG8_STAGEAS(bufoff, gbase, h) PG8_STAGE2(bufoff, gbase, voffA[h][0], voffA[h][1])
; #define PG8_LDA(dst, b, h) do { _Pragma("unroll") for (int m = 0; m < 4; ++m) _Pragma("unroll") for (int k = 0; k < 2; ++k) dst[m][k] = *(const LAS bf16x8*)(lds + PG8_SA(b, h) + aoff + m * 2048 + k * 1024); } while (0)
; #define PG8_WAIT_K0() do { if (EST > 0 && t == 0 && ui > 0) asm volatile("s_waitcnt vmcnt(%0)" :: "n"((HM ? 6 : 8) + EST) : "memory"); else PG8_WAIT_K(); } while (0)
; #define PG8_WAIT_L(n) asm volatile("s_waitcnt lgkmcnt(" #n ")" ::: "memory")
; #define PG8_BAR __builtin_amdgcn_s_barrier()
; #define PG8_SCHED __builtin_amdgcn_sched_barrier(0)
;     ...
;             PG8_WAIT_K0(); PG8_WAIT_L(0); PG8_BAR; PG8_MMA(0, 0, At, B0); PG8_MMA(0, 1, At, B1); PG8_BAR; PG8_SCHED;
;             if constexpr (!HM) PG8_LDA(At, 0, 1);
;             PG8_STAGEB(PG8_SB(0, 0), b2); PG8_STAGEB(PG8_SB(0, 1), b2 + hstepB); PG8_STAGEAS(PG8_SA(0, 0), a2, 0);
;             PG8_WAIT_K0(); PG8_WAIT_L(0); PG8_BAR; if constexpr (!HM) { PG8_MMA(1, 0, At, B0); PG8_MMA(1, 1, At, B1); } PG8_BAR; PG8_SCHED;
.LBB0_694:
	s_add_u32 s36, s30, 0x100
	s_waitcnt lgkmcnt(0)
	s_addc_u32 s37, s31, 0
	s_add_u32 s38, s34, 0x100
	s_addc_u32 s39, s35, 0
	s_barrier
	s_setprio 1
	v_mfma_f32_16x16x32_bf16 v[34:37], v[18:21], v[74:77], 0
	v_mfma_f32_16x16x32_bf16 v[38:41], v[26:29], v[74:77], 0
	v_mfma_f32_16x16x32_bf16 v[42:45], v[18:21], v[90:93], 0
	v_mfma_f32_16x16x32_bf16 v[46:49], v[26:29], v[90:93], 0
	v_mfma_f32_16x16x32_bf16 v[50:53], v[18:21], v[86:89], 0
	v_mfma_f32_16x16x32_bf16 v[54:57], v[26:29], v[86:89], 0
	v_mfma_f32_16x16x32_bf16 v[58:61], v[18:21], v[70:73], 0
	v_mfma_f32_16x16x32_bf16 v[62:65], v[26:29], v[70:73], 0
	v_mfma_f32_16x16x32_bf16 v[118:121], v[22:25], v[82:85], v[34:37]
	v_mfma_f32_16x16x32_bf16 v[38:41], v[30:33], v[82:85], v[38:41]
	v_mfma_f32_16x16x32_bf16 v[42:45], v[22:25], v[98:101], v[42:45]
	v_mfma_f32_16x16x32_bf16 v[46:49], v[30:33], v[98:101], v[46:49]
	v_mfma_f32_16x16x32_bf16 v[50:53], v[22:25], v[94:97], v[50:53]
	v_mfma_f32_16x16x32_bf16 v[54:57], v[30:33], v[94:97], v[54:57]
	v_mfma_f32_16x16x32_bf16 v[58:61], v[22:25], v[78:81], v[58:61]
	v_mfma_f32_16x16x32_bf16 v[62:65], v[30:33], v[78:81], v[62:65]
	v_mfma_f32_16x16x32_bf16 v[66:69], v[2:5], v[74:77], 0
	v_mfma_f32_16x16x32_bf16 v[74:77], v[10:13], v[74:77], 0
	v_mfma_f32_16x16x32_bf16 v[66:69], v[6:9], v[82:85], v[66:69]
	v_mfma_f32_16x16x32_bf16 v[74:77], v[14:17], v[82:85], v[74:77]
	v_mfma_f32_16x16x32_bf16 v[82:85], v[2:5], v[90:93], 0
	v_mfma_f32_16x16x32_bf16 v[90:93], v[10:13], v[90:93], 0
	v_mfma_f32_16x16x32_bf16 v[82:85], v[6:9], v[98:101], v[82:85]
	v_mfma_f32_16x16x32_bf16 v[90:93], v[14:17], v[98:101], v[90:93]
	v_mfma_f32_16x16x32_bf16 v[98:101], v[2:5], v[86:89], 0
	v_mfma_f32_16x16x32_bf16 v[86:89], v[10:13], v[86:89], 0
	v_mfma_f32_16x16x32_bf16 v[134:137], v[14:17], v[94:97], v[86:89]
	v_mfma_f32_16x16x32_bf16 v[86:89], v[2:5], v[70:73], 0
	v_mfma_f32_16x16x32_bf16 v[70:73], v[10:13], v[70:73], 0
	v_mfma_f32_16x16x32_bf16 v[130:133], v[6:9], v[94:97], v[98:101]
	v_mfma_f32_16x16x32_bf16 v[138:141], v[6:9], v[78:81], v[86:89]
	v_mfma_f32_16x16x32_bf16 v[142:145], v[14:17], v[78:81], v[70:73]
	s_setprio 0
	s_barrier
	ds_read_b128 v[106:109], v210 offset:16384
	ds_read_b128 v[110:113], v210 offset:17408
	ds_read_b128 v[98:101], v210 offset:18432
	ds_read_b128 v[102:105], v210 offset:19456
	ds_read_b128 v[86:89], v210 offset:20480
	ds_read_b128 v[94:97], v210 offset:21504
	ds_read_b128 v[70:73], v210 offset:22528
	ds_read_b128 v[78:81], v210 offset:23552
	s_mov_b32 m0, s43
	s_nop 0
	global_load_lds_dwordx4 v1, s[38:39]
	s_mov_b32 m0, s44
	s_nop 0
	global_load_lds_dwordx4 v200, s[38:39]
	s_add_u32 s38, s34, 0x80100
	s_addc_u32 s39, s35, 0
	s_mov_b32 m0, s45
	s_nop 0
	global_load_lds_dwordx4 v1, s[38:39]
	s_and_b64 vcc, exec, s[28:29]
	s_mov_b32 m0, s46
	s_nop 0
	global_load_lds_dwordx4 v200, s[38:39]
	s_mov_b32 m0, s42
	s_nop 0
	global_load_lds_dwordx4 v201, s[36:37]
	s_mov_b32 m0, s47
	s_nop 0
	global_load_lds_dwordx4 v202, s[36:37]
	s_cbranch_vccz .LBB0_721
	s_waitcnt vmcnt(40)
	s_cbranch_execnz .LBB0_697

; #define PG8_STAGEAS(bufoff, gbase, h) PG8_STAGE2(bufoff, gbase, voffA[h][0], voffA[h][1])
; #define PG8_LDA(dst, b, h) do { _Pragma("unroll") for (int m = 0; m < 4; ++m) _Pragma("unroll") for (int k = 0; k < 2; ++k) dst[m][k] = *(const LAS bf16x8*)(lds + PG8_SA(b, h) + aoff + m * 2048 + k * 1024); } while (0)
; #define PG8_LDB(dst, b, h) do { _Pragma("unroll") for (int n = 0; n < 2; ++n) _Pragma("unroll") for (int k = 0; k < 2; ++k) dst[n][k] = *(const LAS bf16x8*)(lds + PG8_SB(b, h) + boff + n * 2048 + k * 1024); } while (0)
; #define PG8_WAIT_K() do { if constexpr (HM) PG8_WAIT_V(6); else PG8_WAIT_V(8); } while (0)
; #define PG8_WAIT_K0() do { if (EST > 0 && t == 0 && ui > 0) asm volatile("s_waitcnt vmcnt(%0)" :: "n"((HM ? 6 : 8) + EST) : "memory"); else PG8_WAIT_K(); } while (0)
; #define PG8_WAIT_L(n) asm volatile("s_waitcnt lgkmcnt(" #n ")" ::: "memory")
; #define PG8_BAR __builtin_amdgcn_s_barrier()
; #define PG8_SCHED __builtin_amdgcn_sched_barrier(0)
;     ...
;             PG8_WAIT_K0(); PG8_WAIT_L(0); PG8_BAR; if constexpr (!HM) { PG8_MMA(1, 0, At, B0); PG8_MMA(1, 1, At, B1); } PG8_BAR; PG8_SCHED;
;             PG8_LDB(B0, 1, 0); PG8_LDB(B1, 1, 1); PG8_SCHED; PG8_LDA(At, 1, 0); if constexpr (!HM) PG8_STAGEAS(PG8_SA(0, 1), a2, 1);
;             PG8_WAIT_K(); PG8_WAIT_L(0); PG8_BAR; PG8_MMA(0, 0, At, B0); PG8_MMA(0, 1, At, B1); PG8_BAR; PG8_SCHED;
.LBB0_697:
	s_add_u32 s28, s30, 0x180
	s_waitcnt lgkmcnt(0)
	s_addc_u32 s29, s31, 0
	s_add_u32 s38, s34, 0x180
	s_addc_u32 s39, s35, 0
	s_barrier
	s_setprio 1
	v_mfma_f32_16x16x32_bf16 v[114:117], v[18:21], v[106:109], 0
	v_mfma_f32_16x16x32_bf16 v[148:151], v[22:25], v[110:113], v[114:117]
	v_mfma_f32_16x16x32_bf16 v[114:117], v[26:29], v[106:109], 0
	v_mfma_f32_16x16x32_bf16 v[152:155], v[30:33], v[110:113], v[114:117]
	v_mfma_f32_16x16x32_bf16 v[114:117], v[18:21], v[98:101], 0
	v_mfma_f32_16x16x32_bf16 v[156:159], v[22:25], v[102:105], v[114:117]
	v_mfma_f32_16x16x32_bf16 v[114:117], v[26:29], v[98:101], 0
	v_mfma_f32_16x16x32_bf16 v[160:163], v[30:33], v[102:105], v[114:117]
	v_mfma_f32_16x16x32_bf16 v[114:117], v[18:21], v[86:89], 0
	v_mfma_f32_16x16x32_bf16 v[18:21], v[18:21], v[70:73], 0
	v_mfma_f32_16x16x32_bf16 v[164:167], v[22:25], v[94:97], v[114:117]
	v_mfma_f32_16x16x32_bf16 v[18:21], v[22:25], v[78:81], v[18:21]
	v_mfma_f32_16x16x32_bf16 v[22:25], v[26:29], v[70:73], 0
	v_mfma_f32_16x16x32_bf16 v[114:117], v[26:29], v[86:89], 0
	v_mfma_f32_16x16x32_bf16 v[26:29], v[30:33], v[78:81], v[22:25]
	v_mfma_f32_16x16x32_bf16 v[168:171], v[30:33], v[94:97], v[114:117]
	v_mfma_f32_16x16x32_bf16 v[22:25], v[2:5], v[106:109], 0
	v_mfma_f32_16x16x32_bf16 v[172:175], v[6:9], v[110:113], v[22:25]
	v_mfma_f32_16x16x32_bf16 v[22:25], v[10:13], v[106:109], 0
	v_mfma_f32_16x16x32_bf16 v[182:185], v[14:17], v[110:113], v[22:25]
	v_mfma_f32_16x16x32_bf16 v[22:25], v[2:5], v[98:101], 0
	v_mfma_f32_16x16x32_bf16 v[186:189], v[6:9], v[102:105], v[22:25]
	v_mfma_f32_16x16x32_bf16 v[22:25], v[10:13], v[98:101], 0
	v_mfma_f32_16x16x32_bf16 v[190:193], v[14:17], v[102:105], v[22:25]
	v_mfma_f32_16x16x32_bf16 v[22:25], v[2:5], v[86:89], 0
	v_mfma_f32_16x16x32_bf16 v[2:5], v[2:5], v[70:73], 0
	v_mfma_f32_16x16x32_bf16 v[194:197], v[6:9], v[94:97], v[22:25]
	v_mfma_f32_16x16x32_bf16 v[22:25], v[10:13], v[86:89], 0
	v_mfma_f32_16x16x32_bf16 v[2:5], v[6:9], v[78:81], v[2:5]
	v_mfma_f32_16x16x32_bf16 v[6:9], v[10:13], v[70:73], 0
	v_mfma_f32_16x16x32_bf16 v[212:215], v[14:17], v[94:97], v[22:25]
	v_mfma_f32_16x16x32_bf16 v[216:219], v[14:17], v[78:81], v[6:9]
	s_setprio 0
	s_barrier
	v_add_u32_e32 v146, 0x18000, v207
	v_add_u32_e32 v147, 0x1c000, v207
	s_nop 1
	ds_read_b128 v[6:9], v146
	ds_read_b128 v[10:13], v146 offset:1024
	ds_read_b128 v[220:223], v146 offset:2048
	ds_read_b128 v[224:227], v146 offset:3072
	ds_read_b128 v[228:231], v147
	ds_read_b128 v[232:235], v147 offset:1024
	ds_read_b128 v[236:239], v147 offset:2048
	ds_read_b128 v[240:243], v147 offset:3072
	ds_read_b128 v[14:17], v210 offset:32768
	ds_read_b128 v[22:25], v210 offset:33792
	ds_read_b128 v[30:33], v210 offset:34816
	ds_read_b128 v[98:101], v210 offset:35840
	ds_read_b128 v[244:247], v210 offset:36864
	ds_read_b128 v[248:251], v210 offset:37888
	ds_read_b128 v[176:179], v210 offset:38912
	ds_read_b128 v[34:37], v210 offset:39936
	s_mov_b32 m0, s48
	s_nop 0
	global_load_lds_dwordx4 v203, s[36:37]
	s_mov_b32 m0, s49
	s_nop 0
	global_load_lds_dwordx4 v204, s[36:37]
	s_waitcnt vmcnt(8)
	s_waitcnt lgkmcnt(0)
	s_barrier
	s_setprio 1
	v_mfma_f32_16x16x32_bf16 v[38:41], v[220:223], v[14:17], v[38:41]
	v_mfma_f32_16x16x32_bf16 v[70:73], v[6:9], v[14:17], v[118:121]
	v_mfma_f32_16x16x32_bf16 v[118:121], v[224:227], v[22:25], v[38:41]
	v_mfma_f32_16x16x32_bf16 v[38:41], v[6:9], v[30:33], v[42:45]
	v_mfma_f32_16x16x32_bf16 v[110:113], v[10:13], v[98:101], v[38:41]
	v_mfma_f32_16x16x32_bf16 v[38:41], v[220:223], v[30:33], v[46:49]
	v_mfma_f32_16x16x32_bf16 v[102:105], v[224:227], v[98:101], v[38:41]
	v_mfma_f32_16x16x32_bf16 v[38:41], v[6:9], v[244:247], v[50:53]
	v_mfma_f32_16x16x32_bf16 v[94:97], v[10:13], v[248:251], v[38:41]
	v_mfma_f32_16x16x32_bf16 v[38:41], v[220:223], v[244:247], v[54:57]
	v_mfma_f32_16x16x32_bf16 v[86:89], v[224:227], v[248:251], v[38:41]
	v_mfma_f32_16x16x32_bf16 v[38:41], v[6:9], v[176:179], v[58:61]
	v_mfma_f32_16x16x32_bf16 v[78:81], v[10:13], v[34:37], v[38:41]
	v_mfma_f32_16x16x32_bf16 v[38:41], v[220:223], v[176:179], v[62:65]
	v_mfma_f32_16x16x32_bf16 v[126:129], v[10:13], v[22:25], v[70:73]
	v_mfma_f32_16x16x32_bf16 v[70:73], v[224:227], v[34:37], v[38:41]
	v_mfma_f32_16x16x32_bf16 v[38:41], v[228:231], v[14:17], v[66:69]
	v_mfma_f32_16x16x32_bf16 v[14:17], v[236:239], v[14:17], v[74:77]
	v_mfma_f32_16x16x32_bf16 v[114:117], v[240:243], v[22:25], v[14:17]
	v_mfma_f32_16x16x32_bf16 v[14:17], v[228:231], v[30:33], v[82:85]
	v_mfma_f32_16x16x32_bf16 v[106:109], v[232:235], v[98:101], v[14:17]
	v_mfma_f32_16x16x32_bf16 v[14:17], v[236:239], v[30:33], v[90:93]
	v_mfma_f32_16x16x32_bf16 v[98:101], v[240:243], v[98:101], v[14:17]
	v_mfma_f32_16x16x32_bf16 v[14:17], v[228:231], v[244:247], v[130:133]
	v_mfma_f32_16x16x32_bf16 v[90:93], v[232:235], v[248:251], v[14:17]
	v_mfma_f32_16x16x32_bf16 v[14:17], v[236:239], v[244:247], v[134:137]
	v_mfma_f32_16x16x32_bf16 v[82:85], v[240:243], v[248:251], v[14:17]
	v_mfma_f32_16x16x32_bf16 v[14:17], v[228:231], v[176:179], v[138:141]
	v_mfma_f32_16x16x32_bf16 v[74:77], v[232:235], v[34:37], v[14:17]
	v_mfma_f32_16x16x32_bf16 v[14:17], v[236:239], v[176:179], v[142:145]
	v_mfma_f32_16x16x32_bf16 v[122:125], v[232:235], v[22:25], v[38:41]
	v_mfma_f32_16x16x32_bf16 v[66:69], v[240:243], v[34:37], v[14:17]
	s_setprio 0
	s_barrier
; #define LAS __attribute__((address_space(3)))
; #define PG8_STAGEB(bufoff, gbase) PG8_STAGE2(bufoff, gbase, voffB[0], voffB[1])
; #define PG8_STAGEA(bufoff, gbase, h) PG8_STAGE2(bufoff, gbase, voffA[h][0], voffA[h][1])
; #define PG8_STAGEAS(bufoff, gbase, h) PG8_STAGE2(bufoff, gbase, voffA[h][0], voffA[h][1])
; #define PG8_LDA(dst, b, h) do { _Pragma("unroll") for (int m = 0; m < 4; ++m) _Pragma("unroll") for (int k = 0; k < 2; ++k) dst[m][k] = *(const LAS bf16x8*)(lds + PG8_SA(b, h) + aoff + m * 2048 + k * 1024); } while (0)
; #define PG8_LDB(dst, b, h) do { _Pragma("unroll") for (int n = 0; n < 2; ++n) _Pragma("unroll") for (int k = 0; k < 2; ++k) dst[n][k] = *(const LAS bf16x8*)(lds + PG8_SB(b, h) + boff + n * 2048 + k * 1024); } while (0)
;     ...
;             const char* a1 = cA + (size_t)(t + 1) * kstep;
;             const char* a2 = last ? nA : cA + (size_t)(t + 2) * kstep; const char* b2 = last ? nB : cB + (size_t)(t + 2) * kstep;
;             const char* a3 = a2 + kstep; const char* b3 = b2 + kstep;
;             PG8_LDB(B0, 0, 0); PG8_LDB(B1, 0, 1); PG8_SCHED; PG8_LDA(At, 0, 0); if constexpr (!HM) PG8_STAGEA(PG8_SA(1, 1), a1, 1);
;             if constexpr (Sched::kGather) { if (last && has_next) { const u32x4 tn = *(const LAS u32x4*)(S.aux + tid * 16); voffA[0][0] = tn.x; voffA[0][1] = tn.y; voffA[1][0] = tn.z; voffA[1][1] = tn.w; } }
;             PG8_WAIT_K0(); PG8_WAIT_L(0); PG8_BAR; PG8_MMA(0, 0, At, B0); PG8_MMA(0, 1, At, B1); PG8_BAR; PG8_SCHED;
;             if constexpr (!HM) PG8_LDA(At, 0, 1);
;             PG8_STAGEB(PG8_SB(0, 0), b2); PG8_STAGEB(PG8_SB(0, 1), b2 + hstepB); PG8_STAGEAS(PG8_SA(0, 0), a2, 0);
;             PG8_WAIT_K0(); PG8_WAIT_L(0); PG8_BAR; if constexpr (!HM) { PG8_MMA(1, 0, At, B0); PG8_MMA(1, 1, At, B1); } PG8_BAR; PG8_SCHED;
;             PG8_LDB(B0, 1, 0); PG8_LDB(B1, 1, 1); PG8_SCHED; PG8_LDA(At, 1, 0); if constexpr (!HM) PG8_STAGEAS(PG8_SA(0, 1), a2, 1);
;             PG8_WAIT_K(); PG8_WAIT_L(0); PG8_BAR; PG8_MMA(0, 0, At, B0); PG8_MMA(0, 1, At, B1); PG8_BAR; PG8_SCHED;
;             if constexpr (!HM) PG8_LDA(At, 1, 1);
;             PG8_STAGEB(PG8_SB(1, 0), b3); PG8_STAGEB(PG8_SB(1, 1), b3 + hstepB); PG8_STAGEAS(PG8_SA(1, 0), a3, 0);
;             PG8_WAIT_K(); PG8_WAIT_L(0); PG8_BAR; if constexpr (!HM) { PG8_MMA(1, 0, At, B0); PG8_MMA(1, 1, At, B1); } PG8_BAR; PG8_SCHED;
	ds_read_b128 v[34:37], v210 offset:49152
	ds_read_b128 v[42:45], v210 offset:50176
	ds_read_b128 v[130:133], v210 offset:51200
	ds_read_b128 v[134:137], v210 offset:52224
	ds_read_b128 v[138:141], v210 offset:53248
	ds_read_b128 v[142:145], v210 offset:54272
	ds_read_b128 v[176:179], v210 offset:55296
	ds_read_b128 v[244:247], v210 offset:56320
	s_mov_b32 m0, s52
	s_nop 0
	global_load_lds_dwordx4 v1, s[38:39]
	s_add_u32 s36, s34, 0x80180
	s_mov_b32 m0, s53
	s_nop 0
	global_load_lds_dwordx4 v200, s[38:39]
	s_addc_u32 s37, s35, 0
	s_mov_b32 m0, s56
	s_nop 0
	global_load_lds_dwordx4 v1, s[36:37]
	s_mov_b32 m0, s57
	s_nop 0
	global_load_lds_dwordx4 v200, s[36:37]
	s_mov_b32 m0, s54
	s_nop 0
	global_load_lds_dwordx4 v201, s[28:29]
	s_mov_b32 m0, s55
	s_nop 0
	global_load_lds_dwordx4 v202, s[28:29]
	s_waitcnt vmcnt(8)
	s_waitcnt lgkmcnt(0)
	s_barrier
	s_setprio 1
	v_mfma_f32_16x16x32_bf16 v[14:17], v[6:9], v[34:37], v[148:151]
	v_mfma_f32_16x16x32_bf16 v[62:65], v[10:13], v[42:45], v[14:17]
	v_mfma_f32_16x16x32_bf16 v[14:17], v[220:223], v[34:37], v[152:155]
	v_mfma_f32_16x16x32_bf16 v[54:57], v[224:227], v[42:45], v[14:17]
	v_mfma_f32_16x16x32_bf16 v[14:17], v[6:9], v[130:133], v[156:159]
	v_mfma_f32_16x16x32_bf16 v[46:49], v[10:13], v[134:137], v[14:17]
	v_mfma_f32_16x16x32_bf16 v[14:17], v[220:223], v[130:133], v[160:163]
	v_mfma_f32_16x16x32_bf16 v[38:41], v[224:227], v[134:137], v[14:17]
	v_mfma_f32_16x16x32_bf16 v[14:17], v[6:9], v[138:141], v[164:167]
	v_mfma_f32_16x16x32_bf16 v[30:33], v[10:13], v[142:145], v[14:17]
	v_mfma_f32_16x16x32_bf16 v[14:17], v[220:223], v[138:141], v[168:171]
	v_mfma_f32_16x16x32_bf16 v[6:9], v[6:9], v[176:179], v[18:21]
	v_mfma_f32_16x16x32_bf16 v[22:25], v[224:227], v[142:145], v[14:17]
	v_mfma_f32_16x16x32_bf16 v[14:17], v[10:13], v[244:247], v[6:9]
	v_mfma_f32_16x16x32_bf16 v[6:9], v[220:223], v[176:179], v[26:29]
	v_mfma_f32_16x16x32_bf16 v[6:9], v[224:227], v[244:247], v[6:9]
	v_mfma_f32_16x16x32_bf16 v[10:13], v[228:231], v[34:37], v[172:175]
	v_mfma_f32_16x16x32_bf16 v[58:61], v[232:235], v[42:45], v[10:13]
	v_mfma_f32_16x16x32_bf16 v[10:13], v[236:239], v[34:37], v[182:185]
	v_mfma_f32_16x16x32_bf16 v[50:53], v[240:243], v[42:45], v[10:13]
	v_mfma_f32_16x16x32_bf16 v[10:13], v[228:231], v[130:133], v[186:189]
	v_mfma_f32_16x16x32_bf16 v[42:45], v[232:235], v[134:137], v[10:13]
	v_mfma_f32_16x16x32_bf16 v[10:13], v[236:239], v[130:133], v[190:193]
	v_mfma_f32_16x16x32_bf16 v[34:37], v[240:243], v[134:137], v[10:13]
	v_mfma_f32_16x16x32_bf16 v[10:13], v[228:231], v[138:141], v[194:197]
	v_mfma_f32_16x16x32_bf16 v[26:29], v[232:235], v[142:145], v[10:13]
	v_mfma_f32_16x16x32_bf16 v[10:13], v[236:239], v[138:141], v[212:215]
	v_mfma_f32_16x16x32_bf16 v[2:5], v[228:231], v[176:179], v[2:5]
	v_mfma_f32_16x16x32_bf16 v[18:21], v[240:243], v[142:145], v[10:13]
	v_mfma_f32_16x16x32_bf16 v[10:13], v[232:235], v[244:247], v[2:5]
	v_mfma_f32_16x16x32_bf16 v[2:5], v[236:239], v[176:179], v[216:219]
	v_mfma_f32_16x16x32_bf16 v[2:5], v[240:243], v[244:247], v[2:5]
	s_setprio 0
	s_barrier
	s_add_u32 s19, s30, 0x200
	s_addc_u32 s21, s31, 0
	s_add_u32 s25, s34, 0x200
	s_addc_u32 s27, s35, 0
	s_mov_b32 s63, 0
.LBB0_698:
	ds_read_b128 v[130:133], v208
	ds_read_b128 v[134:137], v208 offset:1024
	ds_read_b128 v[138:141], v208 offset:2048
	ds_read_b128 v[142:145], v208 offset:3072
	ds_read_b128 v[148:151], v209
	ds_read_b128 v[152:155], v209 offset:1024
	ds_read_b128 v[156:159], v209 offset:2048
	ds_read_b128 v[160:163], v209 offset:3072
	s_cmp_eq_u32 s63, 28
	s_cselect_b32 s38, s0, s19
	s_cselect_b32 s39, s1, s21
	s_cselect_b32 s34, s22, s25
	s_cselect_b32 s35, s23, s27
	s_add_u32 s30, s38, 0x80
	s_addc_u32 s31, s39, 0
	ds_read_b128 v[164:167], v210
	ds_read_b128 v[168:171], v210 offset:1024
	ds_read_b128 v[172:175], v210 offset:2048
	ds_read_b128 v[176:179], v210 offset:3072
	ds_read_b128 v[182:185], v210 offset:4096
	ds_read_b128 v[186:189], v210 offset:5120
	ds_read_b128 v[190:193], v210 offset:6144
	ds_read_b128 v[194:197], v210 offset:7168
	s_mov_b32 m0, s58
	s_nop 0
	global_load_lds_dwordx4 v203, s[28:29]
	s_add_u32 s36, s34, 0x80
	s_mov_b32 m0, s59
	s_nop 0
	global_load_lds_dwordx4 v204, s[28:29]
	s_waitcnt vmcnt(8)
	s_waitcnt lgkmcnt(0)
	s_addc_u32 s37, s35, 0
	s_barrier
	s_setprio 1
	v_mfma_f32_16x16x32_bf16 v[126:129], v[130:133], v[164:167], v[126:129]
	v_mfma_f32_16x16x32_bf16 v[118:121], v[138:141], v[164:167], v[118:121]
	v_mfma_f32_16x16x32_bf16 v[110:113], v[130:133], v[172:175], v[110:113]
	v_mfma_f32_16x16x32_bf16 v[102:105], v[138:141], v[172:175], v[102:105]
	v_mfma_f32_16x16x32_bf16 v[94:97], v[130:133], v[182:185], v[94:97]
	v_mfma_f32_16x16x32_bf16 v[86:89], v[138:141], v[182:185], v[86:89]
	v_mfma_f32_16x16x32_bf16 v[78:81], v[130:133], v[190:193], v[78:81]
	v_mfma_f32_16x16x32_bf16 v[70:73], v[138:141], v[190:193], v[70:73]
	v_mfma_f32_16x16x32_bf16 v[126:129], v[134:137], v[168:171], v[126:129]
	v_mfma_f32_16x16x32_bf16 v[118:121], v[142:145], v[168:171], v[118:121]
	v_mfma_f32_16x16x32_bf16 v[110:113], v[134:137], v[176:179], v[110:113]
	v_mfma_f32_16x16x32_bf16 v[102:105], v[142:145], v[176:179], v[102:105]
	v_mfma_f32_16x16x32_bf16 v[94:97], v[134:137], v[186:189], v[94:97]
	v_mfma_f32_16x16x32_bf16 v[86:89], v[142:145], v[186:189], v[86:89]
	v_mfma_f32_16x16x32_bf16 v[78:81], v[134:137], v[194:197], v[78:81]
	v_mfma_f32_16x16x32_bf16 v[70:73], v[142:145], v[194:197], v[70:73]
	v_mfma_f32_16x16x32_bf16 v[122:125], v[148:151], v[164:167], v[122:125]
	v_mfma_f32_16x16x32_bf16 v[114:117], v[156:159], v[164:167], v[114:117]
	v_mfma_f32_16x16x32_bf16 v[106:109], v[148:151], v[172:175], v[106:109]
	v_mfma_f32_16x16x32_bf16 v[98:101], v[156:159], v[172:175], v[98:101]
	v_mfma_f32_16x16x32_bf16 v[90:93], v[148:151], v[182:185], v[90:93]
	v_mfma_f32_16x16x32_bf16 v[82:85], v[156:159], v[182:185], v[82:85]
	v_mfma_f32_16x16x32_bf16 v[74:77], v[148:151], v[190:193], v[74:77]
	v_mfma_f32_16x16x32_bf16 v[66:69], v[156:159], v[190:193], v[66:69]
	v_mfma_f32_16x16x32_bf16 v[122:125], v[152:155], v[168:171], v[122:125]
	v_mfma_f32_16x16x32_bf16 v[114:117], v[160:163], v[168:171], v[114:117]
	v_mfma_f32_16x16x32_bf16 v[106:109], v[152:155], v[176:179], v[106:109]
	v_mfma_f32_16x16x32_bf16 v[98:101], v[160:163], v[176:179], v[98:101]
	v_mfma_f32_16x16x32_bf16 v[90:93], v[152:155], v[186:189], v[90:93]
	v_mfma_f32_16x16x32_bf16 v[82:85], v[160:163], v[186:189], v[82:85]
	v_mfma_f32_16x16x32_bf16 v[74:77], v[152:155], v[194:197], v[74:77]
	v_mfma_f32_16x16x32_bf16 v[66:69], v[160:163], v[194:197], v[66:69]
	s_setprio 0
	s_barrier
; #define PG8_STAGEB(bufoff, gbase) PG8_STAGE2(bufoff, gbase, voffB[0], voffB[1])
; #define PG8_STAGEAS(bufoff, gbase, h) PG8_STAGE2(bufoff, gbase, voffA[h][0], voffA[h][1])
; #define PG8_LDA(dst, b, h) do { _Pragma("unroll") for (int m = 0; m < 4; ++m) _Pragma("unroll") for (int k = 0; k < 2; ++k) dst[m][k] = *(const LAS bf16x8*)(lds + PG8_SA(b, h) + aoff + m * 2048 + k * 1024); } while (0)
; #define PG8_LDB(dst, b, h) do { _Pragma("unroll") for (int n = 0; n < 2; ++n) _Pragma("unroll") for (int k = 0; k < 2; ++k) dst[n][k] = *(const LAS bf16x8*)(lds + PG8_SB(b, h) + boff + n * 2048 + k * 1024); } while (0)
; #define PG8_WAIT_K() do { if constexpr (HM) PG8_WAIT_V(6); else PG8_WAIT_V(8); } while (0)
; #define PG8_WAIT_K0() do { if (EST > 0 && t == 0 && ui > 0) asm volatile("s_waitcnt vmcnt(%0)" :: "n"((HM ? 6 : 8) + EST) : "memory"); else PG8_WAIT_K(); } while (0)
; #define PG8_WAIT_L(n) asm volatile("s_waitcnt lgkmcnt(" #n ")" ::: "memory")
; #define PG8_BAR __builtin_amdgcn_s_barrier()
; #define PG8_SCHED __builtin_amdgcn_sched_barrier(0)
;     ...
;             if constexpr (!HM) PG8_LDA(At, 0, 1);
;             PG8_STAGEB(PG8_SB(0, 0), b2); PG8_STAGEB(PG8_SB(0, 1), b2 + hstepB); PG8_STAGEAS(PG8_SA(0, 0), a2, 0);
;             PG8_WAIT_K0(); PG8_WAIT_L(0); PG8_BAR; if constexpr (!HM) { PG8_MMA(1, 0, At, B0); PG8_MMA(1, 1, At, B1); } PG8_BAR; PG8_SCHED;
;             PG8_LDB(B0, 1, 0); PG8_LDB(B1, 1, 1); PG8_SCHED; PG8_LDA(At, 1, 0); if constexpr (!HM) PG8_STAGEAS(PG8_SA(0, 1), a2, 1);
;             PG8_WAIT_K(); PG8_WAIT_L(0); PG8_BAR; PG8_MMA(0, 0, At, B0); PG8_MMA(0, 1, At, B1); PG8_BAR; PG8_SCHED;
	ds_read_b128 v[164:167], v210 offset:16384
	ds_read_b128 v[168:171], v210 offset:17408
	ds_read_b128 v[172:175], v210 offset:18432
	ds_read_b128 v[176:179], v210 offset:19456
	ds_read_b128 v[182:185], v210 offset:20480
	ds_read_b128 v[186:189], v210 offset:21504
	ds_read_b128 v[190:193], v210 offset:22528
	ds_read_b128 v[194:197], v210 offset:23552
	s_mov_b32 m0, s43
	s_nop 0
	global_load_lds_dwordx4 v1, s[34:35]
	s_mov_b32 m0, s44
	s_nop 0
	global_load_lds_dwordx4 v200, s[34:35]
	s_add_u32 s64, s34, 0x80000
	s_addc_u32 s65, s35, 0
	s_mov_b32 m0, s45
	s_nop 0
	global_load_lds_dwordx4 v1, s[64:65]
	s_mov_b32 m0, s46
	s_nop 0
	global_load_lds_dwordx4 v200, s[64:65]
	s_mov_b32 m0, s42
	s_nop 0
	global_load_lds_dwordx4 v201, s[38:39]
	s_mov_b32 m0, s47
	s_nop 0
	global_load_lds_dwordx4 v202, s[38:39]
	s_waitcnt vmcnt(8)
	s_waitcnt lgkmcnt(0)
	s_barrier
	s_setprio 1
	v_mfma_f32_16x16x32_bf16 v[62:65], v[130:133], v[164:167], v[62:65]
	v_mfma_f32_16x16x32_bf16 v[54:57], v[138:141], v[164:167], v[54:57]
	v_mfma_f32_16x16x32_bf16 v[46:49], v[130:133], v[172:175], v[46:49]
	v_mfma_f32_16x16x32_bf16 v[38:41], v[138:141], v[172:175], v[38:41]
	v_mfma_f32_16x16x32_bf16 v[30:33], v[130:133], v[182:185], v[30:33]
	v_mfma_f32_16x16x32_bf16 v[22:25], v[138:141], v[182:185], v[22:25]
	v_mfma_f32_16x16x32_bf16 v[14:17], v[130:133], v[190:193], v[14:17]
	v_mfma_f32_16x16x32_bf16 v[6:9], v[138:141], v[190:193], v[6:9]
	v_mfma_f32_16x16x32_bf16 v[62:65], v[134:137], v[168:171], v[62:65]
	v_mfma_f32_16x16x32_bf16 v[54:57], v[142:145], v[168:171], v[54:57]
	v_mfma_f32_16x16x32_bf16 v[46:49], v[134:137], v[176:179], v[46:49]
	v_mfma_f32_16x16x32_bf16 v[38:41], v[142:145], v[176:179], v[38:41]
	v_mfma_f32_16x16x32_bf16 v[30:33], v[134:137], v[186:189], v[30:33]
	v_mfma_f32_16x16x32_bf16 v[22:25], v[142:145], v[186:189], v[22:25]
	v_mfma_f32_16x16x32_bf16 v[14:17], v[134:137], v[194:197], v[14:17]
	v_mfma_f32_16x16x32_bf16 v[6:9], v[142:145], v[194:197], v[6:9]
	v_mfma_f32_16x16x32_bf16 v[58:61], v[148:151], v[164:167], v[58:61]
	v_mfma_f32_16x16x32_bf16 v[50:53], v[156:159], v[164:167], v[50:53]
	v_mfma_f32_16x16x32_bf16 v[42:45], v[148:151], v[172:175], v[42:45]
	v_mfma_f32_16x16x32_bf16 v[34:37], v[156:159], v[172:175], v[34:37]
	v_mfma_f32_16x16x32_bf16 v[26:29], v[148:151], v[182:185], v[26:29]
	v_mfma_f32_16x16x32_bf16 v[18:21], v[156:159], v[182:185], v[18:21]
	v_mfma_f32_16x16x32_bf16 v[10:13], v[148:151], v[190:193], v[10:13]
	v_mfma_f32_16x16x32_bf16 v[2:5], v[156:159], v[190:193], v[2:5]
	v_mfma_f32_16x16x32_bf16 v[58:61], v[152:155], v[168:171], v[58:61]
	v_mfma_f32_16x16x32_bf16 v[50:53], v[160:163], v[168:171], v[50:53]
	v_mfma_f32_16x16x32_bf16 v[42:45], v[152:155], v[176:179], v[42:45]
	v_mfma_f32_16x16x32_bf16 v[34:37], v[160:163], v[176:179], v[34:37]
	v_mfma_f32_16x16x32_bf16 v[26:29], v[152:155], v[186:189], v[26:29]
	v_mfma_f32_16x16x32_bf16 v[18:21], v[160:163], v[186:189], v[18:21]
	v_mfma_f32_16x16x32_bf16 v[10:13], v[152:155], v[194:197], v[10:13]
	v_mfma_f32_16x16x32_bf16 v[2:5], v[160:163], v[194:197], v[2:5]
	s_setprio 0
	s_barrier
	ds_read_b128 v[130:133], v146
	ds_read_b128 v[134:137], v146 offset:1024
	ds_read_b128 v[138:141], v146 offset:2048
	ds_read_b128 v[142:145], v146 offset:3072
	ds_read_b128 v[148:151], v147
	ds_read_b128 v[152:155], v147 offset:1024
	ds_read_b128 v[156:159], v147 offset:2048
	ds_read_b128 v[160:163], v147 offset:3072
	ds_read_b128 v[164:167], v210 offset:32768
	ds_read_b128 v[168:171], v210 offset:33792
	ds_read_b128 v[172:175], v210 offset:34816
	ds_read_b128 v[176:179], v210 offset:35840
	ds_read_b128 v[182:185], v210 offset:36864
	ds_read_b128 v[186:189], v210 offset:37888
	ds_read_b128 v[190:193], v210 offset:38912
	ds_read_b128 v[194:197], v210 offset:39936
	s_mov_b32 m0, s48
	s_nop 0
	global_load_lds_dwordx4 v203, s[38:39]
	s_mov_b32 m0, s49
	s_nop 0
	global_load_lds_dwordx4 v204, s[38:39]
	s_waitcnt vmcnt(8)
	s_waitcnt lgkmcnt(0)
	s_barrier
; #define PG8_STAGEB(bufoff, gbase) PG8_STAGE2(bufoff, gbase, voffB[0], voffB[1])
; #define PG8_STAGEAS(bufoff, gbase, h) PG8_STAGE2(bufoff, gbase, voffA[h][0], voffA[h][1])
; #define PG8_LDA(dst, b, h) do { _Pragma("unroll") for (int m = 0; m < 4; ++m) _Pragma("unroll") for (int k = 0; k < 2; ++k) dst[m][k] = *(const LAS bf16x8*)(lds + PG8_SA(b, h) + aoff + m * 2048 + k * 1024); } while (0)
; #define PG8_WAIT_K() do { if constexpr (HM) PG8_WAIT_V(6); else PG8_WAIT_V(8); } while (0)
; #define PG8_WAIT_L(n) asm volatile("s_waitcnt lgkmcnt(" #n ")" ::: "memory")
; #define PG8_BAR __builtin_amdgcn_s_barrier()
; #define PG8_SCHED __builtin_amdgcn_sched_barrier(0)
;     ...
;             PG8_WAIT_K(); PG8_WAIT_L(0); PG8_BAR; PG8_MMA(0, 0, At, B0); PG8_MMA(0, 1, At, B1); PG8_BAR; PG8_SCHED;
;             if constexpr (!HM) PG8_LDA(At, 1, 1);
;             PG8_STAGEB(PG8_SB(1, 0), b3); PG8_STAGEB(PG8_SB(1, 1), b3 + hstepB); PG8_STAGEAS(PG8_SA(1, 0), a3, 0);
;             PG8_WAIT_K(); PG8_WAIT_L(0); PG8_BAR; if constexpr (!HM) { PG8_MMA(1, 0, At, B0); PG8_MMA(1, 1, At, B1); } PG8_BAR; PG8_SCHED;
;         }
;         if (wr == 0) PG8_BAR;
	s_setprio 1
	v_mfma_f32_16x16x32_bf16 v[126:129], v[130:133], v[164:167], v[126:129]
	v_mfma_f32_16x16x32_bf16 v[118:121], v[138:141], v[164:167], v[118:121]
	v_mfma_f32_16x16x32_bf16 v[110:113], v[130:133], v[172:175], v[110:113]
	v_mfma_f32_16x16x32_bf16 v[102:105], v[138:141], v[172:175], v[102:105]
	v_mfma_f32_16x16x32_bf16 v[94:97], v[130:133], v[182:185], v[94:97]
	v_mfma_f32_16x16x32_bf16 v[86:89], v[138:141], v[182:185], v[86:89]
	v_mfma_f32_16x16x32_bf16 v[78:81], v[130:133], v[190:193], v[78:81]
	v_mfma_f32_16x16x32_bf16 v[70:73], v[138:141], v[190:193], v[70:73]
	v_mfma_f32_16x16x32_bf16 v[126:129], v[134:137], v[168:171], v[126:129]
	v_mfma_f32_16x16x32_bf16 v[118:121], v[142:145], v[168:171], v[118:121]
	v_mfma_f32_16x16x32_bf16 v[110:113], v[134:137], v[176:179], v[110:113]
	v_mfma_f32_16x16x32_bf16 v[102:105], v[142:145], v[176:179], v[102:105]
	v_mfma_f32_16x16x32_bf16 v[94:97], v[134:137], v[186:189], v[94:97]
	v_mfma_f32_16x16x32_bf16 v[86:89], v[142:145], v[186:189], v[86:89]
	v_mfma_f32_16x16x32_bf16 v[78:81], v[134:137], v[194:197], v[78:81]
	v_mfma_f32_16x16x32_bf16 v[70:73], v[142:145], v[194:197], v[70:73]
	v_mfma_f32_16x16x32_bf16 v[122:125], v[148:151], v[164:167], v[122:125]
	v_mfma_f32_16x16x32_bf16 v[114:117], v[156:159], v[164:167], v[114:117]
	v_mfma_f32_16x16x32_bf16 v[106:109], v[148:151], v[172:175], v[106:109]
	v_mfma_f32_16x16x32_bf16 v[98:101], v[156:159], v[172:175], v[98:101]
	v_mfma_f32_16x16x32_bf16 v[90:93], v[148:151], v[182:185], v[90:93]
	v_mfma_f32_16x16x32_bf16 v[82:85], v[156:159], v[182:185], v[82:85]
	v_mfma_f32_16x16x32_bf16 v[74:77], v[148:151], v[190:193], v[74:77]
	v_mfma_f32_16x16x32_bf16 v[66:69], v[156:159], v[190:193], v[66:69]
	v_mfma_f32_16x16x32_bf16 v[122:125], v[152:155], v[168:171], v[122:125]
	v_mfma_f32_16x16x32_bf16 v[114:117], v[160:163], v[168:171], v[114:117]
	v_mfma_f32_16x16x32_bf16 v[106:109], v[152:155], v[176:179], v[106:109]
	v_mfma_f32_16x16x32_bf16 v[98:101], v[160:163], v[176:179], v[98:101]
	v_mfma_f32_16x16x32_bf16 v[90:93], v[152:155], v[186:189], v[90:93]
	v_mfma_f32_16x16x32_bf16 v[82:85], v[160:163], v[186:189], v[82:85]
	v_mfma_f32_16x16x32_bf16 v[74:77], v[152:155], v[194:197], v[74:77]
	v_mfma_f32_16x16x32_bf16 v[66:69], v[160:163], v[194:197], v[66:69]
	s_setprio 0
	s_barrier
	ds_read_b128 v[164:167], v210 offset:49152
	ds_read_b128 v[168:171], v210 offset:50176
	ds_read_b128 v[172:175], v210 offset:51200
	ds_read_b128 v[176:179], v210 offset:52224
	ds_read_b128 v[182:185], v210 offset:53248
	ds_read_b128 v[186:189], v210 offset:54272
	ds_read_b128 v[190:193], v210 offset:55296
	ds_read_b128 v[194:197], v210 offset:56320
	s_mov_b32 m0, s52
	s_nop 0
	global_load_lds_dwordx4 v1, s[36:37]
	s_add_u32 s34, s34, 0x80080
	s_mov_b32 m0, s53
	s_nop 0
	global_load_lds_dwordx4 v200, s[36:37]
	s_addc_u32 s35, s35, 0
	s_mov_b32 m0, s56
	s_nop 0
	global_load_lds_dwordx4 v1, s[34:35]
	s_mov_b32 m0, s57
	s_nop 0
	global_load_lds_dwordx4 v200, s[34:35]
	s_mov_b32 m0, s54
	s_nop 0
	global_load_lds_dwordx4 v201, s[30:31]
	s_mov_b32 m0, s55
	s_nop 0
	global_load_lds_dwordx4 v202, s[30:31]
	s_waitcnt vmcnt(8)
	s_waitcnt lgkmcnt(0)
	s_barrier
	s_setprio 1
	v_mfma_f32_16x16x32_bf16 v[62:65], v[130:133], v[164:167], v[62:65]
	v_mfma_f32_16x16x32_bf16 v[54:57], v[138:141], v[164:167], v[54:57]
	v_mfma_f32_16x16x32_bf16 v[46:49], v[130:133], v[172:175], v[46:49]
	v_mfma_f32_16x16x32_bf16 v[38:41], v[138:141], v[172:175], v[38:41]
	v_mfma_f32_16x16x32_bf16 v[30:33], v[130:133], v[182:185], v[30:33]
	v_mfma_f32_16x16x32_bf16 v[22:25], v[138:141], v[182:185], v[22:25]
	v_mfma_f32_16x16x32_bf16 v[14:17], v[130:133], v[190:193], v[14:17]
	v_mfma_f32_16x16x32_bf16 v[6:9], v[138:141], v[190:193], v[6:9]
	v_mfma_f32_16x16x32_bf16 v[62:65], v[134:137], v[168:171], v[62:65]
	v_mfma_f32_16x16x32_bf16 v[54:57], v[142:145], v[168:171], v[54:57]
	v_mfma_f32_16x16x32_bf16 v[46:49], v[134:137], v[176:179], v[46:49]
	v_mfma_f32_16x16x32_bf16 v[38:41], v[142:145], v[176:179], v[38:41]
	v_mfma_f32_16x16x32_bf16 v[30:33], v[134:137], v[186:189], v[30:33]
	v_mfma_f32_16x16x32_bf16 v[22:25], v[142:145], v[186:189], v[22:25]
	v_mfma_f32_16x16x32_bf16 v[14:17], v[134:137], v[194:197], v[14:17]
	v_mfma_f32_16x16x32_bf16 v[6:9], v[142:145], v[194:197], v[6:9]
	v_mfma_f32_16x16x32_bf16 v[58:61], v[148:151], v[164:167], v[58:61]
	v_mfma_f32_16x16x32_bf16 v[50:53], v[156:159], v[164:167], v[50:53]
	v_mfma_f32_16x16x32_bf16 v[42:45], v[148:151], v[172:175], v[42:45]
	v_mfma_f32_16x16x32_bf16 v[34:37], v[156:159], v[172:175], v[34:37]
	v_mfma_f32_16x16x32_bf16 v[26:29], v[148:151], v[182:185], v[26:29]
	v_mfma_f32_16x16x32_bf16 v[18:21], v[156:159], v[182:185], v[18:21]
	v_mfma_f32_16x16x32_bf16 v[10:13], v[148:151], v[190:193], v[10:13]
	v_mfma_f32_16x16x32_bf16 v[2:5], v[156:159], v[190:193], v[2:5]
	v_mfma_f32_16x16x32_bf16 v[58:61], v[152:155], v[168:171], v[58:61]
	v_mfma_f32_16x16x32_bf16 v[50:53], v[160:163], v[168:171], v[50:53]
	v_mfma_f32_16x16x32_bf16 v[42:45], v[152:155], v[176:179], v[42:45]
	v_mfma_f32_16x16x32_bf16 v[34:37], v[160:163], v[176:179], v[34:37]
	v_mfma_f32_16x16x32_bf16 v[26:29], v[152:155], v[186:189], v[26:29]
	v_mfma_f32_16x16x32_bf16 v[18:21], v[160:163], v[186:189], v[18:21]
	v_mfma_f32_16x16x32_bf16 v[10:13], v[152:155], v[194:197], v[10:13]
	v_mfma_f32_16x16x32_bf16 v[2:5], v[160:163], v[194:197], v[2:5]
	s_setprio 0
	s_barrier
	s_add_i32 s63, s63, 2
	s_add_u32 s19, s19, 0x100
	s_addc_u32 s21, s21, 0
	s_add_u32 s25, s25, 0x100
	s_addc_u32 s27, s27, 0
	s_add_u32 s28, s28, 0x100
	s_addc_u32 s29, s29, 0
	s_cmp_gt_u32 s63, 29
	s_cbranch_scc0 .LBB0_698
	s_and_b64 vcc, exec, s[16:17]
	s_cbranch_vccz .LBB0_701
	s_barrier

; #define PG8_STAGEB(bufoff, gbase) PG8_STAGE2(bufoff, gbase, voffB[0], voffB[1])
; #define PG8_STAGEAS(bufoff, gbase, h) PG8_STAGE2(bufoff, gbase, voffA[h][0], voffA[h][1])
; #define PG8_LDA(dst, b, h) do { _Pragma("unroll") for (int m = 0; m < 4; ++m) _Pragma("unroll") for (int k = 0; k < 2; ++k) dst[m][k] = *(const LAS bf16x8*)(lds + PG8_SA(b, h) + aoff + m * 2048 + k * 1024); } while (0)
; #define PG8_WAIT_K0() do { if (EST > 0 && t == 0 && ui > 0) asm volatile("s_waitcnt vmcnt(%0)" :: "n"((HM ? 6 : 8) + EST) : "memory"); else PG8_WAIT_K(); } while (0)
; #define PG8_WAIT_L(n) asm volatile("s_waitcnt lgkmcnt(" #n ")" ::: "memory")
; #define PG8_BAR __builtin_amdgcn_s_barrier()
; #define PG8_SCHED __builtin_amdgcn_sched_barrier(0)
;     ...
;             PG8_WAIT_K0(); PG8_WAIT_L(0); PG8_BAR; PG8_MMA(0, 0, At, B0); PG8_MMA(0, 1, At, B1); PG8_BAR; PG8_SCHED;
;             if constexpr (!HM) PG8_LDA(At, 0, 1);
;             PG8_STAGEB(PG8_SB(0, 0), b2); PG8_STAGEB(PG8_SB(0, 1), b2 + hstepB); PG8_STAGEAS(PG8_SA(0, 0), a2, 0);
;             PG8_WAIT_K0(); PG8_WAIT_L(0); PG8_BAR; if constexpr (!HM) { PG8_MMA(1, 0, At, B0); PG8_MMA(1, 1, At, B1); } PG8_BAR; PG8_SCHED;
.LBB0_1131:
	s_waitcnt lgkmcnt(0)
	s_add_u32 s18, s48, 0x100
	s_addc_u32 s19, s49, 0
	s_barrier
	s_setprio 1
	v_mov_b64_e32 v[100:101], s[14:15]
	v_mov_b64_e32 v[172:173], s[14:15]
	v_mov_b64_e32 v[168:169], s[14:15]
	v_mov_b64_e32 v[156:157], s[14:15]
	v_mov_b64_e32 v[152:153], s[14:15]
	v_mov_b64_e32 v[144:145], s[14:15]
	v_mov_b64_e32 v[136:137], s[14:15]
	v_mov_b64_e32 v[120:121], s[14:15]
	v_mov_b64_e32 v[112:113], s[14:15]
	v_mov_b32_e32 v24, v56
	v_mov_b32_e32 v25, v57
	v_mov_b64_e32 v[98:99], s[12:13]
	v_mov_b64_e32 v[170:171], s[12:13]
	v_mov_b32_e32 v18, v64
	v_mov_b32_e32 v19, v65
	v_mov_b64_e32 v[166:167], s[12:13]
	v_mov_b64_e32 v[154:155], s[12:13]
	v_mov_b64_e32 v[150:151], s[12:13]
	v_mov_b64_e32 v[142:143], s[12:13]
	v_mov_b64_e32 v[134:135], s[12:13]
	v_mov_b64_e32 v[118:119], s[12:13]
	v_mov_b64_e32 v[110:111], s[12:13]
	v_mov_b32_e32 v48, v76
	v_mov_b32_e32 v49, v77
	s_nop 1
	v_mfma_scale_f32_16x16x128_f8f6f4 v[170:173], v[20:25], v[44:49], v[170:173], v58, v78 op_sel_hi:[0,0,0] cbsz:2 blgp:2
	s_nop 1
	v_mfma_scale_f32_16x16x128_f8f6f4 v[166:169], v[14:19], v[44:49], v[166:169], v66, v78 op_sel_hi:[0,0,0] cbsz:2 blgp:2
	v_mov_b32_e32 v42, v72
	v_mov_b32_e32 v43, v73
	s_nop 1
	v_mfma_scale_f32_16x16x128_f8f6f4 v[154:157], v[20:25], v[38:43], v[154:157], v58, v74 op_sel_hi:[0,0,0] cbsz:2 blgp:2
	s_nop 1
	v_mfma_scale_f32_16x16x128_f8f6f4 v[150:153], v[14:19], v[38:43], v[150:153], v66, v74 op_sel_hi:[0,0,0] cbsz:2 blgp:2
	v_mov_b32_e32 v36, v68
	v_mov_b32_e32 v37, v69
	s_nop 1
	v_mfma_scale_f32_16x16x128_f8f6f4 v[142:145], v[20:25], v[32:37], v[142:145], v58, v70 op_sel_hi:[0,0,0] cbsz:2 blgp:2
	s_nop 1
	v_mfma_scale_f32_16x16x128_f8f6f4 v[134:137], v[14:19], v[32:37], v[134:137], v66, v70 op_sel_hi:[0,0,0] cbsz:2 blgp:2
	v_mov_b32_e32 v30, v60
	v_mov_b32_e32 v31, v61
	s_nop 1
	v_mfma_scale_f32_16x16x128_f8f6f4 v[118:121], v[20:25], v[26:31], v[118:121], v58, v62 op_sel_hi:[0,0,0] cbsz:2 blgp:2
	s_nop 1
	v_mfma_scale_f32_16x16x128_f8f6f4 v[110:113], v[14:19], v[26:31], v[110:113], v66, v62 op_sel_hi:[0,0,0] cbsz:2 blgp:2
	v_mov_b64_e32 v[180:181], s[14:15]
	v_mov_b64_e32 v[176:177], s[14:15]
	v_mov_b64_e32 v[164:165], s[14:15]
	v_mov_b64_e32 v[160:161], s[14:15]
	v_mov_b64_e32 v[148:149], s[14:15]
	v_mov_b64_e32 v[140:141], s[14:15]
	v_mov_b64_e32 v[128:129], s[14:15]
	v_mov_b32_e32 v12, v186
	v_mov_b32_e32 v13, v187
	v_mov_b64_e32 v[178:179], s[12:13]
	v_mov_b32_e32 v6, v182
	v_mov_b32_e32 v7, v183
	v_mov_b64_e32 v[174:175], s[12:13]
	v_mov_b64_e32 v[162:163], s[12:13]
	v_mov_b64_e32 v[158:159], s[12:13]
	v_mov_b64_e32 v[146:147], s[12:13]
	v_mov_b64_e32 v[138:139], s[12:13]
	v_mov_b64_e32 v[126:127], s[12:13]
	s_nop 1
	v_mfma_scale_f32_16x16x128_f8f6f4 v[178:181], v[8:13], v[44:49], v[178:181], v188, v78 op_sel_hi:[0,0,0] cbsz:2 blgp:2
	s_nop 1
	v_mfma_scale_f32_16x16x128_f8f6f4 v[174:177], v[2:7], v[44:49], v[174:177], v184, v78 op_sel_hi:[0,0,0] cbsz:2 blgp:2
	s_nop 1
	v_mfma_scale_f32_16x16x128_f8f6f4 v[162:165], v[8:13], v[38:43], v[162:165], v188, v74 op_sel_hi:[0,0,0] cbsz:2 blgp:2
	s_nop 1
	v_mfma_scale_f32_16x16x128_f8f6f4 v[158:161], v[2:7], v[38:43], v[158:161], v184, v74 op_sel_hi:[0,0,0] cbsz:2 blgp:2
	s_nop 1
	v_mfma_scale_f32_16x16x128_f8f6f4 v[146:149], v[8:13], v[32:37], v[146:149], v188, v70 op_sel_hi:[0,0,0] cbsz:2 blgp:2
	s_nop 1
	v_mfma_scale_f32_16x16x128_f8f6f4 v[138:141], v[2:7], v[32:37], v[138:141], v184, v70 op_sel_hi:[0,0,0] cbsz:2 blgp:2
	s_nop 1
	v_mfma_scale_f32_16x16x128_f8f6f4 v[126:129], v[8:13], v[26:31], v[126:129], v188, v62 op_sel_hi:[0,0,0] cbsz:2 blgp:2
	s_nop 1
	v_mfma_scale_f32_16x16x128_f8f6f4 v[98:101], v[2:7], v[26:31], v[98:101], v184, v62 op_sel_hi:[0,0,0] cbsz:2 blgp:2
	s_setprio 0
	s_barrier
	ds_read_b128 v[44:47], v224 offset:16384
	ds_read_b128 v[80:83], v224 offset:17408
	ds_read_b128 v[38:41], v224 offset:18432
	ds_read_b128 v[72:75], v224 offset:19456
	ds_read_b128 v[32:35], v224 offset:20480
	ds_read_b128 v[194:197], v224 offset:21504
	ds_read_b128 v[26:29], v224 offset:22528
	ds_read_b128 v[190:193], v224 offset:23552
	s_mov_b32 m0, s47
	s_nop 0
	global_load_lds_dwordx4 v217, s[18:19]
	s_mov_b32 m0, s66
	s_nop 0
	global_load_lds_dwordx4 v218, s[18:19]
	s_add_u32 s18, s48, 0x40100
	s_addc_u32 s19, s49, 0
	s_mov_b32 m0, s67
	s_nop 0
	global_load_lds_dwordx4 v217, s[18:19]
	s_and_b64 vcc, exec, s[16:17]
	s_mov_b32 m0, s68
	s_nop 0
	global_load_lds_dwordx4 v218, s[18:19]
	s_mov_b32 m0, s35
	s_nop 0
	global_load_lds_dwordx4 v50, s[24:25]
	s_mov_b32 m0, s69
	s_nop 0
	global_load_lds_dwordx4 v51, s[24:25]
	s_cbranch_vccz .LBB0_1148
	s_waitcnt vmcnt(16)
	s_cbranch_execnz .LBB0_1134

; #define PG8_STAGEAS(bufoff, gbase, h) PG8_STAGE2(bufoff, gbase, voffA[h][0], voffA[h][1])
; #define PG8_LDA(dst, b, h) do { _Pragma("unroll") for (int m = 0; m < 4; ++m) _Pragma("unroll") for (int k = 0; k < 2; ++k) dst[m][k] = *(const LAS bf16x8*)(lds + PG8_SA(b, h) + aoff + m * 2048 + k * 1024); } while (0)
; #define PG8_LDB(dst, b, h) do { _Pragma("unroll") for (int n = 0; n < 2; ++n) _Pragma("unroll") for (int k = 0; k < 2; ++k) dst[n][k] = *(const LAS bf16x8*)(lds + PG8_SB(b, h) + boff + n * 2048 + k * 1024); } while (0)
; #define PG8_WAIT_K() do { if constexpr (HM) PG8_WAIT_V(6); else PG8_WAIT_V(8); } while (0)
; #define PG8_WAIT_K0() do { if (EST > 0 && t == 0 && ui > 0) asm volatile("s_waitcnt vmcnt(%0)" :: "n"((HM ? 6 : 8) + EST) : "memory"); else PG8_WAIT_K(); } while (0)
; #define PG8_WAIT_L(n) asm volatile("s_waitcnt lgkmcnt(" #n ")" ::: "memory")
; #define PG8_BAR __builtin_amdgcn_s_barrier()
; #define PG8_SCHED __builtin_amdgcn_sched_barrier(0)
;     ...
;             PG8_WAIT_K0(); PG8_WAIT_L(0); PG8_BAR; if constexpr (!HM) { PG8_MMA(1, 0, At, B0); PG8_MMA(1, 1, At, B1); } PG8_BAR; PG8_SCHED;
;             PG8_LDB(B0, 1, 0); PG8_LDB(B1, 1, 1); PG8_SCHED; PG8_LDA(At, 1, 0); if constexpr (!HM) PG8_STAGEAS(PG8_SA(0, 1), a2, 1);
;             PG8_WAIT_K(); PG8_WAIT_L(0); PG8_BAR; PG8_MMA(0, 0, At, B0); PG8_MMA(0, 1, At, B1); PG8_BAR; PG8_SCHED;
.LBB0_1134:
	s_waitcnt lgkmcnt(0)
	s_add_u32 s50, s48, 0x180
	s_addc_u32 s51, s49, 0
	s_barrier
	s_setprio 1
	s_mov_b32 s16, 0
	s_mov_b32 s18, s16
	s_mov_b32 s19, s16
	v_mov_b32_e32 v48, v80
	v_mov_b32_e32 v49, v81
	s_mov_b32 s17, s16
	v_mov_b64_e32 v[116:117], s[18:19]
	v_mov_b64_e32 v[108:109], s[18:19]
	v_mov_b32_e32 v42, v72
	v_mov_b32_e32 v43, v73
	v_mov_b64_e32 v[96:97], s[18:19]
	v_mov_b64_e32 v[88:89], s[18:19]
	v_mov_b64_e32 v[80:81], s[18:19]
	v_mov_b64_e32 v[72:73], s[18:19]
	v_mov_b64_e32 v[64:65], s[18:19]
	v_mov_b64_e32 v[114:115], s[16:17]
	v_mov_b64_e32 v[106:107], s[16:17]
	v_mov_b64_e32 v[94:95], s[16:17]
	v_mov_b64_e32 v[86:87], s[16:17]
	v_mov_b64_e32 v[78:79], s[16:17]
	v_mov_b64_e32 v[70:71], s[16:17]
	v_mov_b64_e32 v[62:63], s[16:17]
	v_mov_b64_e32 v[56:57], s[18:19]
	s_nop 1
	v_mfma_scale_f32_16x16x128_f8f6f4 v[114:117], v[20:25], v[44:49], v[114:117], v58, v82 op_sel_hi:[0,0,0] cbsz:2 blgp:2
	s_nop 1
	v_mfma_scale_f32_16x16x128_f8f6f4 v[106:109], v[14:19], v[44:49], v[106:109], v66, v82 op_sel_hi:[0,0,0] cbsz:2 blgp:2
	s_nop 1
	v_mfma_scale_f32_16x16x128_f8f6f4 v[94:97], v[20:25], v[38:43], v[94:97], v58, v74 op_sel_hi:[0,0,0] cbsz:2 blgp:2
	s_nop 1
	v_mfma_scale_f32_16x16x128_f8f6f4 v[86:89], v[14:19], v[38:43], v[86:89], v66, v74 op_sel_hi:[0,0,0] cbsz:2 blgp:2
	v_mov_b32_e32 v36, v194
	v_mov_b32_e32 v37, v195
	s_nop 1
	v_mfma_scale_f32_16x16x128_f8f6f4 v[78:81], v[20:25], v[32:37], v[78:81], v58, v196 op_sel_hi:[0,0,0] cbsz:2 blgp:2
	s_nop 1
	v_mfma_scale_f32_16x16x128_f8f6f4 v[70:73], v[14:19], v[32:37], v[70:73], v66, v196 op_sel_hi:[0,0,0] cbsz:2 blgp:2
	v_mov_b32_e32 v30, v190
	v_mov_b32_e32 v31, v191
	s_nop 1
	v_mfma_scale_f32_16x16x128_f8f6f4 v[62:65], v[20:25], v[26:31], v[62:65], v58, v192 op_sel_hi:[0,0,0] cbsz:2 blgp:2
	v_mov_b64_e32 v[60:61], s[18:19]
	v_mov_b64_e32 v[54:55], s[16:17]
	v_mov_b64_e32 v[58:59], s[16:17]
	s_nop 1
	v_mfma_scale_f32_16x16x128_f8f6f4 v[58:61], v[14:19], v[26:31], v[58:61], v66, v192 op_sel_hi:[0,0,0] cbsz:2 blgp:2
	v_mov_b64_e32 v[132:133], s[18:19]
	v_mov_b64_e32 v[124:125], s[18:19]
	v_mov_b64_e32 v[104:105], s[18:19]
	v_mov_b64_e32 v[92:93], s[18:19]
	v_mov_b64_e32 v[130:131], s[16:17]
	v_mov_b64_e32 v[122:123], s[16:17]
	v_mov_b64_e32 v[102:103], s[16:17]
	v_mov_b64_e32 v[90:91], s[16:17]
	s_nop 1
	v_mfma_scale_f32_16x16x128_f8f6f4 v[130:133], v[8:13], v[44:49], v[130:133], v188, v82 op_sel_hi:[0,0,0] cbsz:2 blgp:2
	s_nop 1
	v_mfma_scale_f32_16x16x128_f8f6f4 v[122:125], v[2:7], v[44:49], v[122:125], v184, v82 op_sel_hi:[0,0,0] cbsz:2 blgp:2
	s_nop 1
	v_mfma_scale_f32_16x16x128_f8f6f4 v[102:105], v[8:13], v[38:43], v[102:105], v188, v74 op_sel_hi:[0,0,0] cbsz:2 blgp:2
	s_nop 1
	v_mfma_scale_f32_16x16x128_f8f6f4 v[90:93], v[2:7], v[38:43], v[90:93], v184, v74 op_sel_hi:[0,0,0] cbsz:2 blgp:2
	v_mov_b64_e32 v[84:85], s[18:19]
	v_mov_b64_e32 v[76:77], s[18:19]
	v_mov_b64_e32 v[68:69], s[18:19]
	v_mov_b64_e32 v[82:83], s[16:17]
	v_mov_b64_e32 v[74:75], s[16:17]
	v_mov_b64_e32 v[66:67], s[16:17]
	s_nop 1
	v_mfma_scale_f32_16x16x128_f8f6f4 v[82:85], v[8:13], v[32:37], v[82:85], v188, v196 op_sel_hi:[0,0,0] cbsz:2 blgp:2
	s_nop 1
	v_mfma_scale_f32_16x16x128_f8f6f4 v[74:77], v[2:7], v[32:37], v[74:77], v184, v196 op_sel_hi:[0,0,0] cbsz:2 blgp:2
	s_nop 1
	v_mfma_scale_f32_16x16x128_f8f6f4 v[66:69], v[8:13], v[26:31], v[66:69], v188, v192 op_sel_hi:[0,0,0] cbsz:2 blgp:2
	s_nop 1
	v_mfma_scale_f32_16x16x128_f8f6f4 v[54:57], v[2:7], v[26:31], v[54:57], v184, v192 op_sel_hi:[0,0,0] cbsz:2 blgp:2
	s_setprio 0
	s_barrier
	v_add_u32_e32 v232, 0x18000, v223
	v_add_u32_e32 v233, 0x1c000, v223
	ds_read_b128 v[20:23], v232
	ds_read_b128 v[38:41], v232 offset:1024
	ds_read_b128 v[14:17], v232 offset:2048
	ds_read_b128 v[34:37], v232 offset:3072
	ds_read_b128 v[8:11], v233
	ds_read_b128 v[30:33], v233 offset:1024
	ds_read_b128 v[2:5], v233 offset:2048
	ds_read_b128 v[26:29], v233 offset:3072
	ds_read_b128 v[42:45], v224 offset:32768
	ds_read_b128 v[46:49], v224 offset:33792
	ds_read_b128 v[182:185], v224 offset:34816
	ds_read_b128 v[198:201], v224 offset:35840
	ds_read_b128 v[188:191], v224 offset:36864
	ds_read_b128 v[202:205], v224 offset:37888
	ds_read_b128 v[194:197], v224 offset:38912
	ds_read_b128 v[206:209], v224 offset:39936
	s_mov_b32 m0, s70
	s_nop 0
	global_load_lds_dwordx4 v52, s[24:25]
	s_mov_b32 m0, s71
	s_nop 0
	global_load_lds_dwordx4 v53, s[24:25]
	s_waitcnt vmcnt(8)
	s_waitcnt lgkmcnt(0)
	s_barrier
; #define PG8_STAGEB(bufoff, gbase) PG8_STAGE2(bufoff, gbase, voffB[0], voffB[1])
; #define PG8_STAGEAS(bufoff, gbase, h) PG8_STAGE2(bufoff, gbase, voffA[h][0], voffA[h][1])
; #define PG8_LDA(dst, b, h) do { _Pragma("unroll") for (int m = 0; m < 4; ++m) _Pragma("unroll") for (int k = 0; k < 2; ++k) dst[m][k] = *(const LAS bf16x8*)(lds + PG8_SA(b, h) + aoff + m * 2048 + k * 1024); } while (0)
; #define PG8_WAIT_K() do { if constexpr (HM) PG8_WAIT_V(6); else PG8_WAIT_V(8); } while (0)
; #define PG8_WAIT_L(n) asm volatile("s_waitcnt lgkmcnt(" #n ")" ::: "memory")
; #define PG8_BAR __builtin_amdgcn_s_barrier()
; #define PG8_SCHED __builtin_amdgcn_sched_barrier(0)
;     ...
;             PG8_WAIT_K(); PG8_WAIT_L(0); PG8_BAR; PG8_MMA(0, 0, At, B0); PG8_MMA(0, 1, At, B1); PG8_BAR; PG8_SCHED;
;             if constexpr (!HM) PG8_LDA(At, 1, 1);
;             PG8_STAGEB(PG8_SB(1, 0), b3); PG8_STAGEB(PG8_SB(1, 1), b3 + hstepB); PG8_STAGEAS(PG8_SA(1, 0), a3, 0);
;             PG8_WAIT_K(); PG8_WAIT_L(0); PG8_BAR; if constexpr (!HM) { PG8_MMA(1, 0, At, B0); PG8_MMA(1, 1, At, B1); } PG8_BAR; PG8_SCHED;
	s_setprio 1
	v_mov_b32_e32 v24, v38
	v_mov_b32_e32 v25, v39
	s_nop 1
	v_mfma_scale_f32_16x16x128_f8f6f4 v[170:173], v[20:25], v[42:47], v[170:173], v40, v48 op_sel_hi:[0,0,0] cbsz:2 blgp:2
	v_mov_b32_e32 v18, v34
	v_mov_b32_e32 v19, v35
	s_nop 1
	v_mfma_scale_f32_16x16x128_f8f6f4 v[166:169], v[14:19], v[42:47], v[166:169], v36, v48 op_sel_hi:[0,0,0] cbsz:2 blgp:2
	v_mov_b32_e32 v186, v198
	v_mov_b32_e32 v187, v199
	s_nop 1
	v_mfma_scale_f32_16x16x128_f8f6f4 v[154:157], v[20:25], v[182:187], v[154:157], v40, v200 op_sel_hi:[0,0,0] cbsz:2 blgp:2
	s_nop 1
	v_mfma_scale_f32_16x16x128_f8f6f4 v[150:153], v[14:19], v[182:187], v[150:153], v36, v200 op_sel_hi:[0,0,0] cbsz:2 blgp:2
	v_mov_b32_e32 v192, v202
	v_mov_b32_e32 v193, v203
	s_nop 1
	v_mfma_scale_f32_16x16x128_f8f6f4 v[142:145], v[20:25], v[188:193], v[142:145], v40, v204 op_sel_hi:[0,0,0] cbsz:2 blgp:2
	s_nop 1
	v_mfma_scale_f32_16x16x128_f8f6f4 v[134:137], v[14:19], v[188:193], v[134:137], v36, v204 op_sel_hi:[0,0,0] cbsz:2 blgp:2
	v_mov_b32_e32 v198, v206
	v_mov_b32_e32 v199, v207
	s_nop 1
	v_mfma_scale_f32_16x16x128_f8f6f4 v[118:121], v[20:25], v[194:199], v[118:121], v40, v208 op_sel_hi:[0,0,0] cbsz:2 blgp:2
	s_nop 1
	v_mfma_scale_f32_16x16x128_f8f6f4 v[110:113], v[14:19], v[194:199], v[110:113], v36, v208 op_sel_hi:[0,0,0] cbsz:2 blgp:2
	v_mov_b32_e32 v12, v30
	v_mov_b32_e32 v13, v31
	s_nop 1
	v_mfma_scale_f32_16x16x128_f8f6f4 v[178:181], v[8:13], v[42:47], v[178:181], v32, v48 op_sel_hi:[0,0,0] cbsz:2 blgp:2
	v_mov_b32_e32 v6, v26
	v_mov_b32_e32 v7, v27
	s_nop 1
	v_mfma_scale_f32_16x16x128_f8f6f4 v[174:177], v[2:7], v[42:47], v[174:177], v28, v48 op_sel_hi:[0,0,0] cbsz:2 blgp:2
	s_nop 1
	v_mfma_scale_f32_16x16x128_f8f6f4 v[162:165], v[8:13], v[182:187], v[162:165], v32, v200 op_sel_hi:[0,0,0] cbsz:2 blgp:2
	s_nop 1
	v_mfma_scale_f32_16x16x128_f8f6f4 v[158:161], v[2:7], v[182:187], v[158:161], v28, v200 op_sel_hi:[0,0,0] cbsz:2 blgp:2
	s_nop 1
	v_mfma_scale_f32_16x16x128_f8f6f4 v[146:149], v[8:13], v[188:193], v[146:149], v32, v204 op_sel_hi:[0,0,0] cbsz:2 blgp:2
	s_nop 1
	v_mfma_scale_f32_16x16x128_f8f6f4 v[138:141], v[2:7], v[188:193], v[138:141], v28, v204 op_sel_hi:[0,0,0] cbsz:2 blgp:2
	s_nop 1
	v_mfma_scale_f32_16x16x128_f8f6f4 v[126:129], v[8:13], v[194:199], v[126:129], v32, v208 op_sel_hi:[0,0,0] cbsz:2 blgp:2
	s_nop 1
	v_mfma_scale_f32_16x16x128_f8f6f4 v[98:101], v[2:7], v[194:199], v[98:101], v28, v208 op_sel_hi:[0,0,0] cbsz:2 blgp:2
	s_setprio 0
	s_barrier
	ds_read_b128 v[42:45], v224 offset:49152
	ds_read_b128 v[46:49], v224 offset:50176
	ds_read_b128 v[182:185], v224 offset:51200
	ds_read_b128 v[198:201], v224 offset:52224
	ds_read_b128 v[188:191], v224 offset:53248
	ds_read_b128 v[202:205], v224 offset:54272
	ds_read_b128 v[194:197], v224 offset:55296
	ds_read_b128 v[206:209], v224 offset:56320
	s_mov_b32 m0, s72
	s_nop 0
	global_load_lds_dwordx4 v217, s[50:51]
	s_add_u32 s18, s48, 0x40180
	s_mov_b32 m0, s73
	s_nop 0
	global_load_lds_dwordx4 v218, s[50:51]
	s_addc_u32 s19, s49, 0
	s_mov_b32 m0, s76
	s_nop 0
	global_load_lds_dwordx4 v217, s[18:19]
	s_mov_b32 m0, s77
	s_nop 0
	global_load_lds_dwordx4 v218, s[18:19]
	s_mov_b32 m0, s74
	s_nop 0
	global_load_lds_dwordx4 v50, s[26:27]
	s_mov_b32 m0, s75
	s_nop 0
	global_load_lds_dwordx4 v51, s[26:27]
	s_waitcnt vmcnt(8)
	s_waitcnt lgkmcnt(0)
	s_barrier
	s_setprio 1
	s_nop 1
	v_mfma_scale_f32_16x16x128_f8f6f4 v[114:117], v[20:25], v[42:47], v[114:117], v40, v48 op_sel_hi:[0,0,0] cbsz:2 blgp:2
	s_nop 1
	v_mfma_scale_f32_16x16x128_f8f6f4 v[106:109], v[14:19], v[42:47], v[106:109], v36, v48 op_sel_hi:[0,0,0] cbsz:2 blgp:2
	v_mov_b32_e32 v186, v198
	v_mov_b32_e32 v187, v199
	s_nop 1
	v_mfma_scale_f32_16x16x128_f8f6f4 v[94:97], v[20:25], v[182:187], v[94:97], v40, v200 op_sel_hi:[0,0,0] cbsz:2 blgp:2
	s_nop 1
	v_mfma_scale_f32_16x16x128_f8f6f4 v[86:89], v[14:19], v[182:187], v[86:89], v36, v200 op_sel_hi:[0,0,0] cbsz:2 blgp:2
	v_mov_b32_e32 v192, v202
	v_mov_b32_e32 v193, v203
	s_nop 1
	v_mfma_scale_f32_16x16x128_f8f6f4 v[78:81], v[20:25], v[188:193], v[78:81], v40, v204 op_sel_hi:[0,0,0] cbsz:2 blgp:2
	s_nop 1
	v_mfma_scale_f32_16x16x128_f8f6f4 v[70:73], v[14:19], v[188:193], v[70:73], v36, v204 op_sel_hi:[0,0,0] cbsz:2 blgp:2
	v_mov_b32_e32 v198, v206
	v_mov_b32_e32 v199, v207
	s_nop 1
	v_mfma_scale_f32_16x16x128_f8f6f4 v[62:65], v[20:25], v[194:199], v[62:65], v40, v208 op_sel_hi:[0,0,0] cbsz:2 blgp:2
	s_nop 1
	v_mfma_scale_f32_16x16x128_f8f6f4 v[58:61], v[14:19], v[194:199], v[58:61], v36, v208 op_sel_hi:[0,0,0] cbsz:2 blgp:2
	s_nop 1
	v_mfma_scale_f32_16x16x128_f8f6f4 v[130:133], v[8:13], v[42:47], v[130:133], v32, v48 op_sel_hi:[0,0,0] cbsz:2 blgp:2
	s_nop 1
	v_mfma_scale_f32_16x16x128_f8f6f4 v[122:125], v[2:7], v[42:47], v[122:125], v28, v48 op_sel_hi:[0,0,0] cbsz:2 blgp:2
	s_nop 1
	v_mfma_scale_f32_16x16x128_f8f6f4 v[102:105], v[8:13], v[182:187], v[102:105], v32, v200 op_sel_hi:[0,0,0] cbsz:2 blgp:2
	s_nop 1
	v_mfma_scale_f32_16x16x128_f8f6f4 v[90:93], v[2:7], v[182:187], v[90:93], v28, v200 op_sel_hi:[0,0,0] cbsz:2 blgp:2
	s_nop 1
	v_mfma_scale_f32_16x16x128_f8f6f4 v[82:85], v[8:13], v[188:193], v[82:85], v32, v204 op_sel_hi:[0,0,0] cbsz:2 blgp:2
	s_nop 1
	v_mfma_scale_f32_16x16x128_f8f6f4 v[74:77], v[2:7], v[188:193], v[74:77], v28, v204 op_sel_hi:[0,0,0] cbsz:2 blgp:2
	s_nop 1
	v_mfma_scale_f32_16x16x128_f8f6f4 v[66:69], v[8:13], v[194:199], v[66:69], v32, v208 op_sel_hi:[0,0,0] cbsz:2 blgp:2
	s_nop 1
	v_mfma_scale_f32_16x16x128_f8f6f4 v[54:57], v[2:7], v[194:199], v[54:57], v28, v208 op_sel_hi:[0,0,0] cbsz:2 blgp:2
	s_setprio 0
	s_barrier
	s_mov_b64 s[18:19], 0x200
	s_xor_b64 s[50:51], s[10:11], -1
	s_branch .LBB0_1136
; #define LAS __attribute__((address_space(3)))
; #define PG8_STAGEB(bufoff, gbase) PG8_STAGE2(bufoff, gbase, voffB[0], voffB[1])
; #define PG8_STAGEA(bufoff, gbase, h) PG8_STAGE2(bufoff, gbase, voffA[h][0], voffA[h][1])
; #define PG8_STAGEAS(bufoff, gbase, h) PG8_STAGE2(bufoff, gbase, voffA[h][0], voffA[h][1])
; #define PG8_LDA(dst, b, h) do { _Pragma("unroll") for (int m = 0; m < 4; ++m) _Pragma("unroll") for (int k = 0; k < 2; ++k) dst[m][k] = *(const LAS bf16x8*)(lds + PG8_SA(b, h) + aoff + m * 2048 + k * 1024); } while (0)
; #define PG8_LDB(dst, b, h) do { _Pragma("unroll") for (int n = 0; n < 2; ++n) _Pragma("unroll") for (int k = 0; k < 2; ++k) dst[n][k] = *(const LAS bf16x8*)(lds + PG8_SB(b, h) + boff + n * 2048 + k * 1024); } while (0)
; #define PG8_WAIT_K0() do { if (EST > 0 && t == 0 && ui > 0) asm volatile("s_waitcnt vmcnt(%0)" :: "n"((HM ? 6 : 8) + EST) : "memory"); else PG8_WAIT_K(); } while (0)
; #define PG8_WAIT_L(n) asm volatile("s_waitcnt lgkmcnt(" #n ")" ::: "memory")
; #define PG8_BAR __builtin_amdgcn_s_barrier()
; #define PG8_SCHED __builtin_amdgcn_sched_barrier(0)
;     ...
;             const char* a1 = cA + (size_t)(t + 1) * kstep;
;             const char* a2 = last ? nA : cA + (size_t)(t + 2) * kstep; const char* b2 = last ? nB : cB + (size_t)(t + 2) * kstep;
;             const char* a3 = a2 + kstep; const char* b3 = b2 + kstep;
;             PG8_LDB(B0, 0, 0); PG8_LDB(B1, 0, 1); PG8_SCHED; PG8_LDA(At, 0, 0); if constexpr (!HM) PG8_STAGEA(PG8_SA(1, 1), a1, 1);
;             if constexpr (Sched::kGather) { if (last && has_next) { const u32x4 tn = *(const LAS u32x4*)(S.aux + tid * 16); voffA[0][0] = tn.x; voffA[0][1] = tn.y; voffA[1][0] = tn.z; voffA[1][1] = tn.w; } }
;             PG8_WAIT_K0(); PG8_WAIT_L(0); PG8_BAR; PG8_MMA(0, 0, At, B0); PG8_MMA(0, 1, At, B1); PG8_BAR; PG8_SCHED;
;             if constexpr (!HM) PG8_LDA(At, 0, 1);
;             PG8_STAGEB(PG8_SB(0, 0), b2); PG8_STAGEB(PG8_SB(0, 1), b2 + hstepB); PG8_STAGEAS(PG8_SA(0, 0), a2, 0);
;             PG8_WAIT_K0(); PG8_WAIT_L(0); PG8_BAR; if constexpr (!HM) { PG8_MMA(1, 0, At, B0); PG8_MMA(1, 1, At, B1); } PG8_BAR; PG8_SCHED;
.LBB0_1135:
	s_and_b64 s[52:53], s[54:55], exec
	s_cselect_b32 s41, 0, s18
	s_cselect_b32 s17, 0, s19
	s_add_u32 s58, s0, s41
	s_addc_u32 s59, s1, s17
	s_add_u32 s17, s48, s18
	s_addc_u32 s41, s49, s19
	s_add_u32 s52, s58, 0x80
	s_addc_u32 s53, s59, 0
	s_waitcnt vmcnt(8)
	s_and_b64 s[54:55], s[54:55], exec
	s_waitcnt lgkmcnt(0)
	s_cselect_b32 s54, s44, s17
	s_cselect_b32 s55, s45, s41
	s_add_u32 s56, s54, 0x80
	s_addc_u32 s57, s55, 0
	s_barrier
	s_setprio 1
	v_mov_b32_e32 v48, v210
	v_mov_b32_e32 v49, v211
	v_mov_b32_e32 v24, v194
	v_mov_b32_e32 v25, v195
	s_nop 1
	v_mfma_scale_f32_16x16x128_f8f6f4 v[170:173], v[20:25], v[44:49], v[170:173], v196, v212 op_sel_hi:[0,0,0] cbsz:2 blgp:2
	v_mov_b32_e32 v18, v190
	v_mov_b32_e32 v19, v191
	s_nop 1
	v_mfma_scale_f32_16x16x128_f8f6f4 v[166:169], v[14:19], v[44:49], v[166:169], v192, v212 op_sel_hi:[0,0,0] cbsz:2 blgp:2
	v_mov_b32_e32 v42, v206
	v_mov_b32_e32 v43, v207
	s_nop 1
	v_mfma_scale_f32_16x16x128_f8f6f4 v[154:157], v[20:25], v[38:43], v[154:157], v196, v208 op_sel_hi:[0,0,0] cbsz:2 blgp:2
	s_nop 1
	v_mfma_scale_f32_16x16x128_f8f6f4 v[150:153], v[14:19], v[38:43], v[150:153], v192, v208 op_sel_hi:[0,0,0] cbsz:2 blgp:2
	v_mov_b32_e32 v36, v202
	v_mov_b32_e32 v37, v203
	s_nop 1
	v_mfma_scale_f32_16x16x128_f8f6f4 v[142:145], v[20:25], v[32:37], v[142:145], v196, v204 op_sel_hi:[0,0,0] cbsz:2 blgp:2
	s_nop 1
	v_mfma_scale_f32_16x16x128_f8f6f4 v[134:137], v[14:19], v[32:37], v[134:137], v192, v204 op_sel_hi:[0,0,0] cbsz:2 blgp:2
	v_mov_b32_e32 v30, v198
	v_mov_b32_e32 v31, v199
	s_nop 1
	v_mfma_scale_f32_16x16x128_f8f6f4 v[118:121], v[20:25], v[26:31], v[118:121], v196, v200 op_sel_hi:[0,0,0] cbsz:2 blgp:2
	s_nop 1
	v_mfma_scale_f32_16x16x128_f8f6f4 v[110:113], v[14:19], v[26:31], v[110:113], v192, v200 op_sel_hi:[0,0,0] cbsz:2 blgp:2
	v_mov_b32_e32 v12, v182
	v_mov_b32_e32 v13, v183
	s_nop 1
	v_mfma_scale_f32_16x16x128_f8f6f4 v[178:181], v[8:13], v[44:49], v[178:181], v184, v212 op_sel_hi:[0,0,0] cbsz:2 blgp:2
	v_mov_b32_e32 v6, v186
	v_mov_b32_e32 v7, v187
	s_nop 1
	v_mfma_scale_f32_16x16x128_f8f6f4 v[174:177], v[2:7], v[44:49], v[174:177], v188, v212 op_sel_hi:[0,0,0] cbsz:2 blgp:2
	s_nop 1
	v_mfma_scale_f32_16x16x128_f8f6f4 v[162:165], v[8:13], v[38:43], v[162:165], v184, v208 op_sel_hi:[0,0,0] cbsz:2 blgp:2
	s_nop 1
	v_mfma_scale_f32_16x16x128_f8f6f4 v[158:161], v[2:7], v[38:43], v[158:161], v188, v208 op_sel_hi:[0,0,0] cbsz:2 blgp:2
	s_nop 1
	v_mfma_scale_f32_16x16x128_f8f6f4 v[146:149], v[8:13], v[32:37], v[146:149], v184, v204 op_sel_hi:[0,0,0] cbsz:2 blgp:2
	s_nop 1
	v_mfma_scale_f32_16x16x128_f8f6f4 v[138:141], v[2:7], v[32:37], v[138:141], v188, v204 op_sel_hi:[0,0,0] cbsz:2 blgp:2
	s_nop 1
	v_mfma_scale_f32_16x16x128_f8f6f4 v[126:129], v[8:13], v[26:31], v[126:129], v184, v200 op_sel_hi:[0,0,0] cbsz:2 blgp:2
	s_nop 1
	v_mfma_scale_f32_16x16x128_f8f6f4 v[98:101], v[2:7], v[26:31], v[98:101], v188, v200 op_sel_hi:[0,0,0] cbsz:2 blgp:2
	s_setprio 0
	s_barrier
	ds_read_b128 v[26:29], v224 offset:16384
	ds_read_b128 v[198:201], v224 offset:17408
	ds_read_b128 v[32:35], v224 offset:18432
	ds_read_b128 v[202:205], v224 offset:19456
	ds_read_b128 v[38:41], v224 offset:20480
	ds_read_b128 v[206:209], v224 offset:21504
	ds_read_b128 v[44:47], v224 offset:22528
	ds_read_b128 v[210:213], v224 offset:23552
	s_mov_b32 m0, s47
	s_nop 0
	global_load_lds_dwordx4 v217, s[54:55]
	s_add_u32 s86, s54, 0x40000
	s_mov_b32 m0, s66
	s_nop 0
	global_load_lds_dwordx4 v218, s[54:55]
	s_addc_u32 s87, s55, 0
	s_mov_b32 m0, s67
	s_nop 0
	global_load_lds_dwordx4 v217, s[86:87]
	s_mov_b32 m0, s68
	s_nop 0
	global_load_lds_dwordx4 v218, s[86:87]
	s_mov_b32 m0, s35
	s_nop 0
	global_load_lds_dwordx4 v50, s[58:59]
	s_mov_b32 m0, s69
	s_nop 0
	global_load_lds_dwordx4 v51, s[58:59]
	s_waitcnt vmcnt(8)
	s_waitcnt lgkmcnt(0)
	s_barrier
	s_setprio 1
	v_mov_b32_e32 v30, v198
	v_mov_b32_e32 v31, v199
	s_nop 1
	v_mfma_scale_f32_16x16x128_f8f6f4 v[114:117], v[20:25], v[26:31], v[114:117], v196, v200 op_sel_hi:[0,0,0] cbsz:2 blgp:2
	s_nop 1
	v_mfma_scale_f32_16x16x128_f8f6f4 v[106:109], v[14:19], v[26:31], v[106:109], v192, v200 op_sel_hi:[0,0,0] cbsz:2 blgp:2
	v_mov_b32_e32 v36, v202
	v_mov_b32_e32 v37, v203
	s_nop 1
	v_mfma_scale_f32_16x16x128_f8f6f4 v[94:97], v[20:25], v[32:37], v[94:97], v196, v204 op_sel_hi:[0,0,0] cbsz:2 blgp:2
	s_nop 1
	v_mfma_scale_f32_16x16x128_f8f6f4 v[86:89], v[14:19], v[32:37], v[86:89], v192, v204 op_sel_hi:[0,0,0] cbsz:2 blgp:2
	v_mov_b32_e32 v42, v206
	v_mov_b32_e32 v43, v207
	s_nop 1
	v_mfma_scale_f32_16x16x128_f8f6f4 v[78:81], v[20:25], v[38:43], v[78:81], v196, v208 op_sel_hi:[0,0,0] cbsz:2 blgp:2
	s_nop 1
	v_mfma_scale_f32_16x16x128_f8f6f4 v[70:73], v[14:19], v[38:43], v[70:73], v192, v208 op_sel_hi:[0,0,0] cbsz:2 blgp:2
	v_mov_b32_e32 v48, v210
	v_mov_b32_e32 v49, v211
	s_nop 1
	v_mfma_scale_f32_16x16x128_f8f6f4 v[62:65], v[20:25], v[44:49], v[62:65], v196, v212 op_sel_hi:[0,0,0] cbsz:2 blgp:2
	s_nop 1
	v_mfma_scale_f32_16x16x128_f8f6f4 v[58:61], v[14:19], v[44:49], v[58:61], v192, v212 op_sel_hi:[0,0,0] cbsz:2 blgp:2
	s_nop 1
	v_mfma_scale_f32_16x16x128_f8f6f4 v[130:133], v[8:13], v[26:31], v[130:133], v184, v200 op_sel_hi:[0,0,0] cbsz:2 blgp:2
	s_nop 1
	v_mfma_scale_f32_16x16x128_f8f6f4 v[122:125], v[2:7], v[26:31], v[122:125], v188, v200 op_sel_hi:[0,0,0] cbsz:2 blgp:2
	s_nop 1
	v_mfma_scale_f32_16x16x128_f8f6f4 v[102:105], v[8:13], v[32:37], v[102:105], v184, v204 op_sel_hi:[0,0,0] cbsz:2 blgp:2
	s_nop 1
	v_mfma_scale_f32_16x16x128_f8f6f4 v[90:93], v[2:7], v[32:37], v[90:93], v188, v204 op_sel_hi:[0,0,0] cbsz:2 blgp:2
	s_nop 1
	v_mfma_scale_f32_16x16x128_f8f6f4 v[82:85], v[8:13], v[38:43], v[82:85], v184, v208 op_sel_hi:[0,0,0] cbsz:2 blgp:2
	s_nop 1
	v_mfma_scale_f32_16x16x128_f8f6f4 v[74:77], v[2:7], v[38:43], v[74:77], v188, v208 op_sel_hi:[0,0,0] cbsz:2 blgp:2
	s_nop 1
	v_mfma_scale_f32_16x16x128_f8f6f4 v[66:69], v[8:13], v[44:49], v[66:69], v184, v212 op_sel_hi:[0,0,0] cbsz:2 blgp:2
	s_nop 1
	v_mfma_scale_f32_16x16x128_f8f6f4 v[54:57], v[2:7], v[44:49], v[54:57], v188, v212 op_sel_hi:[0,0,0] cbsz:2 blgp:2
	s_setprio 0
	s_barrier
; #define PG8_STAGEB(bufoff, gbase) PG8_STAGE2(bufoff, gbase, voffB[0], voffB[1])
; #define PG8_STAGEAS(bufoff, gbase, h) PG8_STAGE2(bufoff, gbase, voffA[h][0], voffA[h][1])
; #define PG8_LDA(dst, b, h) do { _Pragma("unroll") for (int m = 0; m < 4; ++m) _Pragma("unroll") for (int k = 0; k < 2; ++k) dst[m][k] = *(const LAS bf16x8*)(lds + PG8_SA(b, h) + aoff + m * 2048 + k * 1024); } while (0)
; #define PG8_LDB(dst, b, h) do { _Pragma("unroll") for (int n = 0; n < 2; ++n) _Pragma("unroll") for (int k = 0; k < 2; ++k) dst[n][k] = *(const LAS bf16x8*)(lds + PG8_SB(b, h) + boff + n * 2048 + k * 1024); } while (0)
; #define PG8_WAIT_K() do { if constexpr (HM) PG8_WAIT_V(6); else PG8_WAIT_V(8); } while (0)
; #define PG8_WAIT_L(n) asm volatile("s_waitcnt lgkmcnt(" #n ")" ::: "memory")
; #define PG8_BAR __builtin_amdgcn_s_barrier()
; #define PG8_SCHED __builtin_amdgcn_sched_barrier(0)
;     ...
;             PG8_LDB(B0, 1, 0); PG8_LDB(B1, 1, 1); PG8_SCHED; PG8_LDA(At, 1, 0); if constexpr (!HM) PG8_STAGEAS(PG8_SA(0, 1), a2, 1);
;             PG8_WAIT_K(); PG8_WAIT_L(0); PG8_BAR; PG8_MMA(0, 0, At, B0); PG8_MMA(0, 1, At, B1); PG8_BAR; PG8_SCHED;
;             if constexpr (!HM) PG8_LDA(At, 1, 1);
;             PG8_STAGEB(PG8_SB(1, 0), b3); PG8_STAGEB(PG8_SB(1, 1), b3 + hstepB); PG8_STAGEAS(PG8_SA(1, 0), a3, 0);
;             PG8_WAIT_K(); PG8_WAIT_L(0); PG8_BAR; if constexpr (!HM) { PG8_MMA(1, 0, At, B0); PG8_MMA(1, 1, At, B1); } PG8_BAR; PG8_SCHED;
;         }
	ds_read_b128 v[20:23], v232
	ds_read_b128 v[38:41], v232 offset:1024
	ds_read_b128 v[14:17], v232 offset:2048
	ds_read_b128 v[34:37], v232 offset:3072
	ds_read_b128 v[8:11], v233
	ds_read_b128 v[30:33], v233 offset:1024
	ds_read_b128 v[2:5], v233 offset:2048
	ds_read_b128 v[26:29], v233 offset:3072
	ds_read_b128 v[42:45], v224 offset:32768
	ds_read_b128 v[46:49], v224 offset:33792
	ds_read_b128 v[182:185], v224 offset:34816
	ds_read_b128 v[198:201], v224 offset:35840
	ds_read_b128 v[188:191], v224 offset:36864
	ds_read_b128 v[202:205], v224 offset:37888
	ds_read_b128 v[194:197], v224 offset:38912
	ds_read_b128 v[206:209], v224 offset:39936
	s_mov_b32 m0, s70
	s_nop 0
	global_load_lds_dwordx4 v52, s[58:59]
	s_mov_b32 m0, s71
	s_nop 0
	global_load_lds_dwordx4 v53, s[58:59]
	s_waitcnt vmcnt(8)
	s_waitcnt lgkmcnt(0)
	s_barrier
	s_setprio 1
	v_mov_b32_e32 v24, v38
	v_mov_b32_e32 v25, v39
	s_nop 1
	v_mfma_scale_f32_16x16x128_f8f6f4 v[170:173], v[20:25], v[42:47], v[170:173], v40, v48 op_sel_hi:[0,0,0] cbsz:2 blgp:2
	v_mov_b32_e32 v18, v34
	v_mov_b32_e32 v19, v35
	s_nop 1
	v_mfma_scale_f32_16x16x128_f8f6f4 v[166:169], v[14:19], v[42:47], v[166:169], v36, v48 op_sel_hi:[0,0,0] cbsz:2 blgp:2
	v_mov_b32_e32 v186, v198
	v_mov_b32_e32 v187, v199
	s_nop 1
	v_mfma_scale_f32_16x16x128_f8f6f4 v[154:157], v[20:25], v[182:187], v[154:157], v40, v200 op_sel_hi:[0,0,0] cbsz:2 blgp:2
	s_nop 1
	v_mfma_scale_f32_16x16x128_f8f6f4 v[150:153], v[14:19], v[182:187], v[150:153], v36, v200 op_sel_hi:[0,0,0] cbsz:2 blgp:2
	v_mov_b32_e32 v192, v202
	v_mov_b32_e32 v193, v203
	s_nop 1
	v_mfma_scale_f32_16x16x128_f8f6f4 v[142:145], v[20:25], v[188:193], v[142:145], v40, v204 op_sel_hi:[0,0,0] cbsz:2 blgp:2
	s_nop 1
	v_mfma_scale_f32_16x16x128_f8f6f4 v[134:137], v[14:19], v[188:193], v[134:137], v36, v204 op_sel_hi:[0,0,0] cbsz:2 blgp:2
	v_mov_b32_e32 v198, v206
	v_mov_b32_e32 v199, v207
	s_nop 1
	v_mfma_scale_f32_16x16x128_f8f6f4 v[118:121], v[20:25], v[194:199], v[118:121], v40, v208 op_sel_hi:[0,0,0] cbsz:2 blgp:2
	s_nop 1
	v_mfma_scale_f32_16x16x128_f8f6f4 v[110:113], v[14:19], v[194:199], v[110:113], v36, v208 op_sel_hi:[0,0,0] cbsz:2 blgp:2
	v_mov_b32_e32 v12, v30
	v_mov_b32_e32 v13, v31
	s_nop 1
	v_mfma_scale_f32_16x16x128_f8f6f4 v[178:181], v[8:13], v[42:47], v[178:181], v32, v48 op_sel_hi:[0,0,0] cbsz:2 blgp:2
	v_mov_b32_e32 v6, v26
	v_mov_b32_e32 v7, v27
	s_nop 1
	v_mfma_scale_f32_16x16x128_f8f6f4 v[174:177], v[2:7], v[42:47], v[174:177], v28, v48 op_sel_hi:[0,0,0] cbsz:2 blgp:2
	s_nop 1
	v_mfma_scale_f32_16x16x128_f8f6f4 v[162:165], v[8:13], v[182:187], v[162:165], v32, v200 op_sel_hi:[0,0,0] cbsz:2 blgp:2
	s_nop 1
	v_mfma_scale_f32_16x16x128_f8f6f4 v[158:161], v[2:7], v[182:187], v[158:161], v28, v200 op_sel_hi:[0,0,0] cbsz:2 blgp:2
	s_nop 1
	v_mfma_scale_f32_16x16x128_f8f6f4 v[146:149], v[8:13], v[188:193], v[146:149], v32, v204 op_sel_hi:[0,0,0] cbsz:2 blgp:2
	s_nop 1
	v_mfma_scale_f32_16x16x128_f8f6f4 v[138:141], v[2:7], v[188:193], v[138:141], v28, v204 op_sel_hi:[0,0,0] cbsz:2 blgp:2
	s_nop 1
	v_mfma_scale_f32_16x16x128_f8f6f4 v[126:129], v[8:13], v[194:199], v[126:129], v32, v208 op_sel_hi:[0,0,0] cbsz:2 blgp:2
	s_nop 1
	v_mfma_scale_f32_16x16x128_f8f6f4 v[98:101], v[2:7], v[194:199], v[98:101], v28, v208 op_sel_hi:[0,0,0] cbsz:2 blgp:2
	s_setprio 0
	s_barrier
	ds_read_b128 v[42:45], v224 offset:49152
	ds_read_b128 v[46:49], v224 offset:50176
	ds_read_b128 v[182:185], v224 offset:51200
	ds_read_b128 v[198:201], v224 offset:52224
	ds_read_b128 v[188:191], v224 offset:53248
	ds_read_b128 v[202:205], v224 offset:54272
	ds_read_b128 v[194:197], v224 offset:55296
	ds_read_b128 v[206:209], v224 offset:56320
	s_mov_b32 m0, s72
	s_nop 0
	global_load_lds_dwordx4 v217, s[56:57]
	s_add_u32 s54, s54, 0x40080
	s_mov_b32 m0, s73
	s_nop 0
	global_load_lds_dwordx4 v218, s[56:57]
	s_addc_u32 s55, s55, 0
	s_mov_b32 m0, s76
	s_nop 0
	global_load_lds_dwordx4 v217, s[54:55]
	s_mov_b32 m0, s77
	s_nop 0
	global_load_lds_dwordx4 v218, s[54:55]
	s_mov_b32 m0, s74
	s_nop 0
	global_load_lds_dwordx4 v50, s[52:53]
	s_mov_b32 m0, s75
	s_nop 0
	global_load_lds_dwordx4 v51, s[52:53]
	s_waitcnt vmcnt(8)
	s_waitcnt lgkmcnt(0)
	s_barrier
	s_setprio 1
	s_nop 1
	v_mfma_scale_f32_16x16x128_f8f6f4 v[114:117], v[20:25], v[42:47], v[114:117], v40, v48 op_sel_hi:[0,0,0] cbsz:2 blgp:2
	s_nop 1
	v_mfma_scale_f32_16x16x128_f8f6f4 v[106:109], v[14:19], v[42:47], v[106:109], v36, v48 op_sel_hi:[0,0,0] cbsz:2 blgp:2
	v_mov_b32_e32 v186, v198
	v_mov_b32_e32 v187, v199
	s_nop 1
	v_mfma_scale_f32_16x16x128_f8f6f4 v[94:97], v[20:25], v[182:187], v[94:97], v40, v200 op_sel_hi:[0,0,0] cbsz:2 blgp:2
	s_nop 1
	v_mfma_scale_f32_16x16x128_f8f6f4 v[86:89], v[14:19], v[182:187], v[86:89], v36, v200 op_sel_hi:[0,0,0] cbsz:2 blgp:2
	v_mov_b32_e32 v192, v202
	v_mov_b32_e32 v193, v203
	s_nop 1
	v_mfma_scale_f32_16x16x128_f8f6f4 v[78:81], v[20:25], v[188:193], v[78:81], v40, v204 op_sel_hi:[0,0,0] cbsz:2 blgp:2
	s_nop 1
	v_mfma_scale_f32_16x16x128_f8f6f4 v[70:73], v[14:19], v[188:193], v[70:73], v36, v204 op_sel_hi:[0,0,0] cbsz:2 blgp:2
	v_mov_b32_e32 v198, v206
	v_mov_b32_e32 v199, v207
	s_nop 1
	v_mfma_scale_f32_16x16x128_f8f6f4 v[62:65], v[20:25], v[194:199], v[62:65], v40, v208 op_sel_hi:[0,0,0] cbsz:2 blgp:2
	s_nop 1
	v_mfma_scale_f32_16x16x128_f8f6f4 v[58:61], v[14:19], v[194:199], v[58:61], v36, v208 op_sel_hi:[0,0,0] cbsz:2 blgp:2
	s_nop 1
	v_mfma_scale_f32_16x16x128_f8f6f4 v[130:133], v[8:13], v[42:47], v[130:133], v32, v48 op_sel_hi:[0,0,0] cbsz:2 blgp:2
	s_nop 1
	v_mfma_scale_f32_16x16x128_f8f6f4 v[122:125], v[2:7], v[42:47], v[122:125], v28, v48 op_sel_hi:[0,0,0] cbsz:2 blgp:2
	s_nop 1
	v_mfma_scale_f32_16x16x128_f8f6f4 v[102:105], v[8:13], v[182:187], v[102:105], v32, v200 op_sel_hi:[0,0,0] cbsz:2 blgp:2
	s_nop 1
	v_mfma_scale_f32_16x16x128_f8f6f4 v[90:93], v[2:7], v[182:187], v[90:93], v28, v200 op_sel_hi:[0,0,0] cbsz:2 blgp:2
	s_nop 1
	v_mfma_scale_f32_16x16x128_f8f6f4 v[82:85], v[8:13], v[188:193], v[82:85], v32, v204 op_sel_hi:[0,0,0] cbsz:2 blgp:2
	s_nop 1
	v_mfma_scale_f32_16x16x128_f8f6f4 v[74:77], v[2:7], v[188:193], v[74:77], v28, v204 op_sel_hi:[0,0,0] cbsz:2 blgp:2
	s_nop 1
	v_mfma_scale_f32_16x16x128_f8f6f4 v[66:69], v[8:13], v[194:199], v[66:69], v32, v208 op_sel_hi:[0,0,0] cbsz:2 blgp:2
	s_nop 1
	v_mfma_scale_f32_16x16x128_f8f6f4 v[54:57], v[2:7], v[194:199], v[54:57], v28, v208 op_sel_hi:[0,0,0] cbsz:2 blgp:2
	s_setprio 0
	s_barrier
	s_add_i32 s16, s16, 2
	s_add_u32 s18, s18, 0x100
	s_addc_u32 s19, s19, 0
	s_cmp_gt_u32 s16, 13
	s_cbranch_scc1 .LBB0_1140

; #define PG8_STAGEB(bufoff, gbase) PG8_STAGE2(bufoff, gbase, voffB[0], voffB[1])
; #define PG8_STAGEAS(bufoff, gbase, h) PG8_STAGE2(bufoff, gbase, voffA[h][0], voffA[h][1])
; #define PG8_LDA(dst, b, h) do { _Pragma("unroll") for (int m = 0; m < 4; ++m) _Pragma("unroll") for (int k = 0; k < 2; ++k) dst[m][k] = *(const LAS bf16x8*)(lds + PG8_SA(b, h) + aoff + m * 2048 + k * 1024); } while (0)
; #define PG8_WAIT_K0() do { if (EST > 0 && t == 0 && ui > 0) asm volatile("s_waitcnt vmcnt(%0)" :: "n"((HM ? 6 : 8) + EST) : "memory"); else PG8_WAIT_K(); } while (0)
; #define PG8_WAIT_L(n) asm volatile("s_waitcnt lgkmcnt(" #n ")" ::: "memory")
; #define PG8_BAR __builtin_amdgcn_s_barrier()
; #define PG8_SCHED __builtin_amdgcn_sched_barrier(0)
;     ...
;             PG8_WAIT_K0(); PG8_WAIT_L(0); PG8_BAR; PG8_MMA(0, 0, At, B0); PG8_MMA(0, 1, At, B1); PG8_BAR; PG8_SCHED;
;             if constexpr (!HM) PG8_LDA(At, 0, 1);
;             PG8_STAGEB(PG8_SB(0, 0), b2); PG8_STAGEB(PG8_SB(0, 1), b2 + hstepB); PG8_STAGEAS(PG8_SA(0, 0), a2, 0);
;             PG8_WAIT_K0(); PG8_WAIT_L(0); PG8_BAR; if constexpr (!HM) { PG8_MMA(1, 0, At, B0); PG8_MMA(1, 1, At, B1); } PG8_BAR; PG8_SCHED;
.LBB0_1181:
	s_waitcnt lgkmcnt(0)
	s_add_u32 s50, s46, 0x100
	s_addc_u32 s51, s47, 0
	s_barrier
	s_setprio 1
	v_mov_b32_e32 v36, v80
	v_mov_b32_e32 v37, v81
	v_mov_b64_e32 v[108:109], s[14:15]
	v_mov_b32_e32 v42, v92
	v_mov_b32_e32 v43, v93
	v_mov_b64_e32 v[104:105], s[14:15]
	v_mov_b32_e32 v30, v72
	v_mov_b32_e32 v31, v73
	v_mov_b64_e32 v[92:93], s[14:15]
	v_mov_b64_e32 v[88:89], s[14:15]
	v_mov_b32_e32 v24, v64
	v_mov_b32_e32 v25, v65
	v_mov_b64_e32 v[80:81], s[14:15]
	v_mov_b64_e32 v[72:73], s[14:15]
	v_mov_b64_e32 v[64:65], s[14:15]
	v_mov_b64_e32 v[106:107], s[12:13]
	v_mov_b64_e32 v[102:103], s[12:13]
	v_mov_b64_e32 v[90:91], s[12:13]
	v_mov_b64_e32 v[86:87], s[12:13]
	v_mov_b64_e32 v[78:79], s[12:13]
	v_mov_b64_e32 v[70:71], s[12:13]
	v_mov_b64_e32 v[62:63], s[12:13]
	v_mov_b32_e32 v48, v56
	v_mov_b32_e32 v49, v57
	v_mov_b64_e32 v[56:57], s[14:15]
	s_nop 1
	v_mfma_scale_f32_16x16x128_f8f6f4 v[106:109], v[44:49], v[32:37], v[106:109], v58, v82 op_sel_hi:[0,0,0] cbsz:2 blgp:2
	s_nop 1
	v_mfma_scale_f32_16x16x128_f8f6f4 v[102:105], v[38:43], v[32:37], v[102:105], v94, v82 op_sel_hi:[0,0,0] cbsz:2 blgp:2
	s_nop 1
	v_mfma_scale_f32_16x16x128_f8f6f4 v[90:93], v[44:49], v[26:31], v[90:93], v58, v74 op_sel_hi:[0,0,0] cbsz:2 blgp:2
	s_nop 1
	v_mfma_scale_f32_16x16x128_f8f6f4 v[86:89], v[38:43], v[26:31], v[86:89], v94, v74 op_sel_hi:[0,0,0] cbsz:2 blgp:2
	s_nop 1
	v_mfma_scale_f32_16x16x128_f8f6f4 v[78:81], v[44:49], v[20:25], v[78:81], v58, v66 op_sel_hi:[0,0,0] cbsz:2 blgp:2
	s_nop 1
	v_mfma_scale_f32_16x16x128_f8f6f4 v[70:73], v[38:43], v[20:25], v[70:73], v94, v66 op_sel_hi:[0,0,0] cbsz:2 blgp:2
	v_mov_b32_e32 v18, v126
	v_mov_b32_e32 v19, v127
	s_nop 1
	v_mfma_scale_f32_16x16x128_f8f6f4 v[62:65], v[44:49], v[14:19], v[62:65], v58, v128 op_sel_hi:[0,0,0] cbsz:2 blgp:2
	v_mov_b64_e32 v[60:61], s[14:15]
	v_mov_b64_e32 v[54:55], s[12:13]
	v_mov_b64_e32 v[58:59], s[12:13]
	s_nop 1
	v_mfma_scale_f32_16x16x128_f8f6f4 v[58:61], v[38:43], v[14:19], v[58:61], v94, v128 op_sel_hi:[0,0,0] cbsz:2 blgp:2
	v_mov_b64_e32 v[116:117], s[14:15]
	v_mov_b64_e32 v[112:113], s[14:15]
	v_mov_b64_e32 v[100:101], s[14:15]
	v_mov_b64_e32 v[96:97], s[14:15]
	v_mov_b64_e32 v[114:115], s[12:13]
	v_mov_b64_e32 v[110:111], s[12:13]
	v_mov_b64_e32 v[98:99], s[12:13]
	v_mov_b64_e32 v[94:95], s[12:13]
	v_mov_b32_e32 v12, v122
	v_mov_b32_e32 v13, v123
	s_nop 1
	v_mfma_scale_f32_16x16x128_f8f6f4 v[114:117], v[8:13], v[32:37], v[114:117], v124, v82 op_sel_hi:[0,0,0] cbsz:2 blgp:2
	v_mov_b32_e32 v6, v118
	v_mov_b32_e32 v7, v119
	s_nop 1
	v_mfma_scale_f32_16x16x128_f8f6f4 v[110:113], v[2:7], v[32:37], v[110:113], v120, v82 op_sel_hi:[0,0,0] cbsz:2 blgp:2
	s_nop 1
	v_mfma_scale_f32_16x16x128_f8f6f4 v[98:101], v[8:13], v[26:31], v[98:101], v124, v74 op_sel_hi:[0,0,0] cbsz:2 blgp:2
	s_nop 1
	v_mfma_scale_f32_16x16x128_f8f6f4 v[94:97], v[2:7], v[26:31], v[94:97], v120, v74 op_sel_hi:[0,0,0] cbsz:2 blgp:2
	v_mov_b64_e32 v[84:85], s[14:15]
	v_mov_b64_e32 v[76:77], s[14:15]
	v_mov_b64_e32 v[82:83], s[12:13]
	v_mov_b64_e32 v[74:75], s[12:13]
	s_nop 1
	v_mfma_scale_f32_16x16x128_f8f6f4 v[82:85], v[8:13], v[20:25], v[82:85], v124, v66 op_sel_hi:[0,0,0] cbsz:2 blgp:2
	s_nop 1
	v_mfma_scale_f32_16x16x128_f8f6f4 v[74:77], v[2:7], v[20:25], v[74:77], v120, v66 op_sel_hi:[0,0,0] cbsz:2 blgp:2
	v_mov_b64_e32 v[68:69], s[14:15]
	v_mov_b64_e32 v[66:67], s[12:13]
	s_nop 1
	v_mfma_scale_f32_16x16x128_f8f6f4 v[66:69], v[8:13], v[14:19], v[66:69], v124, v128 op_sel_hi:[0,0,0] cbsz:2 blgp:2
	s_nop 1
	v_mfma_scale_f32_16x16x128_f8f6f4 v[54:57], v[2:7], v[14:19], v[54:57], v120, v128 op_sel_hi:[0,0,0] cbsz:2 blgp:2
	s_setprio 0
	s_barrier
	s_mov_b32 m0, s45
	s_nop 0
	global_load_lds_dwordx4 v153, s[50:51]
	s_mov_b32 m0, s62
	s_nop 0
	global_load_lds_dwordx4 v154, s[50:51]
	s_add_u32 s50, s46, 0x40100
	s_addc_u32 s51, s47, 0
	s_mov_b32 m0, s63
	s_nop 0
	global_load_lds_dwordx4 v153, s[50:51]
	s_and_b64 vcc, exec, s[48:49]
	s_mov_b32 m0, s64
	s_nop 0
	global_load_lds_dwordx4 v154, s[50:51]
	s_mov_b32 m0, s17
	s_nop 0
	global_load_lds_dwordx4 v50, s[24:25]
	s_mov_b32 m0, s65
	s_nop 0
	global_load_lds_dwordx4 v51, s[24:25]
	s_cbranch_vccz .LBB0_1198
	s_waitcnt vmcnt(10)
	s_cbranch_execnz .LBB0_1184

; #define LAS __attribute__((address_space(3)))
; #define PG8_RC() int R[2], C[2]; { int t_ = threadIdx.x; asm volatile("" : "+v"(t_)); _Pragma("unroll") for (int i = 0; i < 2; ++i) stage_rc(t_ * 16 + i * 8192, R[i], C[i]); }
; #define PG8_STAGEB(bufoff, gbase) PG8_STAGE2(bufoff, gbase, voffB[0], voffB[1])
; #define PG8_STAGEAS(bufoff, gbase, h) PG8_STAGE2(bufoff, gbase, voffA[h][0], voffA[h][1])
; #define PG8_LDA(dst, b, h) do { _Pragma("unroll") for (int m = 0; m < 4; ++m) _Pragma("unroll") for (int k = 0; k < 2; ++k) dst[m][k] = *(const LAS bf16x8*)(lds + PG8_SA(b, h) + aoff + m * 2048 + k * 1024); } while (0)
; #define PG8_LDB(dst, b, h) do { _Pragma("unroll") for (int n = 0; n < 2; ++n) _Pragma("unroll") for (int k = 0; k < 2; ++k) dst[n][k] = *(const LAS bf16x8*)(lds + PG8_SB(b, h) + boff + n * 2048 + k * 1024); } while (0)
; #define PG8_WAIT_K() do { if constexpr (HM) PG8_WAIT_V(6); else PG8_WAIT_V(8); } while (0)
; #define PG8_WAIT_L(n) asm volatile("s_waitcnt lgkmcnt(" #n ")" ::: "memory")
; #define PG8_BAR __builtin_amdgcn_s_barrier()
; #define PG8_SCHED __builtin_amdgcn_sched_barrier(0)
;     ...
;                 if (t == 2 && has_next) {
;                     if constexpr (HM) asm volatile("s_waitcnt vmcnt(12)" : "+v"(gtok0), "+v"(gtok1), "+v"(gtok2), "+v"(gtok3) :: "memory");
;                     else asm volatile("s_waitcnt vmcnt(16)" : "+v"(gtok0), "+v"(gtok1), "+v"(gtok2), "+v"(gtok3) :: "memory");
;                     PG8_RC(); *(LAS u32x4*)(S.aux + tid * 16) = (u32x4){(unsigned)(((int)gtok0 >> 2) * S.lda + C[0]) * 2u, (unsigned)(((int)gtok1 >> 2) * S.lda + C[1]) * 2u, (unsigned)(((int)gtok2 >> 2) * S.lda + C[0]) * 2u, (unsigned)(((int)gtok3 >> 2) * S.lda + C[1]) * 2u};
;     ...
;             PG8_LDB(B0, 1, 0); PG8_LDB(B1, 1, 1); PG8_SCHED; PG8_LDA(At, 1, 0); if constexpr (!HM) PG8_STAGEAS(PG8_SA(0, 1), a2, 1);
;             PG8_WAIT_K(); PG8_WAIT_L(0); PG8_BAR; PG8_MMA(0, 0, At, B0); PG8_MMA(0, 1, At, B1); PG8_BAR; PG8_SCHED;
;             if constexpr (!HM) PG8_LDA(At, 1, 1);
;             PG8_STAGEB(PG8_SB(1, 0), b3); PG8_STAGEB(PG8_SB(1, 1), b3 + hstepB); PG8_STAGEAS(PG8_SA(1, 0), a3, 0);
;             PG8_WAIT_K(); PG8_WAIT_L(0); PG8_BAR; if constexpr (!HM) { PG8_MMA(1, 0, At, B0); PG8_MMA(1, 1, At, B1); } PG8_BAR; PG8_SCHED;
.LBB0_1184:
	s_waitcnt lgkmcnt(0)
	s_add_u32 s48, s46, 0x180
	s_addc_u32 s49, s47, 0
	s_barrier
	s_barrier
	v_add_u32_e32 v164, 0x18000, v159
	v_add_u32_e32 v165, 0x1c000, v159
	ds_read_b128 v[2:5], v164
	ds_read_b128 v[118:121], v164 offset:1024
	ds_read_b128 v[8:11], v164 offset:2048
	ds_read_b128 v[122:125], v164 offset:3072
	ds_read_b128 v[14:17], v165
	ds_read_b128 v[126:129], v165 offset:1024
	ds_read_b128 v[20:23], v165 offset:2048
	ds_read_b128 v[132:135], v165 offset:3072
	ds_read_b128 v[26:29], v160 offset:32768
	ds_read_b128 v[136:139], v160 offset:33792
	ds_read_b128 v[32:35], v160 offset:34816
	ds_read_b128 v[140:143], v160 offset:35840
	ds_read_b128 v[38:41], v160 offset:36864
	ds_read_b128 v[144:147], v160 offset:37888
	ds_read_b128 v[44:47], v160 offset:38912
	ds_read_b128 v[166:169], v160 offset:39936
	s_waitcnt vmcnt(6)
	s_waitcnt lgkmcnt(0)
	s_barrier
	s_setprio 1
	v_mov_b32_e32 v30, v136
	v_mov_b32_e32 v31, v137
	v_mov_b32_e32 v6, v118
	v_mov_b32_e32 v7, v119
	s_nop 1
	v_mfma_scale_f32_16x16x128_f8f6f4 v[106:109], v[2:7], v[26:31], v[106:109], v120, v138 op_sel_hi:[0,0,0] cbsz:2 blgp:2
	v_mov_b32_e32 v12, v122
	v_mov_b32_e32 v13, v123
	s_nop 1
	v_mfma_scale_f32_16x16x128_f8f6f4 v[102:105], v[8:13], v[26:31], v[102:105], v124, v138 op_sel_hi:[0,0,0] cbsz:2 blgp:2
	v_mov_b32_e32 v36, v140
	v_mov_b32_e32 v37, v141
	s_nop 1
	v_mfma_scale_f32_16x16x128_f8f6f4 v[90:93], v[2:7], v[32:37], v[90:93], v120, v142 op_sel_hi:[0,0,0] cbsz:2 blgp:2
	s_nop 1
	v_mfma_scale_f32_16x16x128_f8f6f4 v[86:89], v[8:13], v[32:37], v[86:89], v124, v142 op_sel_hi:[0,0,0] cbsz:2 blgp:2
	v_mov_b32_e32 v42, v144
	v_mov_b32_e32 v43, v145
	s_nop 1
	v_mfma_scale_f32_16x16x128_f8f6f4 v[78:81], v[2:7], v[38:43], v[78:81], v120, v146 op_sel_hi:[0,0,0] cbsz:2 blgp:2
	s_nop 1
	v_mfma_scale_f32_16x16x128_f8f6f4 v[70:73], v[8:13], v[38:43], v[70:73], v124, v146 op_sel_hi:[0,0,0] cbsz:2 blgp:2
	v_mov_b32_e32 v48, v166
	v_mov_b32_e32 v49, v167
	s_nop 1
	v_mfma_scale_f32_16x16x128_f8f6f4 v[62:65], v[2:7], v[44:49], v[62:65], v120, v168 op_sel_hi:[0,0,0] cbsz:2 blgp:2
	s_nop 1
	v_mfma_scale_f32_16x16x128_f8f6f4 v[58:61], v[8:13], v[44:49], v[58:61], v124, v168 op_sel_hi:[0,0,0] cbsz:2 blgp:2
	v_mov_b32_e32 v18, v126
	v_mov_b32_e32 v19, v127
	s_nop 1
	v_mfma_scale_f32_16x16x128_f8f6f4 v[114:117], v[14:19], v[26:31], v[114:117], v128, v138 op_sel_hi:[0,0,0] cbsz:2 blgp:2
	v_mov_b32_e32 v24, v132
	v_mov_b32_e32 v25, v133
	s_nop 1
	v_mfma_scale_f32_16x16x128_f8f6f4 v[110:113], v[20:25], v[26:31], v[110:113], v134, v138 op_sel_hi:[0,0,0] cbsz:2 blgp:2
	s_nop 1
	v_mfma_scale_f32_16x16x128_f8f6f4 v[98:101], v[14:19], v[32:37], v[98:101], v128, v142 op_sel_hi:[0,0,0] cbsz:2 blgp:2
	s_nop 1
	v_mfma_scale_f32_16x16x128_f8f6f4 v[94:97], v[20:25], v[32:37], v[94:97], v134, v142 op_sel_hi:[0,0,0] cbsz:2 blgp:2
	s_nop 1
	v_mfma_scale_f32_16x16x128_f8f6f4 v[82:85], v[14:19], v[38:43], v[82:85], v128, v146 op_sel_hi:[0,0,0] cbsz:2 blgp:2
	s_nop 1
	v_mfma_scale_f32_16x16x128_f8f6f4 v[74:77], v[20:25], v[38:43], v[74:77], v134, v146 op_sel_hi:[0,0,0] cbsz:2 blgp:2
	s_nop 1
	v_mfma_scale_f32_16x16x128_f8f6f4 v[66:69], v[14:19], v[44:49], v[66:69], v128, v168 op_sel_hi:[0,0,0] cbsz:2 blgp:2
	s_nop 1
	v_mfma_scale_f32_16x16x128_f8f6f4 v[54:57], v[20:25], v[44:49], v[54:57], v134, v168 op_sel_hi:[0,0,0] cbsz:2 blgp:2
	s_setprio 0
	s_barrier
	s_mov_b32 m0, s66
	s_nop 0
	global_load_lds_dwordx4 v153, s[48:49]
	s_mov_b32 m0, s67
	s_nop 0
	global_load_lds_dwordx4 v154, s[48:49]
	s_add_u32 s48, s46, 0x40180
	s_addc_u32 s49, s47, 0
	s_mov_b32 m0, s70
	s_nop 0
	global_load_lds_dwordx4 v153, s[48:49]
	s_mov_b32 m0, s71
	s_nop 0
	global_load_lds_dwordx4 v154, s[48:49]
	s_mov_b32 m0, s68
	s_nop 0
	global_load_lds_dwordx4 v50, s[26:27]
	s_mov_b32 m0, s69
	s_nop 0
	global_load_lds_dwordx4 v51, s[26:27]
	s_waitcnt vmcnt(6)
	s_waitcnt lgkmcnt(0)
	s_barrier
	s_barrier
	v_add_u32_e32 v2, 0, v152
	s_and_b64 vcc, exec, s[8:9]
	v_add_u32_e32 v166, 0x20000, v2
	s_cbranch_vccnz .LBB0_1186
	v_mov_b32_e32 v2, v0
	s_waitcnt vmcnt(12)
	s_nop 0
	v_ashrrev_i32_e32 v4, 31, v2
	v_lshrrev_b32_e32 v4, 26, v4
	v_lshlrev_b32_e32 v3, 4, v2
	v_add_u32_e32 v4, v2, v4
	v_bfe_i32 v2, v2, 27, 1
	v_lshrrev_b32_e32 v2, 22, v2
	v_add_u32_e32 v2, v3, v2
	v_and_b32_e32 v2, 0xfffffc00, v2
	v_sub_u32_e32 v2, v3, v2
	v_lshrrev_b32_e32 v5, 4, v2
	v_bitop3_b32 v5, v5, v2, 32 bitop3:0x6c
	v_ashrrev_i32_e32 v2, 31, v2
	v_lshrrev_b32_e32 v2, 26, v2
	v_add_u32_e32 v2, v5, v2
	v_and_b32_e32 v2, 0xc0, v2
	v_lshrrev_b32_e32 v4, 1, v4
	v_sub_u32_e32 v2, v5, v2
	v_and_b32_e32 v4, 32, v4
	v_ashrrev_i16_sdwa v2, v1, sext(v2) dst_sel:DWORD dst_unused:UNUSED_PAD src0_sel:DWORD src1_sel:BYTE_0
	v_add_u32_sdwa v4, v4, sext(v2) dst_sel:DWORD dst_unused:UNUSED_PAD src0_sel:DWORD src1_sel:WORD_0
	v_add_u32_e32 v2, 0x2000, v3
	v_ashrrev_i32_e32 v3, 31, v2
	v_lshrrev_b32_e32 v3, 22, v3
	v_add_u32_e32 v3, v2, v3
	v_ashrrev_i32_e32 v3, 10, v3
	v_mul_i32_i24_e32 v5, 0x400, v3
	v_sub_u32_e32 v2, v2, v5
	v_lshrrev_b32_e32 v5, 4, v2
	v_bitop3_b32 v5, v5, v2, 32 bitop3:0x6c
	v_ashrrev_i32_e32 v2, 31, v2
	v_lshrrev_b32_e32 v2, 26, v2
	v_add_u32_e32 v2, v5, v2
	v_and_b32_e32 v2, 0xc0, v2
	v_lshlrev_b32_e32 v3, 5, v3
	v_sub_u32_e32 v2, v5, v2
	v_and_b32_e32 v3, 32, v3
	v_ashrrev_i16_sdwa v2, v1, sext(v2) dst_sel:DWORD dst_unused:UNUSED_PAD src0_sel:DWORD src1_sel:BYTE_0
	v_add_u32_sdwa v5, v3, sext(v2) dst_sel:DWORD dst_unused:UNUSED_PAD src0_sel:DWORD src1_sel:WORD_0
	v_lshlrev_b32_e32 v2, 8, v131
	v_lshlrev_b32_e32 v6, 8, v53
	v_and_b32_e32 v2, 0x7ffffc00, v2
	v_and_b32_e32 v6, 0x7ffffc00, v6
	v_add_lshl_u32 v2, v4, v2, 1
	v_lshlrev_b32_e32 v3, 8, v130
	v_add_lshl_u32 v4, v4, v6, 1
	v_lshlrev_b32_e32 v6, 8, v52
	v_and_b32_e32 v3, 0x7ffffc00, v3
	v_and_b32_e32 v6, 0x7ffffc00, v6
	v_add_lshl_u32 v3, v5, v3, 1
	v_add_lshl_u32 v5, v5, v6, 1
	ds_write_b128 v166, v[2:5]
; #define LAS __attribute__((address_space(3)))
; #define PG8_STAGEB(bufoff, gbase) PG8_STAGE2(bufoff, gbase, voffB[0], voffB[1])
; #define PG8_STAGEA(bufoff, gbase, h) PG8_STAGE2(bufoff, gbase, voffA[h][0], voffA[h][1])
; #define PG8_STAGEAS(bufoff, gbase, h) PG8_STAGE2(bufoff, gbase, voffA[h][0], voffA[h][1])
; #define PG8_LDA(dst, b, h) do { _Pragma("unroll") for (int m = 0; m < 4; ++m) _Pragma("unroll") for (int k = 0; k < 2; ++k) dst[m][k] = *(const LAS bf16x8*)(lds + PG8_SA(b, h) + aoff + m * 2048 + k * 1024); } while (0)
; #define PG8_LDB(dst, b, h) do { _Pragma("unroll") for (int n = 0; n < 2; ++n) _Pragma("unroll") for (int k = 0; k < 2; ++k) dst[n][k] = *(const LAS bf16x8*)(lds + PG8_SB(b, h) + boff + n * 2048 + k * 1024); } while (0)
; #define PG8_WAIT_K() do { if constexpr (HM) PG8_WAIT_V(6); else PG8_WAIT_V(8); } while (0)
; #define PG8_WAIT_K0() do { if (EST > 0 && t == 0 && ui > 0) asm volatile("s_waitcnt vmcnt(%0)" :: "n"((HM ? 6 : 8) + EST) : "memory"); else PG8_WAIT_K(); } while (0)
; #define PG8_WAIT_L(n) asm volatile("s_waitcnt lgkmcnt(" #n ")" ::: "memory")
; #define PG8_BAR __builtin_amdgcn_s_barrier()
; #define PG8_SCHED __builtin_amdgcn_sched_barrier(0)
;     ...
;             PG8_LDB(B0, 0, 0); PG8_LDB(B1, 0, 1); PG8_SCHED; PG8_LDA(At, 0, 0); if constexpr (!HM) PG8_STAGEA(PG8_SA(1, 1), a1, 1);
;             if constexpr (Sched::kGather) { if (last && has_next) { const u32x4 tn = *(const LAS u32x4*)(S.aux + tid * 16); voffA[0][0] = tn.x; voffA[0][1] = tn.y; voffA[1][0] = tn.z; voffA[1][1] = tn.w; } }
;             PG8_WAIT_K0(); PG8_WAIT_L(0); PG8_BAR; PG8_MMA(0, 0, At, B0); PG8_MMA(0, 1, At, B1); PG8_BAR; PG8_SCHED;
;             if constexpr (!HM) PG8_LDA(At, 0, 1);
;             PG8_STAGEB(PG8_SB(0, 0), b2); PG8_STAGEB(PG8_SB(0, 1), b2 + hstepB); PG8_STAGEAS(PG8_SA(0, 0), a2, 0);
;             PG8_WAIT_K0(); PG8_WAIT_L(0); PG8_BAR; if constexpr (!HM) { PG8_MMA(1, 0, At, B0); PG8_MMA(1, 1, At, B1); } PG8_BAR; PG8_SCHED;
;             PG8_LDB(B0, 1, 0); PG8_LDB(B1, 1, 1); PG8_SCHED; PG8_LDA(At, 1, 0); if constexpr (!HM) PG8_STAGEAS(PG8_SA(0, 1), a2, 1);
;             PG8_WAIT_K(); PG8_WAIT_L(0); PG8_BAR; PG8_MMA(0, 0, At, B0); PG8_MMA(0, 1, At, B1); PG8_BAR; PG8_SCHED;
.LBB0_1186:
	ds_read_b128 v[2:5], v163
	ds_read_b128 v[118:121], v163 offset:1024
	ds_read_b128 v[8:11], v163 offset:2048
	ds_read_b128 v[122:125], v163 offset:3072
	ds_read_b128 v[14:17], v162
	ds_read_b128 v[126:129], v162 offset:1024
	ds_read_b128 v[20:23], v162 offset:2048
	ds_read_b128 v[130:133], v162 offset:3072
	s_add_u32 s50, s46, 0x200
	s_addc_u32 s51, s47, 0
	ds_read_b128 v[26:29], v160
	ds_read_b128 v[134:137], v160 offset:1024
	ds_read_b128 v[32:35], v160 offset:2048
	ds_read_b128 v[138:141], v160 offset:3072
	ds_read_b128 v[38:41], v160 offset:4096
	ds_read_b128 v[142:145], v160 offset:5120
	ds_read_b128 v[44:47], v160 offset:6144
	ds_read_b128 v[146:149], v160 offset:7168
	s_waitcnt vmcnt(6)
	s_waitcnt lgkmcnt(0)
	s_add_u32 s48, s46, 0x280
	s_addc_u32 s49, s47, 0
	s_barrier
	s_setprio 1
	v_mov_b32_e32 v30, v134
	v_mov_b32_e32 v31, v135
	v_mov_b32_e32 v6, v118
	v_mov_b32_e32 v7, v119
	s_nop 1
	v_mfma_scale_f32_16x16x128_f8f6f4 v[106:109], v[2:7], v[26:31], v[106:109], v120, v136 op_sel_hi:[0,0,0] cbsz:2 blgp:2
	v_mov_b32_e32 v12, v122
	v_mov_b32_e32 v13, v123
	s_nop 1
	v_mfma_scale_f32_16x16x128_f8f6f4 v[102:105], v[8:13], v[26:31], v[102:105], v124, v136 op_sel_hi:[0,0,0] cbsz:2 blgp:2
	v_mov_b32_e32 v36, v138
	v_mov_b32_e32 v37, v139
	s_nop 1
	v_mfma_scale_f32_16x16x128_f8f6f4 v[90:93], v[2:7], v[32:37], v[90:93], v120, v140 op_sel_hi:[0,0,0] cbsz:2 blgp:2
	s_nop 1
	v_mfma_scale_f32_16x16x128_f8f6f4 v[86:89], v[8:13], v[32:37], v[86:89], v124, v140 op_sel_hi:[0,0,0] cbsz:2 blgp:2
	v_mov_b32_e32 v42, v142
	v_mov_b32_e32 v43, v143
	s_nop 1
	v_mfma_scale_f32_16x16x128_f8f6f4 v[78:81], v[2:7], v[38:43], v[78:81], v120, v144 op_sel_hi:[0,0,0] cbsz:2 blgp:2
	s_nop 1
	v_mfma_scale_f32_16x16x128_f8f6f4 v[70:73], v[8:13], v[38:43], v[70:73], v124, v144 op_sel_hi:[0,0,0] cbsz:2 blgp:2
	v_mov_b32_e32 v48, v146
	v_mov_b32_e32 v49, v147
	s_nop 1
	v_mfma_scale_f32_16x16x128_f8f6f4 v[62:65], v[2:7], v[44:49], v[62:65], v120, v148 op_sel_hi:[0,0,0] cbsz:2 blgp:2
	s_nop 1
	v_mfma_scale_f32_16x16x128_f8f6f4 v[58:61], v[8:13], v[44:49], v[58:61], v124, v148 op_sel_hi:[0,0,0] cbsz:2 blgp:2
	v_mov_b32_e32 v18, v126
	v_mov_b32_e32 v19, v127
	s_nop 1
	v_mfma_scale_f32_16x16x128_f8f6f4 v[114:117], v[14:19], v[26:31], v[114:117], v128, v136 op_sel_hi:[0,0,0] cbsz:2 blgp:2
	v_mov_b32_e32 v24, v130
	v_mov_b32_e32 v25, v131
	s_nop 1
	v_mfma_scale_f32_16x16x128_f8f6f4 v[110:113], v[20:25], v[26:31], v[110:113], v132, v136 op_sel_hi:[0,0,0] cbsz:2 blgp:2
	s_nop 1
	v_mfma_scale_f32_16x16x128_f8f6f4 v[98:101], v[14:19], v[32:37], v[98:101], v128, v140 op_sel_hi:[0,0,0] cbsz:2 blgp:2
	s_nop 1
	v_mfma_scale_f32_16x16x128_f8f6f4 v[94:97], v[20:25], v[32:37], v[94:97], v132, v140 op_sel_hi:[0,0,0] cbsz:2 blgp:2
	s_nop 1
	v_mfma_scale_f32_16x16x128_f8f6f4 v[82:85], v[14:19], v[38:43], v[82:85], v128, v144 op_sel_hi:[0,0,0] cbsz:2 blgp:2
	s_nop 1
	v_mfma_scale_f32_16x16x128_f8f6f4 v[74:77], v[20:25], v[38:43], v[74:77], v132, v144 op_sel_hi:[0,0,0] cbsz:2 blgp:2
	s_nop 1
	v_mfma_scale_f32_16x16x128_f8f6f4 v[66:69], v[14:19], v[44:49], v[66:69], v128, v148 op_sel_hi:[0,0,0] cbsz:2 blgp:2
	s_nop 1
	v_mfma_scale_f32_16x16x128_f8f6f4 v[54:57], v[20:25], v[44:49], v[54:57], v132, v148 op_sel_hi:[0,0,0] cbsz:2 blgp:2
	s_setprio 0
	s_barrier
	s_mov_b32 m0, s45
	s_nop 0
	global_load_lds_dwordx4 v153, s[50:51]
	s_mov_b32 m0, s62
	s_nop 0
	global_load_lds_dwordx4 v154, s[50:51]
	s_add_u32 s50, s46, 0x40200
	s_addc_u32 s51, s47, 0
	s_mov_b32 m0, s63
	s_nop 0
	global_load_lds_dwordx4 v153, s[50:51]
	s_mov_b32 m0, s64
	s_nop 0
	global_load_lds_dwordx4 v154, s[50:51]
	s_mov_b32 m0, s17
	s_nop 0
	global_load_lds_dwordx4 v50, s[34:35]
	s_mov_b32 m0, s65
	s_nop 0
	global_load_lds_dwordx4 v51, s[34:35]
	s_waitcnt vmcnt(6)
	s_waitcnt lgkmcnt(0)
	s_barrier
	s_barrier
	ds_read_b128 v[2:5], v164
	ds_read_b128 v[118:121], v164 offset:1024
	ds_read_b128 v[8:11], v164 offset:2048
	ds_read_b128 v[122:125], v164 offset:3072
	ds_read_b128 v[14:17], v165
	ds_read_b128 v[126:129], v165 offset:1024
	ds_read_b128 v[20:23], v165 offset:2048
	ds_read_b128 v[130:133], v165 offset:3072
	ds_read_b128 v[26:29], v160 offset:32768
	ds_read_b128 v[134:137], v160 offset:33792
	ds_read_b128 v[32:35], v160 offset:34816
	ds_read_b128 v[138:141], v160 offset:35840
	ds_read_b128 v[38:41], v160 offset:36864
	ds_read_b128 v[142:145], v160 offset:37888
	ds_read_b128 v[44:47], v160 offset:38912
	ds_read_b128 v[146:149], v160 offset:39936
	s_waitcnt vmcnt(6)
	s_waitcnt lgkmcnt(0)
	s_barrier
; #define LAS __attribute__((address_space(3)))
; #define PG8_STAGEB(bufoff, gbase) PG8_STAGE2(bufoff, gbase, voffB[0], voffB[1])
; #define PG8_STAGEA(bufoff, gbase, h) PG8_STAGE2(bufoff, gbase, voffA[h][0], voffA[h][1])
; #define PG8_STAGEAS(bufoff, gbase, h) PG8_STAGE2(bufoff, gbase, voffA[h][0], voffA[h][1])
; #define PG8_LDA(dst, b, h) do { _Pragma("unroll") for (int m = 0; m < 4; ++m) _Pragma("unroll") for (int k = 0; k < 2; ++k) dst[m][k] = *(const LAS bf16x8*)(lds + PG8_SA(b, h) + aoff + m * 2048 + k * 1024); } while (0)
; #define PG8_LDB(dst, b, h) do { _Pragma("unroll") for (int n = 0; n < 2; ++n) _Pragma("unroll") for (int k = 0; k < 2; ++k) dst[n][k] = *(const LAS bf16x8*)(lds + PG8_SB(b, h) + boff + n * 2048 + k * 1024); } while (0)
;     ...
;             const char* a1 = cA + (size_t)(t + 1) * kstep;
;             const char* a2 = last ? nA : cA + (size_t)(t + 2) * kstep; const char* b2 = last ? nB : cB + (size_t)(t + 2) * kstep;
;             const char* a3 = a2 + kstep; const char* b3 = b2 + kstep;
;             PG8_LDB(B0, 0, 0); PG8_LDB(B1, 0, 1); PG8_SCHED; PG8_LDA(At, 0, 0); if constexpr (!HM) PG8_STAGEA(PG8_SA(1, 1), a1, 1);
;             if constexpr (Sched::kGather) { if (last && has_next) { const u32x4 tn = *(const LAS u32x4*)(S.aux + tid * 16); voffA[0][0] = tn.x; voffA[0][1] = tn.y; voffA[1][0] = tn.z; voffA[1][1] = tn.w; } }
;             PG8_WAIT_K0(); PG8_WAIT_L(0); PG8_BAR; PG8_MMA(0, 0, At, B0); PG8_MMA(0, 1, At, B1); PG8_BAR; PG8_SCHED;
;             if constexpr (!HM) PG8_LDA(At, 0, 1);
;             PG8_STAGEB(PG8_SB(0, 0), b2); PG8_STAGEB(PG8_SB(0, 1), b2 + hstepB); PG8_STAGEAS(PG8_SA(0, 0), a2, 0);
;             PG8_WAIT_K0(); PG8_WAIT_L(0); PG8_BAR; if constexpr (!HM) { PG8_MMA(1, 0, At, B0); PG8_MMA(1, 1, At, B1); } PG8_BAR; PG8_SCHED;
;             PG8_LDB(B0, 1, 0); PG8_LDB(B1, 1, 1); PG8_SCHED; PG8_LDA(At, 1, 0); if constexpr (!HM) PG8_STAGEAS(PG8_SA(0, 1), a2, 1);
;             PG8_WAIT_K(); PG8_WAIT_L(0); PG8_BAR; PG8_MMA(0, 0, At, B0); PG8_MMA(0, 1, At, B1); PG8_BAR; PG8_SCHED;
;             if constexpr (!HM) PG8_LDA(At, 1, 1);
;             PG8_STAGEB(PG8_SB(1, 0), b3); PG8_STAGEB(PG8_SB(1, 1), b3 + hstepB); PG8_STAGEAS(PG8_SA(1, 0), a3, 0);
;             PG8_WAIT_K(); PG8_WAIT_L(0); PG8_BAR; if constexpr (!HM) { PG8_MMA(1, 0, At, B0); PG8_MMA(1, 1, At, B1); } PG8_BAR; PG8_SCHED;
	s_setprio 1
	v_mov_b32_e32 v30, v134
	v_mov_b32_e32 v31, v135
	v_mov_b32_e32 v6, v118
	v_mov_b32_e32 v7, v119
	s_nop 1
	v_mfma_scale_f32_16x16x128_f8f6f4 v[106:109], v[2:7], v[26:31], v[106:109], v120, v136 op_sel_hi:[0,0,0] cbsz:2 blgp:2
	v_mov_b32_e32 v12, v122
	v_mov_b32_e32 v13, v123
	s_nop 1
	v_mfma_scale_f32_16x16x128_f8f6f4 v[102:105], v[8:13], v[26:31], v[102:105], v124, v136 op_sel_hi:[0,0,0] cbsz:2 blgp:2
	v_mov_b32_e32 v36, v138
	v_mov_b32_e32 v37, v139
	s_nop 1
	v_mfma_scale_f32_16x16x128_f8f6f4 v[90:93], v[2:7], v[32:37], v[90:93], v120, v140 op_sel_hi:[0,0,0] cbsz:2 blgp:2
	s_nop 1
	v_mfma_scale_f32_16x16x128_f8f6f4 v[86:89], v[8:13], v[32:37], v[86:89], v124, v140 op_sel_hi:[0,0,0] cbsz:2 blgp:2
	v_mov_b32_e32 v42, v142
	v_mov_b32_e32 v43, v143
	s_nop 1
	v_mfma_scale_f32_16x16x128_f8f6f4 v[78:81], v[2:7], v[38:43], v[78:81], v120, v144 op_sel_hi:[0,0,0] cbsz:2 blgp:2
	s_nop 1
	v_mfma_scale_f32_16x16x128_f8f6f4 v[70:73], v[8:13], v[38:43], v[70:73], v124, v144 op_sel_hi:[0,0,0] cbsz:2 blgp:2
	v_mov_b32_e32 v48, v146
	v_mov_b32_e32 v49, v147
	s_nop 1
	v_mfma_scale_f32_16x16x128_f8f6f4 v[62:65], v[2:7], v[44:49], v[62:65], v120, v148 op_sel_hi:[0,0,0] cbsz:2 blgp:2
	s_nop 1
	v_mfma_scale_f32_16x16x128_f8f6f4 v[58:61], v[8:13], v[44:49], v[58:61], v124, v148 op_sel_hi:[0,0,0] cbsz:2 blgp:2
	v_mov_b32_e32 v18, v126
	v_mov_b32_e32 v19, v127
	s_nop 1
	v_mfma_scale_f32_16x16x128_f8f6f4 v[114:117], v[14:19], v[26:31], v[114:117], v128, v136 op_sel_hi:[0,0,0] cbsz:2 blgp:2
	v_mov_b32_e32 v24, v130
	v_mov_b32_e32 v25, v131
	s_nop 1
	v_mfma_scale_f32_16x16x128_f8f6f4 v[110:113], v[20:25], v[26:31], v[110:113], v132, v136 op_sel_hi:[0,0,0] cbsz:2 blgp:2
	s_nop 1
	v_mfma_scale_f32_16x16x128_f8f6f4 v[98:101], v[14:19], v[32:37], v[98:101], v128, v140 op_sel_hi:[0,0,0] cbsz:2 blgp:2
	s_nop 1
	v_mfma_scale_f32_16x16x128_f8f6f4 v[94:97], v[20:25], v[32:37], v[94:97], v132, v140 op_sel_hi:[0,0,0] cbsz:2 blgp:2
	s_nop 1
	v_mfma_scale_f32_16x16x128_f8f6f4 v[82:85], v[14:19], v[38:43], v[82:85], v128, v144 op_sel_hi:[0,0,0] cbsz:2 blgp:2
	s_nop 1
	v_mfma_scale_f32_16x16x128_f8f6f4 v[74:77], v[20:25], v[38:43], v[74:77], v132, v144 op_sel_hi:[0,0,0] cbsz:2 blgp:2
	s_nop 1
	v_mfma_scale_f32_16x16x128_f8f6f4 v[66:69], v[14:19], v[44:49], v[66:69], v128, v148 op_sel_hi:[0,0,0] cbsz:2 blgp:2
	s_nop 1
	v_mfma_scale_f32_16x16x128_f8f6f4 v[54:57], v[20:25], v[44:49], v[54:57], v132, v148 op_sel_hi:[0,0,0] cbsz:2 blgp:2
	s_setprio 0
	s_barrier
	s_mov_b32 m0, s66
	s_nop 0
	global_load_lds_dwordx4 v153, s[48:49]
	s_mov_b32 m0, s67
	s_nop 0
	global_load_lds_dwordx4 v154, s[48:49]
	s_add_u32 s48, s46, 0x40280
	s_addc_u32 s49, s47, 0
	s_mov_b32 m0, s70
	s_nop 0
	global_load_lds_dwordx4 v153, s[48:49]
	s_mov_b32 m0, s71
	s_nop 0
	global_load_lds_dwordx4 v154, s[48:49]
	s_mov_b32 m0, s68
	s_nop 0
	global_load_lds_dwordx4 v50, s[36:37]
	s_mov_b32 m0, s69
	s_nop 0
	global_load_lds_dwordx4 v51, s[36:37]
	s_waitcnt vmcnt(6)
	s_waitcnt lgkmcnt(0)
	s_barrier
	s_barrier
	s_mov_b32 s39, 2
	s_mov_b64 s[48:49], 0x300
	s_branch .LBB0_1188
.LBB0_1187:
	s_and_b64 s[50:51], s[52:53], exec
	s_cselect_b32 s50, 0, s48
	s_cselect_b32 s41, 0, s49
	s_add_u32 s56, s0, s50
	s_addc_u32 s57, s1, s41
	s_add_u32 s41, s46, s48
	s_addc_u32 s54, s47, s49
	s_add_u32 s50, s56, 0x80
	s_addc_u32 s51, s57, 0
	s_waitcnt vmcnt(6)
	s_and_b64 s[52:53], s[52:53], exec
	s_waitcnt lgkmcnt(0)
	s_cselect_b32 s52, s42, s41
	s_cselect_b32 s53, s43, s54
	s_add_u32 s54, s52, 0x80
	s_addc_u32 s55, s53, 0
	s_barrier
	s_setprio 1
	v_mov_b32_e32 v36, v138
	v_mov_b32_e32 v37, v139
	v_mov_b32_e32 v48, v146
	v_mov_b32_e32 v49, v147
	s_nop 1
	v_mfma_scale_f32_16x16x128_f8f6f4 v[106:109], v[44:49], v[32:37], v[106:109], v148, v140 op_sel_hi:[0,0,0] cbsz:2 blgp:2
	v_mov_b32_e32 v42, v142
	v_mov_b32_e32 v43, v143
	s_nop 1
	v_mfma_scale_f32_16x16x128_f8f6f4 v[102:105], v[38:43], v[32:37], v[102:105], v144, v140 op_sel_hi:[0,0,0] cbsz:2 blgp:2
	v_mov_b32_e32 v30, v134
	v_mov_b32_e32 v31, v135
	s_nop 1
	v_mfma_scale_f32_16x16x128_f8f6f4 v[90:93], v[44:49], v[26:31], v[90:93], v148, v136 op_sel_hi:[0,0,0] cbsz:2 blgp:2
	s_nop 1
	v_mfma_scale_f32_16x16x128_f8f6f4 v[86:89], v[38:43], v[26:31], v[86:89], v144, v136 op_sel_hi:[0,0,0] cbsz:2 blgp:2
	v_mov_b32_e32 v24, v130
	v_mov_b32_e32 v25, v131
	s_nop 1
	v_mfma_scale_f32_16x16x128_f8f6f4 v[78:81], v[44:49], v[20:25], v[78:81], v148, v132 op_sel_hi:[0,0,0] cbsz:2 blgp:2
	s_nop 1
	v_mfma_scale_f32_16x16x128_f8f6f4 v[70:73], v[38:43], v[20:25], v[70:73], v144, v132 op_sel_hi:[0,0,0] cbsz:2 blgp:2
	v_mov_b32_e32 v18, v126
	v_mov_b32_e32 v19, v127
	s_nop 1
	v_mfma_scale_f32_16x16x128_f8f6f4 v[62:65], v[44:49], v[14:19], v[62:65], v148, v128 op_sel_hi:[0,0,0] cbsz:2 blgp:2
	s_nop 1
	v_mfma_scale_f32_16x16x128_f8f6f4 v[58:61], v[38:43], v[14:19], v[58:61], v144, v128 op_sel_hi:[0,0,0] cbsz:2 blgp:2
	v_mov_b32_e32 v12, v122
	v_mov_b32_e32 v13, v123
	s_nop 1
	v_mfma_scale_f32_16x16x128_f8f6f4 v[114:117], v[8:13], v[32:37], v[114:117], v124, v140 op_sel_hi:[0,0,0] cbsz:2 blgp:2
	v_mov_b32_e32 v6, v118
	v_mov_b32_e32 v7, v119
	s_nop 1
	v_mfma_scale_f32_16x16x128_f8f6f4 v[110:113], v[2:7], v[32:37], v[110:113], v120, v140 op_sel_hi:[0,0,0] cbsz:2 blgp:2
	s_nop 1
	v_mfma_scale_f32_16x16x128_f8f6f4 v[98:101], v[8:13], v[26:31], v[98:101], v124, v136 op_sel_hi:[0,0,0] cbsz:2 blgp:2
	s_nop 1
	v_mfma_scale_f32_16x16x128_f8f6f4 v[94:97], v[2:7], v[26:31], v[94:97], v120, v136 op_sel_hi:[0,0,0] cbsz:2 blgp:2
	s_nop 1
	v_mfma_scale_f32_16x16x128_f8f6f4 v[82:85], v[8:13], v[20:25], v[82:85], v124, v132 op_sel_hi:[0,0,0] cbsz:2 blgp:2
	s_nop 1
	v_mfma_scale_f32_16x16x128_f8f6f4 v[74:77], v[2:7], v[20:25], v[74:77], v120, v132 op_sel_hi:[0,0,0] cbsz:2 blgp:2
	s_nop 1
	v_mfma_scale_f32_16x16x128_f8f6f4 v[66:69], v[8:13], v[14:19], v[66:69], v124, v128 op_sel_hi:[0,0,0] cbsz:2 blgp:2
	s_nop 1
	v_mfma_scale_f32_16x16x128_f8f6f4 v[54:57], v[2:7], v[14:19], v[54:57], v120, v128 op_sel_hi:[0,0,0] cbsz:2 blgp:2
	s_setprio 0
	s_barrier
; #define PG8_STAGEB(bufoff, gbase) PG8_STAGE2(bufoff, gbase, voffB[0], voffB[1])
; #define PG8_STAGEAS(bufoff, gbase, h) PG8_STAGE2(bufoff, gbase, voffA[h][0], voffA[h][1])
; #define PG8_LDA(dst, b, h) do { _Pragma("unroll") for (int m = 0; m < 4; ++m) _Pragma("unroll") for (int k = 0; k < 2; ++k) dst[m][k] = *(const LAS bf16x8*)(lds + PG8_SA(b, h) + aoff + m * 2048 + k * 1024); } while (0)
; #define PG8_LDB(dst, b, h) do { _Pragma("unroll") for (int n = 0; n < 2; ++n) _Pragma("unroll") for (int k = 0; k < 2; ++k) dst[n][k] = *(const LAS bf16x8*)(lds + PG8_SB(b, h) + boff + n * 2048 + k * 1024); } while (0)
; #define PG8_WAIT_K() do { if constexpr (HM) PG8_WAIT_V(6); else PG8_WAIT_V(8); } while (0)
; #define PG8_WAIT_K0() do { if (EST > 0 && t == 0 && ui > 0) asm volatile("s_waitcnt vmcnt(%0)" :: "n"((HM ? 6 : 8) + EST) : "memory"); else PG8_WAIT_K(); } while (0)
; #define PG8_WAIT_L(n) asm volatile("s_waitcnt lgkmcnt(" #n ")" ::: "memory")
; #define PG8_BAR __builtin_amdgcn_s_barrier()
; #define PG8_SCHED __builtin_amdgcn_sched_barrier(0)
;     ...
;             PG8_STAGEB(PG8_SB(0, 0), b2); PG8_STAGEB(PG8_SB(0, 1), b2 + hstepB); PG8_STAGEAS(PG8_SA(0, 0), a2, 0);
;             PG8_WAIT_K0(); PG8_WAIT_L(0); PG8_BAR; if constexpr (!HM) { PG8_MMA(1, 0, At, B0); PG8_MMA(1, 1, At, B1); } PG8_BAR; PG8_SCHED;
;             PG8_LDB(B0, 1, 0); PG8_LDB(B1, 1, 1); PG8_SCHED; PG8_LDA(At, 1, 0); if constexpr (!HM) PG8_STAGEAS(PG8_SA(0, 1), a2, 1);
;             PG8_WAIT_K(); PG8_WAIT_L(0); PG8_BAR; PG8_MMA(0, 0, At, B0); PG8_MMA(0, 1, At, B1); PG8_BAR; PG8_SCHED;
;             if constexpr (!HM) PG8_LDA(At, 1, 1);
;             PG8_STAGEB(PG8_SB(1, 0), b3); PG8_STAGEB(PG8_SB(1, 1), b3 + hstepB); PG8_STAGEAS(PG8_SA(1, 0), a3, 0);
;             PG8_WAIT_K(); PG8_WAIT_L(0); PG8_BAR; if constexpr (!HM) { PG8_MMA(1, 0, At, B0); PG8_MMA(1, 1, At, B1); } PG8_BAR; PG8_SCHED;
;         }
	s_mov_b32 m0, s45
	s_nop 0
	global_load_lds_dwordx4 v153, s[52:53]
	s_add_u32 s78, s52, 0x40000
	s_mov_b32 m0, s62
	s_nop 0
	global_load_lds_dwordx4 v154, s[52:53]
	s_addc_u32 s79, s53, 0
	s_mov_b32 m0, s63
	s_nop 0
	global_load_lds_dwordx4 v153, s[78:79]
	s_mov_b32 m0, s64
	s_nop 0
	global_load_lds_dwordx4 v154, s[78:79]
	s_mov_b32 m0, s17
	s_nop 0
	global_load_lds_dwordx4 v50, s[56:57]
	s_mov_b32 m0, s65
	s_nop 0
	global_load_lds_dwordx4 v51, s[56:57]
	s_waitcnt vmcnt(6)
	s_waitcnt lgkmcnt(0)
	s_barrier
	s_barrier
	ds_read_b128 v[2:5], v164
	ds_read_b128 v[118:121], v164 offset:1024
	ds_read_b128 v[8:11], v164 offset:2048
	ds_read_b128 v[122:125], v164 offset:3072
	ds_read_b128 v[14:17], v165
	ds_read_b128 v[126:129], v165 offset:1024
	ds_read_b128 v[20:23], v165 offset:2048
	ds_read_b128 v[130:133], v165 offset:3072
	ds_read_b128 v[26:29], v160 offset:32768
	ds_read_b128 v[134:137], v160 offset:33792
	ds_read_b128 v[32:35], v160 offset:34816
	ds_read_b128 v[138:141], v160 offset:35840
	ds_read_b128 v[38:41], v160 offset:36864
	ds_read_b128 v[142:145], v160 offset:37888
	ds_read_b128 v[44:47], v160 offset:38912
	ds_read_b128 v[146:149], v160 offset:39936
	s_waitcnt vmcnt(6)
	s_waitcnt lgkmcnt(0)
	s_barrier
	s_setprio 1
	v_mov_b32_e32 v30, v134
	v_mov_b32_e32 v31, v135
	v_mov_b32_e32 v6, v118
	v_mov_b32_e32 v7, v119
	s_nop 1
	v_mfma_scale_f32_16x16x128_f8f6f4 v[106:109], v[2:7], v[26:31], v[106:109], v120, v136 op_sel_hi:[0,0,0] cbsz:2 blgp:2
	v_mov_b32_e32 v12, v122
	v_mov_b32_e32 v13, v123
	s_nop 1
	v_mfma_scale_f32_16x16x128_f8f6f4 v[102:105], v[8:13], v[26:31], v[102:105], v124, v136 op_sel_hi:[0,0,0] cbsz:2 blgp:2
	v_mov_b32_e32 v36, v138
	v_mov_b32_e32 v37, v139
	s_nop 1
	v_mfma_scale_f32_16x16x128_f8f6f4 v[90:93], v[2:7], v[32:37], v[90:93], v120, v140 op_sel_hi:[0,0,0] cbsz:2 blgp:2
	s_nop 1
	v_mfma_scale_f32_16x16x128_f8f6f4 v[86:89], v[8:13], v[32:37], v[86:89], v124, v140 op_sel_hi:[0,0,0] cbsz:2 blgp:2
	v_mov_b32_e32 v42, v142
	v_mov_b32_e32 v43, v143
	s_nop 1
	v_mfma_scale_f32_16x16x128_f8f6f4 v[78:81], v[2:7], v[38:43], v[78:81], v120, v144 op_sel_hi:[0,0,0] cbsz:2 blgp:2
	s_nop 1
	v_mfma_scale_f32_16x16x128_f8f6f4 v[70:73], v[8:13], v[38:43], v[70:73], v124, v144 op_sel_hi:[0,0,0] cbsz:2 blgp:2
	v_mov_b32_e32 v48, v146
	v_mov_b32_e32 v49, v147
	s_nop 1
	v_mfma_scale_f32_16x16x128_f8f6f4 v[62:65], v[2:7], v[44:49], v[62:65], v120, v148 op_sel_hi:[0,0,0] cbsz:2 blgp:2
	s_nop 1
	v_mfma_scale_f32_16x16x128_f8f6f4 v[58:61], v[8:13], v[44:49], v[58:61], v124, v148 op_sel_hi:[0,0,0] cbsz:2 blgp:2
	v_mov_b32_e32 v18, v126
	v_mov_b32_e32 v19, v127
	s_nop 1
	v_mfma_scale_f32_16x16x128_f8f6f4 v[114:117], v[14:19], v[26:31], v[114:117], v128, v136 op_sel_hi:[0,0,0] cbsz:2 blgp:2
	v_mov_b32_e32 v24, v130
	v_mov_b32_e32 v25, v131
	s_nop 1
	v_mfma_scale_f32_16x16x128_f8f6f4 v[110:113], v[20:25], v[26:31], v[110:113], v132, v136 op_sel_hi:[0,0,0] cbsz:2 blgp:2
	s_nop 1
	v_mfma_scale_f32_16x16x128_f8f6f4 v[98:101], v[14:19], v[32:37], v[98:101], v128, v140 op_sel_hi:[0,0,0] cbsz:2 blgp:2
	s_nop 1
	v_mfma_scale_f32_16x16x128_f8f6f4 v[94:97], v[20:25], v[32:37], v[94:97], v132, v140 op_sel_hi:[0,0,0] cbsz:2 blgp:2
	s_nop 1
	v_mfma_scale_f32_16x16x128_f8f6f4 v[82:85], v[14:19], v[38:43], v[82:85], v128, v144 op_sel_hi:[0,0,0] cbsz:2 blgp:2
	s_nop 1
	v_mfma_scale_f32_16x16x128_f8f6f4 v[74:77], v[20:25], v[38:43], v[74:77], v132, v144 op_sel_hi:[0,0,0] cbsz:2 blgp:2
	s_nop 1
	v_mfma_scale_f32_16x16x128_f8f6f4 v[66:69], v[14:19], v[44:49], v[66:69], v128, v148 op_sel_hi:[0,0,0] cbsz:2 blgp:2
	s_nop 1
	v_mfma_scale_f32_16x16x128_f8f6f4 v[54:57], v[20:25], v[44:49], v[54:57], v132, v148 op_sel_hi:[0,0,0] cbsz:2 blgp:2
	s_setprio 0
	s_barrier
	s_mov_b32 m0, s66
	s_nop 0
	global_load_lds_dwordx4 v153, s[54:55]
	s_add_u32 s52, s52, 0x40080
	s_mov_b32 m0, s67
	s_nop 0
	global_load_lds_dwordx4 v154, s[54:55]
	s_addc_u32 s53, s53, 0
	s_mov_b32 m0, s70
	s_nop 0
	global_load_lds_dwordx4 v153, s[52:53]
	s_mov_b32 m0, s71
	s_nop 0
	global_load_lds_dwordx4 v154, s[52:53]
	s_mov_b32 m0, s68
	s_nop 0
	global_load_lds_dwordx4 v50, s[50:51]
	s_mov_b32 m0, s69
	s_nop 0
	global_load_lds_dwordx4 v51, s[50:51]
	s_waitcnt vmcnt(6)
	s_waitcnt lgkmcnt(0)
	s_barrier
	s_barrier
	s_add_i32 s39, s39, 2
	s_add_u32 s48, s48, 0x100
	s_addc_u32 s49, s49, 0
	s_cmp_gt_u32 s39, 13
	s_cbranch_scc1 .LBB0_1190

; #define LAS __attribute__((address_space(3)))
; #define PG8_STAGEB(bufoff, gbase) PG8_STAGE2(bufoff, gbase, voffB[0], voffB[1])
; #define PG8_STAGEA(bufoff, gbase, h) PG8_STAGE2(bufoff, gbase, voffA[h][0], voffA[h][1])
; #define PG8_STAGEAS(bufoff, gbase, h) PG8_STAGE2(bufoff, gbase, voffA[h][0], voffA[h][1])
; #define PG8_LDA(dst, b, h) do { _Pragma("unroll") for (int m = 0; m < 4; ++m) _Pragma("unroll") for (int k = 0; k < 2; ++k) dst[m][k] = *(const LAS bf16x8*)(lds + PG8_SA(b, h) + aoff + m * 2048 + k * 1024); } while (0)
; #define PG8_LDB(dst, b, h) do { _Pragma("unroll") for (int n = 0; n < 2; ++n) _Pragma("unroll") for (int k = 0; k < 2; ++k) dst[n][k] = *(const LAS bf16x8*)(lds + PG8_SB(b, h) + boff + n * 2048 + k * 1024); } while (0)
; #define PG8_WAIT_K0() do { if (EST > 0 && t == 0 && ui > 0) asm volatile("s_waitcnt vmcnt(%0)" :: "n"((HM ? 6 : 8) + EST) : "memory"); else PG8_WAIT_K(); } while (0)
; #define PG8_WAIT_L(n) asm volatile("s_waitcnt lgkmcnt(" #n ")" ::: "memory")
; #define PG8_BAR __builtin_amdgcn_s_barrier()
; #define PG8_SCHED __builtin_amdgcn_sched_barrier(0)
;     ...
;             const char* a1 = cA + (size_t)(t + 1) * kstep;
;             const char* a2 = last ? nA : cA + (size_t)(t + 2) * kstep; const char* b2 = last ? nB : cB + (size_t)(t + 2) * kstep;
;             const char* a3 = a2 + kstep; const char* b3 = b2 + kstep;
;             PG8_LDB(B0, 0, 0); PG8_LDB(B1, 0, 1); PG8_SCHED; PG8_LDA(At, 0, 0); if constexpr (!HM) PG8_STAGEA(PG8_SA(1, 1), a1, 1);
;             if constexpr (Sched::kGather) { if (last && has_next) { const u32x4 tn = *(const LAS u32x4*)(S.aux + tid * 16); voffA[0][0] = tn.x; voffA[0][1] = tn.y; voffA[1][0] = tn.z; voffA[1][1] = tn.w; } }
;             PG8_WAIT_K0(); PG8_WAIT_L(0); PG8_BAR; PG8_MMA(0, 0, At, B0); PG8_MMA(0, 1, At, B1); PG8_BAR; PG8_SCHED;
;             if constexpr (!HM) PG8_LDA(At, 0, 1);
;             PG8_STAGEB(PG8_SB(0, 0), b2); PG8_STAGEB(PG8_SB(0, 1), b2 + hstepB); PG8_STAGEAS(PG8_SA(0, 0), a2, 0);
;             PG8_WAIT_K0(); PG8_WAIT_L(0); PG8_BAR; if constexpr (!HM) { PG8_MMA(1, 0, At, B0); PG8_MMA(1, 1, At, B1); } PG8_BAR; PG8_SCHED;
.LBB0_1290:
	ds_read_b128 v[26:29], v184
	ds_read_b128 v[30:33], v184 offset:1024
	ds_read_b128 v[18:21], v184 offset:2048
	ds_read_b128 v[22:25], v184 offset:3072
	ds_read_b128 v[10:13], v185
	ds_read_b128 v[14:17], v185 offset:1024
	ds_read_b128 v[2:5], v185 offset:2048
	ds_read_b128 v[6:9], v185 offset:3072
	s_cmp_eq_u32 s73, 12
	s_cselect_b32 s42, s0, s25
	s_cselect_b32 s43, s1, s27
	s_cselect_b32 s40, s30, s29
	s_cselect_b32 s41, s31, s72
	s_add_u32 s38, s42, 0x80
	s_addc_u32 s39, s43, 0
	ds_read_b128 v[190:193], v186
	ds_read_b128 v[194:197], v186 offset:1024
	ds_read_b128 v[198:201], v186 offset:2048
	ds_read_b128 v[202:205], v186 offset:3072
	ds_read_b128 v[206:209], v186 offset:4096
	ds_read_b128 v[210:213], v186 offset:5120
	ds_read_b128 v[214:217], v186 offset:6144
	ds_read_b128 v[218:221], v186 offset:7168
	s_mov_b32 m0, s68
	s_nop 0
	global_load_lds_dwordx4 v167, s[36:37]
	s_mov_b32 m0, s69
	s_nop 0
	global_load_lds_dwordx4 v168, s[36:37]
	s_waitcnt vmcnt(8)
	s_waitcnt lgkmcnt(0)
	s_barrier
	s_setprio 1
	v_mfma_scale_f32_16x16x128_f8f6f4 v[158:161], v[26:33], v[190:197], v[158:161], v1, v164 op_sel_hi:[0,0,0]
	v_mfma_scale_f32_16x16x128_f8f6f4 v[154:157], v[18:25], v[190:197], v[154:157], v1, v164 op_sel_hi:[0,0,0]
	v_mfma_scale_f32_16x16x128_f8f6f4 v[142:145], v[26:33], v[198:205], v[142:145], v1, v164 op_sel_hi:[0,0,0]
	v_mfma_scale_f32_16x16x128_f8f6f4 v[138:141], v[18:25], v[198:205], v[138:141], v1, v164 op_sel_hi:[0,0,0]
	v_mfma_scale_f32_16x16x128_f8f6f4 v[126:129], v[26:33], v[206:213], v[126:129], v1, v164 op_sel_hi:[0,0,0]
	v_mfma_scale_f32_16x16x128_f8f6f4 v[122:125], v[18:25], v[206:213], v[122:125], v1, v164 op_sel_hi:[0,0,0]
	v_mfma_scale_f32_16x16x128_f8f6f4 v[110:113], v[26:33], v[214:221], v[110:113], v1, v164 op_sel_hi:[0,0,0]
	v_mfma_scale_f32_16x16x128_f8f6f4 v[106:109], v[18:25], v[214:221], v[106:109], v1, v164 op_sel_hi:[0,0,0]
	v_mfma_scale_f32_16x16x128_f8f6f4 v[150:153], v[10:17], v[190:197], v[150:153], v1, v164 op_sel_hi:[0,0,0]
	v_mfma_scale_f32_16x16x128_f8f6f4 v[146:149], v[2:9], v[190:197], v[146:149], v1, v164 op_sel_hi:[0,0,0]
	v_mfma_scale_f32_16x16x128_f8f6f4 v[134:137], v[10:17], v[198:205], v[134:137], v1, v164 op_sel_hi:[0,0,0]
	v_mfma_scale_f32_16x16x128_f8f6f4 v[130:133], v[2:9], v[198:205], v[130:133], v1, v164 op_sel_hi:[0,0,0]
	v_mfma_scale_f32_16x16x128_f8f6f4 v[118:121], v[10:17], v[206:213], v[118:121], v1, v164 op_sel_hi:[0,0,0]
	v_mfma_scale_f32_16x16x128_f8f6f4 v[114:117], v[2:9], v[206:213], v[114:117], v1, v164 op_sel_hi:[0,0,0]
	v_mfma_scale_f32_16x16x128_f8f6f4 v[102:105], v[10:17], v[214:221], v[102:105], v1, v164 op_sel_hi:[0,0,0]
	v_mfma_scale_f32_16x16x128_f8f6f4 v[98:101], v[2:9], v[214:221], v[98:101], v1, v164 op_sel_hi:[0,0,0]
	s_setprio 0
	s_barrier
	ds_read_b128 v[190:193], v186 offset:16384
	ds_read_b128 v[194:197], v186 offset:17408
	ds_read_b128 v[198:201], v186 offset:18432
	ds_read_b128 v[202:205], v186 offset:19456
	ds_read_b128 v[206:209], v186 offset:20480
	ds_read_b128 v[210:213], v186 offset:21504
	ds_read_b128 v[214:217], v186 offset:22528
	ds_read_b128 v[218:221], v186 offset:23552
	s_mov_b32 m0, s55
	s_nop 0
	global_load_lds_dwordx4 v169, s[40:41]
	s_mov_b32 m0, s56
	s_nop 0
	global_load_lds_dwordx4 v170, s[40:41]
	s_add_u32 s74, s40, 0x40000
	s_addc_u32 s75, s41, 0
	s_mov_b32 m0, s57
	s_nop 0
	global_load_lds_dwordx4 v169, s[74:75]
	s_mov_b32 m0, s58
	s_nop 0
	global_load_lds_dwordx4 v170, s[74:75]
	s_mov_b32 m0, s54
	s_nop 0
	global_load_lds_dwordx4 v165, s[42:43]
	s_mov_b32 m0, s59
	s_nop 0
	global_load_lds_dwordx4 v166, s[42:43]
	s_waitcnt vmcnt(8)
	s_waitcnt lgkmcnt(0)
	s_barrier
	s_setprio 1
	v_mfma_scale_f32_16x16x128_f8f6f4 v[94:97], v[26:33], v[190:197], v[94:97], v1, v164 op_sel_hi:[0,0,0]
	v_mfma_scale_f32_16x16x128_f8f6f4 v[90:93], v[18:25], v[190:197], v[90:93], v1, v164 op_sel_hi:[0,0,0]
	v_mfma_scale_f32_16x16x128_f8f6f4 v[78:81], v[26:33], v[198:205], v[78:81], v1, v164 op_sel_hi:[0,0,0]
	v_mfma_scale_f32_16x16x128_f8f6f4 v[74:77], v[18:25], v[198:205], v[74:77], v1, v164 op_sel_hi:[0,0,0]
	v_mfma_scale_f32_16x16x128_f8f6f4 v[62:65], v[26:33], v[206:213], v[62:65], v1, v164 op_sel_hi:[0,0,0]
	v_mfma_scale_f32_16x16x128_f8f6f4 v[58:61], v[18:25], v[206:213], v[58:61], v1, v164 op_sel_hi:[0,0,0]
	v_mfma_scale_f32_16x16x128_f8f6f4 v[46:49], v[26:33], v[214:221], v[46:49], v1, v164 op_sel_hi:[0,0,0]
	v_mfma_scale_f32_16x16x128_f8f6f4 v[42:45], v[18:25], v[214:221], v[42:45], v1, v164 op_sel_hi:[0,0,0]
	v_mfma_scale_f32_16x16x128_f8f6f4 v[86:89], v[10:17], v[190:197], v[86:89], v1, v164 op_sel_hi:[0,0,0]
	v_mfma_scale_f32_16x16x128_f8f6f4 v[82:85], v[2:9], v[190:197], v[82:85], v1, v164 op_sel_hi:[0,0,0]
	v_mfma_scale_f32_16x16x128_f8f6f4 v[70:73], v[10:17], v[198:205], v[70:73], v1, v164 op_sel_hi:[0,0,0]
	v_mfma_scale_f32_16x16x128_f8f6f4 v[66:69], v[2:9], v[198:205], v[66:69], v1, v164 op_sel_hi:[0,0,0]
	v_mfma_scale_f32_16x16x128_f8f6f4 v[54:57], v[10:17], v[206:213], v[54:57], v1, v164 op_sel_hi:[0,0,0]
	v_mfma_scale_f32_16x16x128_f8f6f4 v[50:53], v[2:9], v[206:213], v[50:53], v1, v164 op_sel_hi:[0,0,0]
	v_mfma_scale_f32_16x16x128_f8f6f4 v[38:41], v[10:17], v[214:221], v[38:41], v1, v164 op_sel_hi:[0,0,0]
	v_mfma_scale_f32_16x16x128_f8f6f4 v[34:37], v[2:9], v[214:221], v[34:37], v1, v164 op_sel_hi:[0,0,0]
	s_setprio 0
	s_barrier
; #define PG8_STAGEB(bufoff, gbase) PG8_STAGE2(bufoff, gbase, voffB[0], voffB[1])
; #define PG8_STAGEAS(bufoff, gbase, h) PG8_STAGE2(bufoff, gbase, voffA[h][0], voffA[h][1])
; #define PG8_LDA(dst, b, h) do { _Pragma("unroll") for (int m = 0; m < 4; ++m) _Pragma("unroll") for (int k = 0; k < 2; ++k) dst[m][k] = *(const LAS bf16x8*)(lds + PG8_SA(b, h) + aoff + m * 2048 + k * 1024); } while (0)
; #define PG8_LDB(dst, b, h) do { _Pragma("unroll") for (int n = 0; n < 2; ++n) _Pragma("unroll") for (int k = 0; k < 2; ++k) dst[n][k] = *(const LAS bf16x8*)(lds + PG8_SB(b, h) + boff + n * 2048 + k * 1024); } while (0)
; #define PG8_WAIT_K() do { if constexpr (HM) PG8_WAIT_V(6); else PG8_WAIT_V(8); } while (0)
; #define PG8_WAIT_L(n) asm volatile("s_waitcnt lgkmcnt(" #n ")" ::: "memory")
; #define PG8_BAR __builtin_amdgcn_s_barrier()
; #define PG8_SCHED __builtin_amdgcn_sched_barrier(0)
;     ...
;             PG8_LDB(B0, 1, 0); PG8_LDB(B1, 1, 1); PG8_SCHED; PG8_LDA(At, 1, 0); if constexpr (!HM) PG8_STAGEAS(PG8_SA(0, 1), a2, 1);
;             PG8_WAIT_K(); PG8_WAIT_L(0); PG8_BAR; PG8_MMA(0, 0, At, B0); PG8_MMA(0, 1, At, B1); PG8_BAR; PG8_SCHED;
;             if constexpr (!HM) PG8_LDA(At, 1, 1);
;             PG8_STAGEB(PG8_SB(1, 0), b3); PG8_STAGEB(PG8_SB(1, 1), b3 + hstepB); PG8_STAGEAS(PG8_SA(1, 0), a3, 0);
;             PG8_WAIT_K(); PG8_WAIT_L(0); PG8_BAR; if constexpr (!HM) { PG8_MMA(1, 0, At, B0); PG8_MMA(1, 1, At, B1); } PG8_BAR; PG8_SCHED;
;         }
	ds_read_b128 v[2:5], v187
	ds_read_b128 v[6:9], v187 offset:1024
	ds_read_b128 v[10:13], v187 offset:2048
	ds_read_b128 v[14:17], v187 offset:3072
	ds_read_b128 v[18:21], v188
	ds_read_b128 v[22:25], v188 offset:1024
	ds_read_b128 v[26:29], v188 offset:2048
	ds_read_b128 v[30:33], v188 offset:3072
	ds_read_b128 v[190:193], v186 offset:32768
	ds_read_b128 v[194:197], v186 offset:33792
	ds_read_b128 v[198:201], v186 offset:34816
	ds_read_b128 v[202:205], v186 offset:35840
	ds_read_b128 v[206:209], v186 offset:36864
	ds_read_b128 v[210:213], v186 offset:37888
	ds_read_b128 v[214:217], v186 offset:38912
	ds_read_b128 v[218:221], v186 offset:39936
	s_mov_b32 m0, s60
	s_nop 0
	global_load_lds_dwordx4 v167, s[42:43]
	s_mov_b32 m0, s61
	s_nop 0
	global_load_lds_dwordx4 v168, s[42:43]
	s_waitcnt vmcnt(8)
	s_waitcnt lgkmcnt(0)
	s_barrier
	s_setprio 1
	v_mfma_scale_f32_16x16x128_f8f6f4 v[158:161], v[2:9], v[190:197], v[158:161], v1, v164 op_sel_hi:[0,0,0]
	v_mfma_scale_f32_16x16x128_f8f6f4 v[154:157], v[10:17], v[190:197], v[154:157], v1, v164 op_sel_hi:[0,0,0]
	v_mfma_scale_f32_16x16x128_f8f6f4 v[142:145], v[2:9], v[198:205], v[142:145], v1, v164 op_sel_hi:[0,0,0]
	v_mfma_scale_f32_16x16x128_f8f6f4 v[138:141], v[10:17], v[198:205], v[138:141], v1, v164 op_sel_hi:[0,0,0]
	v_mfma_scale_f32_16x16x128_f8f6f4 v[126:129], v[2:9], v[206:213], v[126:129], v1, v164 op_sel_hi:[0,0,0]
	v_mfma_scale_f32_16x16x128_f8f6f4 v[122:125], v[10:17], v[206:213], v[122:125], v1, v164 op_sel_hi:[0,0,0]
	v_mfma_scale_f32_16x16x128_f8f6f4 v[110:113], v[2:9], v[214:221], v[110:113], v1, v164 op_sel_hi:[0,0,0]
	v_mfma_scale_f32_16x16x128_f8f6f4 v[106:109], v[10:17], v[214:221], v[106:109], v1, v164 op_sel_hi:[0,0,0]
	v_mfma_scale_f32_16x16x128_f8f6f4 v[150:153], v[18:25], v[190:197], v[150:153], v1, v164 op_sel_hi:[0,0,0]
	v_mfma_scale_f32_16x16x128_f8f6f4 v[146:149], v[26:33], v[190:197], v[146:149], v1, v164 op_sel_hi:[0,0,0]
	v_mfma_scale_f32_16x16x128_f8f6f4 v[134:137], v[18:25], v[198:205], v[134:137], v1, v164 op_sel_hi:[0,0,0]
	v_mfma_scale_f32_16x16x128_f8f6f4 v[130:133], v[26:33], v[198:205], v[130:133], v1, v164 op_sel_hi:[0,0,0]
	v_mfma_scale_f32_16x16x128_f8f6f4 v[118:121], v[18:25], v[206:213], v[118:121], v1, v164 op_sel_hi:[0,0,0]
	v_mfma_scale_f32_16x16x128_f8f6f4 v[114:117], v[26:33], v[206:213], v[114:117], v1, v164 op_sel_hi:[0,0,0]
	v_mfma_scale_f32_16x16x128_f8f6f4 v[102:105], v[18:25], v[214:221], v[102:105], v1, v164 op_sel_hi:[0,0,0]
	v_mfma_scale_f32_16x16x128_f8f6f4 v[98:101], v[26:33], v[214:221], v[98:101], v1, v164 op_sel_hi:[0,0,0]
	s_setprio 0
	s_barrier
	ds_read_b128 v[190:193], v186 offset:49152
	ds_read_b128 v[194:197], v186 offset:50176
	ds_read_b128 v[198:201], v186 offset:51200
	ds_read_b128 v[202:205], v186 offset:52224
	ds_read_b128 v[206:209], v186 offset:53248
	ds_read_b128 v[210:213], v186 offset:54272
	ds_read_b128 v[214:217], v186 offset:55296
	ds_read_b128 v[218:221], v186 offset:56320
	s_add_u32 s42, s40, 0x80
	s_addc_u32 s43, s41, 0
	s_mov_b32 m0, s62
	s_nop 0
	global_load_lds_dwordx4 v169, s[42:43]
	s_add_u32 s40, s40, 0x40080
	s_mov_b32 m0, s63
	s_nop 0
	global_load_lds_dwordx4 v170, s[42:43]
	s_addc_u32 s41, s41, 0
	s_mov_b32 m0, s66
	s_nop 0
	global_load_lds_dwordx4 v169, s[40:41]
	s_mov_b32 m0, s67
	s_nop 0
	global_load_lds_dwordx4 v170, s[40:41]
	s_mov_b32 m0, s64
	s_nop 0
	global_load_lds_dwordx4 v165, s[38:39]
	s_mov_b32 m0, s65
	s_nop 0
	global_load_lds_dwordx4 v166, s[38:39]
	s_waitcnt vmcnt(8)
	s_waitcnt lgkmcnt(0)
	s_barrier
	s_setprio 1
	v_mfma_scale_f32_16x16x128_f8f6f4 v[94:97], v[2:9], v[190:197], v[94:97], v1, v164 op_sel_hi:[0,0,0]
	v_mfma_scale_f32_16x16x128_f8f6f4 v[90:93], v[10:17], v[190:197], v[90:93], v1, v164 op_sel_hi:[0,0,0]
	v_mfma_scale_f32_16x16x128_f8f6f4 v[78:81], v[2:9], v[198:205], v[78:81], v1, v164 op_sel_hi:[0,0,0]
	v_mfma_scale_f32_16x16x128_f8f6f4 v[74:77], v[10:17], v[198:205], v[74:77], v1, v164 op_sel_hi:[0,0,0]
	v_mfma_scale_f32_16x16x128_f8f6f4 v[62:65], v[2:9], v[206:213], v[62:65], v1, v164 op_sel_hi:[0,0,0]
	v_mfma_scale_f32_16x16x128_f8f6f4 v[58:61], v[10:17], v[206:213], v[58:61], v1, v164 op_sel_hi:[0,0,0]
	v_mfma_scale_f32_16x16x128_f8f6f4 v[46:49], v[2:9], v[214:221], v[46:49], v1, v164 op_sel_hi:[0,0,0]
	v_mfma_scale_f32_16x16x128_f8f6f4 v[42:45], v[10:17], v[214:221], v[42:45], v1, v164 op_sel_hi:[0,0,0]
	v_mfma_scale_f32_16x16x128_f8f6f4 v[86:89], v[18:25], v[190:197], v[86:89], v1, v164 op_sel_hi:[0,0,0]
	v_mfma_scale_f32_16x16x128_f8f6f4 v[82:85], v[26:33], v[190:197], v[82:85], v1, v164 op_sel_hi:[0,0,0]
	v_mfma_scale_f32_16x16x128_f8f6f4 v[70:73], v[18:25], v[198:205], v[70:73], v1, v164 op_sel_hi:[0,0,0]
	v_mfma_scale_f32_16x16x128_f8f6f4 v[66:69], v[26:33], v[198:205], v[66:69], v1, v164 op_sel_hi:[0,0,0]
	v_mfma_scale_f32_16x16x128_f8f6f4 v[54:57], v[18:25], v[206:213], v[54:57], v1, v164 op_sel_hi:[0,0,0]
	v_mfma_scale_f32_16x16x128_f8f6f4 v[50:53], v[26:33], v[206:213], v[50:53], v1, v164 op_sel_hi:[0,0,0]
	v_mfma_scale_f32_16x16x128_f8f6f4 v[38:41], v[18:25], v[214:221], v[38:41], v1, v164 op_sel_hi:[0,0,0]
	v_mfma_scale_f32_16x16x128_f8f6f4 v[34:37], v[26:33], v[214:221], v[34:37], v1, v164 op_sel_hi:[0,0,0]
	s_setprio 0
	s_barrier
	s_add_i32 s73, s73, 2
	s_add_u32 s25, s25, 0x100
	s_addc_u32 s27, s27, 0
	s_add_u32 s29, s29, 0x100
	s_addc_u32 s72, s72, 0
	s_add_u32 s36, s36, 0x100
	s_addc_u32 s37, s37, 0
	s_cmp_gt_u32 s73, 13
	s_cbranch_scc0 .LBB0_1290
	s_and_b64 vcc, exec, s[20:21]
	s_cbranch_vccz .LBB0_1293
	s_barrier

; #define LAS __attribute__((address_space(3)))
; #define PG8_STAGEB(bufoff, gbase) PG8_STAGE2(bufoff, gbase, voffB[0], voffB[1])
; #define PG8_STAGEA(bufoff, gbase, h) PG8_STAGE2(bufoff, gbase, voffA[h][0], voffA[h][1])
; #define PG8_STAGEAS(bufoff, gbase, h) PG8_STAGE2(bufoff, gbase, voffA[h][0], voffA[h][1])
; #define PG8_LDA(dst, b, h) do { _Pragma("unroll") for (int m = 0; m < 4; ++m) _Pragma("unroll") for (int k = 0; k < 2; ++k) dst[m][k] = *(const LAS bf16x8*)(lds + PG8_SA(b, h) + aoff + m * 2048 + k * 1024); } while (0)
; #define PG8_LDB(dst, b, h) do { _Pragma("unroll") for (int n = 0; n < 2; ++n) _Pragma("unroll") for (int k = 0; k < 2; ++k) dst[n][k] = *(const LAS bf16x8*)(lds + PG8_SB(b, h) + boff + n * 2048 + k * 1024); } while (0)
;     ...
;             const char* a1 = cA + (size_t)(t + 1) * kstep;
;             const char* a2 = last ? nA : cA + (size_t)(t + 2) * kstep; const char* b2 = last ? nB : cB + (size_t)(t + 2) * kstep;
;             const char* a3 = a2 + kstep; const char* b3 = b2 + kstep;
;             PG8_LDB(B0, 0, 0); PG8_LDB(B1, 0, 1); PG8_SCHED; PG8_LDA(At, 0, 0); if constexpr (!HM) PG8_STAGEA(PG8_SA(1, 1), a1, 1);
;             if constexpr (Sched::kGather) { if (last && has_next) { const u32x4 tn = *(const LAS u32x4*)(S.aux + tid * 16); voffA[0][0] = tn.x; voffA[0][1] = tn.y; voffA[1][0] = tn.z; voffA[1][1] = tn.w; } }
;             PG8_WAIT_K0(); PG8_WAIT_L(0); PG8_BAR; PG8_MMA(0, 0, At, B0); PG8_MMA(0, 1, At, B1); PG8_BAR; PG8_SCHED;
;             if constexpr (!HM) PG8_LDA(At, 0, 1);
;             PG8_STAGEB(PG8_SB(0, 0), b2); PG8_STAGEB(PG8_SB(0, 1), b2 + hstepB); PG8_STAGEAS(PG8_SA(0, 0), a2, 0);
;             PG8_WAIT_K0(); PG8_WAIT_L(0); PG8_BAR; if constexpr (!HM) { PG8_MMA(1, 0, At, B0); PG8_MMA(1, 1, At, B1); } PG8_BAR; PG8_SCHED;
;             PG8_LDB(B0, 1, 0); PG8_LDB(B1, 1, 1); PG8_SCHED; PG8_LDA(At, 1, 0); if constexpr (!HM) PG8_STAGEAS(PG8_SA(0, 1), a2, 1);
;             PG8_WAIT_K(); PG8_WAIT_L(0); PG8_BAR; PG8_MMA(0, 0, At, B0); PG8_MMA(0, 1, At, B1); PG8_BAR; PG8_SCHED;
;             if constexpr (!HM) PG8_LDA(At, 1, 1);
;             PG8_STAGEB(PG8_SB(1, 0), b3); PG8_STAGEB(PG8_SB(1, 1), b3 + hstepB); PG8_STAGEAS(PG8_SA(1, 0), a3, 0);
;             PG8_WAIT_K(); PG8_WAIT_L(0); PG8_BAR; if constexpr (!HM) { PG8_MMA(1, 0, At, B0); PG8_MMA(1, 1, At, B1); } PG8_BAR; PG8_SCHED;
;         }
.LBB0_1346:
	ds_read_b128 v[68:71], v100
	ds_read_b128 v[72:75], v100 offset:1024
	ds_read_b128 v[76:79], v100 offset:2048
	ds_read_b128 v[80:83], v100 offset:3072
	ds_read_b128 v[106:109], v101
	ds_read_b128 v[110:113], v101 offset:1024
	ds_read_b128 v[114:117], v101 offset:2048
	ds_read_b128 v[118:121], v101 offset:3072
	s_cmp_eq_u32 s66, 12
	s_cselect_b32 s40, s0, s25
	s_cselect_b32 s41, s1, s29
	s_cselect_b32 s38, s34, s31
	s_cselect_b32 s39, s35, s65
	s_add_u32 s36, s40, 0x80
	s_addc_u32 s37, s41, 0
	ds_read_b128 v[122:125], v102
	ds_read_b128 v[126:129], v102 offset:1024
	ds_read_b128 v[130:133], v102 offset:2048
	ds_read_b128 v[134:137], v102 offset:3072
	ds_read_b128 v[138:141], v102 offset:4096
	ds_read_b128 v[142:145], v102 offset:5120
	ds_read_b128 v[146:149], v102 offset:6144
	ds_read_b128 v[150:153], v102 offset:7168
	s_waitcnt vmcnt(6)
	s_waitcnt lgkmcnt(0)
	s_barrier
	s_setprio 1
	v_mfma_scale_f32_16x16x128_f8f6f4 v[62:65], v[68:75], v[122:129], v[62:65], v1, v86 op_sel_hi:[0,0,0]
	v_mfma_scale_f32_16x16x128_f8f6f4 v[58:61], v[76:83], v[122:129], v[58:61], v1, v86 op_sel_hi:[0,0,0]
	v_mfma_scale_f32_16x16x128_f8f6f4 v[46:49], v[68:75], v[130:137], v[46:49], v1, v86 op_sel_hi:[0,0,0]
	v_mfma_scale_f32_16x16x128_f8f6f4 v[42:45], v[76:83], v[130:137], v[42:45], v1, v86 op_sel_hi:[0,0,0]
	v_mfma_scale_f32_16x16x128_f8f6f4 v[30:33], v[68:75], v[138:145], v[30:33], v1, v86 op_sel_hi:[0,0,0]
	v_mfma_scale_f32_16x16x128_f8f6f4 v[26:29], v[76:83], v[138:145], v[26:29], v1, v86 op_sel_hi:[0,0,0]
	v_mfma_scale_f32_16x16x128_f8f6f4 v[14:17], v[68:75], v[146:153], v[14:17], v1, v86 op_sel_hi:[0,0,0]
	v_mfma_scale_f32_16x16x128_f8f6f4 v[10:13], v[76:83], v[146:153], v[10:13], v1, v86 op_sel_hi:[0,0,0]
	v_mfma_scale_f32_16x16x128_f8f6f4 v[54:57], v[106:113], v[122:129], v[54:57], v1, v86 op_sel_hi:[0,0,0]
	v_mfma_scale_f32_16x16x128_f8f6f4 v[50:53], v[114:121], v[122:129], v[50:53], v1, v86 op_sel_hi:[0,0,0]
	v_mfma_scale_f32_16x16x128_f8f6f4 v[38:41], v[106:113], v[130:137], v[38:41], v1, v86 op_sel_hi:[0,0,0]
	v_mfma_scale_f32_16x16x128_f8f6f4 v[34:37], v[114:121], v[130:137], v[34:37], v1, v86 op_sel_hi:[0,0,0]
	v_mfma_scale_f32_16x16x128_f8f6f4 v[22:25], v[106:113], v[138:145], v[22:25], v1, v86 op_sel_hi:[0,0,0]
	v_mfma_scale_f32_16x16x128_f8f6f4 v[18:21], v[114:121], v[138:145], v[18:21], v1, v86 op_sel_hi:[0,0,0]
	v_mfma_scale_f32_16x16x128_f8f6f4 v[6:9], v[106:113], v[146:153], v[6:9], v1, v86 op_sel_hi:[0,0,0]
	v_mfma_scale_f32_16x16x128_f8f6f4 v[2:5], v[114:121], v[146:153], v[2:5], v1, v86 op_sel_hi:[0,0,0]
	s_setprio 0
	s_barrier
	s_mov_b32 m0, s51
	s_nop 0
	global_load_lds_dwordx4 v89, s[38:39]
	s_add_u32 s68, s38, 0x40000
	s_mov_b32 m0, s52
	s_nop 0
	global_load_lds_dwordx4 v90, s[38:39]
	s_addc_u32 s69, s39, 0
	s_mov_b32 m0, s53
	s_nop 0
	global_load_lds_dwordx4 v89, s[68:69]
	s_mov_b32 m0, s54
	s_nop 0
	global_load_lds_dwordx4 v90, s[68:69]
	s_mov_b32 m0, s50
	s_nop 0
	global_load_lds_dwordx4 v87, s[40:41]
	s_mov_b32 m0, s55
	s_nop 0
	global_load_lds_dwordx4 v88, s[40:41]
	s_waitcnt vmcnt(6)
	s_waitcnt lgkmcnt(0)
	s_barrier
	s_barrier
	ds_read_b128 v[68:71], v103
	ds_read_b128 v[72:75], v103 offset:1024
	ds_read_b128 v[76:79], v103 offset:2048
	ds_read_b128 v[80:83], v103 offset:3072
	ds_read_b128 v[106:109], v104
	ds_read_b128 v[110:113], v104 offset:1024
	ds_read_b128 v[114:117], v104 offset:2048
	ds_read_b128 v[118:121], v104 offset:3072
	ds_read_b128 v[122:125], v102 offset:32768
	ds_read_b128 v[126:129], v102 offset:33792
	ds_read_b128 v[130:133], v102 offset:34816
	ds_read_b128 v[134:137], v102 offset:35840
	ds_read_b128 v[138:141], v102 offset:36864
	ds_read_b128 v[142:145], v102 offset:37888
	ds_read_b128 v[146:149], v102 offset:38912
	ds_read_b128 v[150:153], v102 offset:39936
	s_waitcnt vmcnt(6)
	s_waitcnt lgkmcnt(0)
	s_barrier
	s_setprio 1
	v_mfma_scale_f32_16x16x128_f8f6f4 v[62:65], v[68:75], v[122:129], v[62:65], v1, v86 op_sel_hi:[0,0,0]
	v_mfma_scale_f32_16x16x128_f8f6f4 v[58:61], v[76:83], v[122:129], v[58:61], v1, v86 op_sel_hi:[0,0,0]
	v_mfma_scale_f32_16x16x128_f8f6f4 v[46:49], v[68:75], v[130:137], v[46:49], v1, v86 op_sel_hi:[0,0,0]
	v_mfma_scale_f32_16x16x128_f8f6f4 v[42:45], v[76:83], v[130:137], v[42:45], v1, v86 op_sel_hi:[0,0,0]
	v_mfma_scale_f32_16x16x128_f8f6f4 v[30:33], v[68:75], v[138:145], v[30:33], v1, v86 op_sel_hi:[0,0,0]
	v_mfma_scale_f32_16x16x128_f8f6f4 v[26:29], v[76:83], v[138:145], v[26:29], v1, v86 op_sel_hi:[0,0,0]
	v_mfma_scale_f32_16x16x128_f8f6f4 v[14:17], v[68:75], v[146:153], v[14:17], v1, v86 op_sel_hi:[0,0,0]
	v_mfma_scale_f32_16x16x128_f8f6f4 v[10:13], v[76:83], v[146:153], v[10:13], v1, v86 op_sel_hi:[0,0,0]
	s_add_u32 s40, s38, 0x80
	v_mfma_scale_f32_16x16x128_f8f6f4 v[54:57], v[106:113], v[122:129], v[54:57], v1, v86 op_sel_hi:[0,0,0]
	v_mfma_scale_f32_16x16x128_f8f6f4 v[50:53], v[114:121], v[122:129], v[50:53], v1, v86 op_sel_hi:[0,0,0]
	v_mfma_scale_f32_16x16x128_f8f6f4 v[38:41], v[106:113], v[130:137], v[38:41], v1, v86 op_sel_hi:[0,0,0]
	v_mfma_scale_f32_16x16x128_f8f6f4 v[34:37], v[114:121], v[130:137], v[34:37], v1, v86 op_sel_hi:[0,0,0]
	v_mfma_scale_f32_16x16x128_f8f6f4 v[22:25], v[106:113], v[138:145], v[22:25], v1, v86 op_sel_hi:[0,0,0]
	v_mfma_scale_f32_16x16x128_f8f6f4 v[18:21], v[114:121], v[138:145], v[18:21], v1, v86 op_sel_hi:[0,0,0]
	v_mfma_scale_f32_16x16x128_f8f6f4 v[6:9], v[106:113], v[146:153], v[6:9], v1, v86 op_sel_hi:[0,0,0]
	v_mfma_scale_f32_16x16x128_f8f6f4 v[2:5], v[114:121], v[146:153], v[2:5], v1, v86 op_sel_hi:[0,0,0]
	s_addc_u32 s41, s39, 0
	s_setprio 0
	s_barrier
	s_mov_b32 m0, s56
	s_nop 0
	global_load_lds_dwordx4 v89, s[40:41]
	s_add_u32 s38, s38, 0x40080
	s_mov_b32 m0, s57
	s_nop 0
	global_load_lds_dwordx4 v90, s[40:41]
	s_addc_u32 s39, s39, 0
	s_mov_b32 m0, s60
	s_nop 0
	global_load_lds_dwordx4 v89, s[38:39]
	s_mov_b32 m0, s61
	s_nop 0
	global_load_lds_dwordx4 v90, s[38:39]
	s_mov_b32 m0, s58
	s_nop 0
	global_load_lds_dwordx4 v87, s[36:37]
	s_mov_b32 m0, s59
	s_nop 0
	global_load_lds_dwordx4 v88, s[36:37]
	s_waitcnt vmcnt(6)
	s_waitcnt lgkmcnt(0)
	s_barrier
	s_barrier
	s_add_i32 s66, s66, 2
	s_add_u32 s25, s25, 0x100
	s_addc_u32 s29, s29, 0
	s_add_u32 s31, s31, 0x100
	s_addc_u32 s65, s65, 0
	s_cmp_gt_u32 s66, 13
	s_cbranch_scc0 .LBB0_1346
	s_and_b64 vcc, exec, s[20:21]
	s_cbranch_vccz .LBB0_1349
	s_barrier
